# weight-copy loops: counted waits (vmcnt(16) instead of the merged vmcnt(0)) so the second item of each pair stays in flight during the first item's transpose
# speedup vs baseline: 1.0067x; 1.0067x over previous
; #define LAS __attribute__((address_space(3)))
; __device__ __forceinline__ void t64_load(const float* Wsrc, int ldw, int lane, f32x4 (&tv)[16]) {
;     const float* p = Wsrc + (size_t)(lane >> 3) * ldw + 4 * (lane & 7);
; #pragma unroll
;     for (int i = 0; i < 16; ++i) { tv[i] = __builtin_nontemporal_load((const f32x4*)p); p += 8 * ldw; }
; }
; __device__ __forceinline__ void t64_finish(const f32x4 (&tv)[16], unsigned char* dst, int ldd, int f8, LAS unsigned char* scr, int lane) {
;     const int g = lane >> 4, i16 = lane & 15;
; #pragma unroll
;     for (int i = 0; i < 16; ++i) { v2u w; w.x = cvt_pk_bf16(tv[i].x, tv[i].y); w.y = cvt_pk_bf16(tv[i].z, tv[i].w); *(LAS v2u*)(scr + (8 * i + (lane >> 3)) * 64 + 8 * (lane & 7)) = w; }
;     LDS_WAIT(); asm volatile("" ::: "memory");
;     const int q = i16 >> 2, pp = i16 & 3;
;     bf16x8 o[8];
; #pragma unroll
;     for (int jj = 0; jj < 8; ++jj) { const int c = 4 * jj + g, nb = c & 1, kg = c >> 1;
;         LAS unsigned char* ra = scr + (8 * kg + q) * 64 + 32 * nb + 8 * pp;
;         const s16x4 lo = __builtin_bit_cast(s16x4, __builtin_amdgcn_ds_read_tr16_b64_v4i16((LAS s16x4*)ra));
;         const s16x4 hi = __builtin_bit_cast(s16x4, __builtin_amdgcn_ds_read_tr16_b64_v4i16((LAS s16x4*)(ra + 4 * 64)));
;         o[jj] = __builtin_shufflevector(lo, hi, 0, 1, 2, 3, 4, 5, 6, 7); }
;     LDS_WAIT(); asm volatile("" ::: "memory");
; #pragma unroll
;     for (int jj = 0; jj < 8; ++jj) { const int c = 4 * jj + g, nb = c & 1, kg = c >> 1; const int n = 16 * nb + i16;
;         *(LAS bf16x8*)(scr + n * 256 + 16 * (kg ^ (n & 15))) = o[jj]; }
;     LDS_WAIT(); asm volatile("" ::: "memory");
;     const int rr = lane >> 3, cc = lane & 7;
; #pragma unroll
;     for (int it = 0; it < 4; ++it) { const int n = 8 * it + rr;
;         const v4u v0 = *(const LAS v4u*)(scr + n * 256 + 16 * ((2 * cc) ^ (n & 15))), v1 = *(const LAS v4u*)(scr + n * 256 + 16 * ((2 * cc + 1) ^ (n & 15)));
;         if (f8) { v4u o4; o4.x = pk4_fp8(bf_lo(v0.x) * W8_SCALE, bf_hi(v0.x) * W8_SCALE, bf_lo(v0.y) * W8_SCALE, bf_hi(v0.y) * W8_SCALE);
;             o4.y = pk4_fp8(bf_lo(v0.z) * W8_SCALE, bf_hi(v0.z) * W8_SCALE, bf_lo(v0.w) * W8_SCALE, bf_hi(v0.w) * W8_SCALE);
;             o4.z = pk4_fp8(bf_lo(v1.x) * W8_SCALE, bf_hi(v1.x) * W8_SCALE, bf_lo(v1.y) * W8_SCALE, bf_hi(v1.y) * W8_SCALE);
.LBB0_20:
	s_add_u32 s57, s26, s64
	s_addc_u32 s64, s27, s65
	s_lshl_b64 s[20:21], s[20:21], 12
	s_lshl_b64 s[62:63], s[62:63], 1
	s_add_u32 s20, s57, s20
	s_addc_u32 s21, s64, s21
	s_add_u32 s20, s20, s62
	s_addc_u32 s21, s21, s63
	v_mad_i64_i32 v[0:1], s[62:63], s0, v130, 0
	v_lshl_add_u64 v[0:1], v[0:1], 2, s[60:61]
	v_lshlrev_b32_e32 v134, 2, v132
	v_lshl_add_u64 v[0:1], v[0:1], 0, v[134:135]
	s_lshl_b32 s0, s0, 5
	v_lshl_add_u64 v[8:9], v[0:1], 0, s[0:1]
	global_load_dwordx4 v[0:3], v[0:1], off nt
	s_nop 0
	global_load_dwordx4 v[4:7], v[8:9], off nt
	v_lshl_add_u64 v[8:9], v[8:9], 0, s[0:1]
	v_lshl_add_u64 v[16:17], v[8:9], 0, s[0:1]
	global_load_dwordx4 v[8:11], v[8:9], off nt
	s_nop 0
	global_load_dwordx4 v[12:15], v[16:17], off nt
	v_lshl_add_u64 v[16:17], v[16:17], 0, s[0:1]
	v_lshl_add_u64 v[24:25], v[16:17], 0, s[0:1]
	global_load_dwordx4 v[16:19], v[16:17], off nt
	s_nop 0
	global_load_dwordx4 v[20:23], v[24:25], off nt
	v_lshl_add_u64 v[24:25], v[24:25], 0, s[0:1]
	v_lshl_add_u64 v[32:33], v[24:25], 0, s[0:1]
	v_lshl_add_u64 v[36:37], v[32:33], 0, s[0:1]
	v_lshl_add_u64 v[40:41], v[36:37], 0, s[0:1]
	v_lshl_add_u64 v[44:45], v[40:41], 0, s[0:1]
	v_lshl_add_u64 v[48:49], v[44:45], 0, s[0:1]
	v_lshl_add_u64 v[52:53], v[48:49], 0, s[0:1]
	v_lshl_add_u64 v[56:57], v[52:53], 0, s[0:1]
	v_lshl_add_u64 v[60:61], v[56:57], 0, s[0:1]
	global_load_dwordx4 v[24:27], v[24:25], off nt
	s_nop 0
	global_load_dwordx4 v[28:31], v[32:33], off nt
	s_nop 0
	global_load_dwordx4 v[32:35], v[36:37], off nt
	s_nop 0
	global_load_dwordx4 v[36:39], v[40:41], off nt
	s_nop 0
	global_load_dwordx4 v[40:43], v[44:45], off nt
	s_nop 0
	global_load_dwordx4 v[44:47], v[48:49], off nt
	s_nop 0
	global_load_dwordx4 v[48:51], v[52:53], off nt
	s_nop 0
	global_load_dwordx4 v[52:55], v[56:57], off nt
	s_nop 0
	global_load_dwordx4 v[56:59], v[60:61], off nt
	v_lshl_add_u64 v[60:61], v[60:61], 0, s[0:1]
	global_load_dwordx4 v[60:63], v[60:61], off nt
	s_waitcnt vmcnt(16)
	s_branch .LBB0_21
.LcvwP0_b:
	s_waitcnt vmcnt(0)
.LBB0_21:
	v_cvt_pk_bf16_f32 v174, v64, v65
	v_cvt_pk_bf16_f32 v175, v66, v67
	ds_write_b64 v149, v[174:175]
	v_cvt_pk_bf16_f32 v174, v68, v69
	v_cvt_pk_bf16_f32 v175, v70, v71
	ds_write_b64 v149, v[174:175] offset:512
	v_cvt_pk_bf16_f32 v174, v72, v73
	v_cvt_pk_bf16_f32 v175, v74, v75
	ds_write_b64 v149, v[174:175] offset:1024
	v_cvt_pk_bf16_f32 v174, v76, v77
	v_cvt_pk_bf16_f32 v175, v78, v79
	ds_write_b64 v149, v[174:175] offset:1536
	v_cvt_pk_bf16_f32 v174, v80, v81
	v_cvt_pk_bf16_f32 v175, v82, v83
	ds_write_b64 v149, v[174:175] offset:2048
	v_cvt_pk_bf16_f32 v174, v84, v85
	v_cvt_pk_bf16_f32 v175, v86, v87
	ds_write_b64 v149, v[174:175] offset:2560
	v_cvt_pk_bf16_f32 v174, v88, v89
	v_cvt_pk_bf16_f32 v175, v90, v91
	ds_write_b64 v149, v[174:175] offset:3072
	v_cvt_pk_bf16_f32 v174, v92, v93
	v_cvt_pk_bf16_f32 v175, v94, v95
	ds_write_b64 v149, v[174:175] offset:3584
	v_cvt_pk_bf16_f32 v174, v96, v97
	v_cvt_pk_bf16_f32 v175, v98, v99
	ds_write_b64 v149, v[174:175] offset:4096
	v_cvt_pk_bf16_f32 v174, v100, v101
	v_cvt_pk_bf16_f32 v175, v102, v103
	ds_write_b64 v149, v[174:175] offset:4608
	v_cvt_pk_bf16_f32 v174, v104, v105
	v_cvt_pk_bf16_f32 v175, v106, v107
	ds_write_b64 v149, v[174:175] offset:5120
	v_cvt_pk_bf16_f32 v174, v108, v109
	v_cvt_pk_bf16_f32 v175, v110, v111
	ds_write_b64 v149, v[174:175] offset:5632
	v_cvt_pk_bf16_f32 v174, v112, v113
	v_cvt_pk_bf16_f32 v175, v114, v115
	ds_write_b64 v149, v[174:175] offset:6144
	v_cvt_pk_bf16_f32 v174, v116, v117
	v_cvt_pk_bf16_f32 v175, v118, v119
	ds_write_b64 v149, v[174:175] offset:6656
	v_cvt_pk_bf16_f32 v174, v120, v121
	v_cvt_pk_bf16_f32 v175, v122, v123
	ds_write_b64 v149, v[174:175] offset:7168
	v_cvt_pk_bf16_f32 v174, v124, v125
	v_cvt_pk_bf16_f32 v175, v126, v127
	ds_write_b64 v149, v[174:175] offset:7680
	s_waitcnt lgkmcnt(0)
	ds_read_b64_tr_b16 v[174:175], v131
	ds_read_b64_tr_b16 v[176:177], v131 offset:256
	ds_read_b64_tr_b16 v[178:179], v163
	ds_read_b64_tr_b16 v[180:181], v163 offset:256
	ds_read_b64_tr_b16 v[182:183], v164
	ds_read_b64_tr_b16 v[184:185], v164 offset:256
	ds_read_b64_tr_b16 v[186:187], v165
	ds_read_b64_tr_b16 v[188:189], v165 offset:256
	ds_read_b64_tr_b16 v[190:191], v166
	ds_read_b64_tr_b16 v[192:193], v166 offset:256
	ds_read_b64_tr_b16 v[194:195], v167
	ds_read_b64_tr_b16 v[196:197], v167 offset:256
	ds_read_b64_tr_b16 v[198:199], v168
	ds_read_b64_tr_b16 v[200:201], v168 offset:256
	ds_read_b64_tr_b16 v[202:203], v169
	ds_read_b64_tr_b16 v[204:205], v169 offset:256
	s_waitcnt lgkmcnt(0)
	s_waitcnt lgkmcnt(14)
	ds_write_b128 v150, v[174:177]
	s_waitcnt lgkmcnt(13)
	ds_write_b128 v151, v[178:181]
	s_waitcnt lgkmcnt(12)
	ds_write_b128 v152, v[182:185]
	s_waitcnt lgkmcnt(11)
	ds_write_b128 v153, v[186:189]
	s_waitcnt lgkmcnt(10)
	ds_write_b128 v154, v[190:193]
	s_waitcnt lgkmcnt(9)
	ds_write_b128 v155, v[194:197]
	s_waitcnt lgkmcnt(8)
	ds_write_b128 v156, v[198:201]
	s_waitcnt lgkmcnt(7)
	ds_write_b128 v157, v[202:205]
	s_waitcnt lgkmcnt(0)
	ds_read_b128 v[174:177], v170
	ds_read_b128 v[178:181], v171
	ds_read_b128 v[182:185], v158
	ds_read_b128 v[186:189], v159
	v_lshl_add_u64 v[190:191], s[22:23], 0, v[136:137]
	v_lshl_add_u64 v[170:171], v[190:191], 0, v[144:145]
	s_waitcnt lgkmcnt(3)
	global_store_dwordx4 v[170:171], v[174:177], off
	s_waitcnt lgkmcnt(2)
	global_store_dwordx4 v[170:171], v[178:181], off offset:16
	v_lshl_add_u64 v[170:171], v[190:191], 0, v[138:139]
	s_waitcnt lgkmcnt(1)
	global_store_dwordx4 v[170:171], v[182:185], off
	s_waitcnt lgkmcnt(0)
	global_store_dwordx4 v[170:171], v[186:189], off offset:16
	ds_read_b128 v[174:177], v172
	ds_read_b128 v[170:173], v173
	ds_read_b128 v[178:181], v160
	ds_read_b128 v[182:185], v161
	v_lshl_add_u64 v[186:187], v[190:191], 0, v[140:141]
	s_waitcnt lgkmcnt(3)
	global_store_dwordx4 v[186:187], v[174:177], off
	s_waitcnt lgkmcnt(2)
	global_store_dwordx4 v[186:187], v[170:173], off offset:16
	s_nop 1
	v_lshl_add_u64 v[170:171], v[190:191], 0, v[142:143]
	s_waitcnt lgkmcnt(1)
	global_store_dwordx4 v[170:171], v[178:181], off
	s_waitcnt lgkmcnt(0)
	global_store_dwordx4 v[170:171], v[182:185], off offset:16
	s_waitcnt lgkmcnt(0)

; __device__ __forceinline__ void t64_load(const float* Wsrc, int ldw, int lane, f32x4 (&tv)[16]) {
;     const float* p = Wsrc + (size_t)(lane >> 3) * ldw + 4 * (lane & 7);
; #pragma unroll
;     for (int i = 0; i < 16; ++i) { tv[i] = __builtin_nontemporal_load((const f32x4*)p); p += 8 * ldw; }
; }
; __device__ __forceinline__ XItem sitem(const float* w_in, const float* w_out, bf16* BTIN, bf16* BTOUT, int r) {
;     XItem it; it.f8 = 0; it.ldd = DM * 2;
;     if (r < CVS_IN) { const int nblk = INW / 32, kb = r / nblk, nb = r % nblk; it.src = w_in + (size_t)(128 * kb) * INW + win_src_col(32 * nb); it.ldw = INW;
;         it.dst = (unsigned char*)BTIN + ((size_t)(32 * nb) * DM + 128 * kb) * 2; return it; }
;     r -= CVS_IN;
;     { const int nblk = DM / 32, kb = r / nblk, nb = r % nblk; it.src = w_out + (size_t)(128 * kb) * DM + 32 * nb; it.ldw = DM;
;         it.dst = (unsigned char*)BTOUT + ((size_t)(32 * nb) * DM + 128 * kb) * 2; return it; }
; }
.LBB0_35:
	s_add_u32 s33, s26, s66
	s_addc_u32 s66, s27, s67
	s_lshl_b64 s[22:23], s[22:23], 12
	s_lshl_b64 s[64:65], s[64:65], 1
	s_add_u32 s22, s33, s22
	s_addc_u32 s23, s66, s23
	s_add_u32 s22, s22, s64
	s_addc_u32 s23, s23, s65
	v_mad_i64_i32 v[64:65], s[64:65], s0, v130, 0
	v_lshl_add_u64 v[64:65], v[64:65], 2, s[62:63]
	v_lshlrev_b32_e32 v134, 2, v132
	v_lshl_add_u64 v[64:65], v[64:65], 0, v[134:135]
	s_lshl_b32 s0, s0, 5
	v_lshl_add_u64 v[72:73], v[64:65], 0, s[0:1]
	global_load_dwordx4 v[64:67], v[64:65], off nt
	s_nop 0
	global_load_dwordx4 v[68:71], v[72:73], off nt
	v_lshl_add_u64 v[72:73], v[72:73], 0, s[0:1]
	v_lshl_add_u64 v[80:81], v[72:73], 0, s[0:1]
	global_load_dwordx4 v[72:75], v[72:73], off nt
	s_nop 0
	global_load_dwordx4 v[76:79], v[80:81], off nt
	v_lshl_add_u64 v[80:81], v[80:81], 0, s[0:1]
	v_lshl_add_u64 v[88:89], v[80:81], 0, s[0:1]
	global_load_dwordx4 v[80:83], v[80:81], off nt
	s_nop 0
	global_load_dwordx4 v[84:87], v[88:89], off nt
	v_lshl_add_u64 v[88:89], v[88:89], 0, s[0:1]
	v_lshl_add_u64 v[96:97], v[88:89], 0, s[0:1]
	v_lshl_add_u64 v[100:101], v[96:97], 0, s[0:1]
	v_lshl_add_u64 v[104:105], v[100:101], 0, s[0:1]
	v_lshl_add_u64 v[108:109], v[104:105], 0, s[0:1]
	v_lshl_add_u64 v[112:113], v[108:109], 0, s[0:1]
	v_lshl_add_u64 v[116:117], v[112:113], 0, s[0:1]
	v_lshl_add_u64 v[120:121], v[116:117], 0, s[0:1]
	v_lshl_add_u64 v[124:125], v[120:121], 0, s[0:1]
	global_load_dwordx4 v[88:91], v[88:89], off nt
	s_nop 0
	global_load_dwordx4 v[92:95], v[96:97], off nt
	s_nop 0
	global_load_dwordx4 v[96:99], v[100:101], off nt
	s_nop 0
	global_load_dwordx4 v[100:103], v[104:105], off nt
	s_nop 0
	global_load_dwordx4 v[104:107], v[108:109], off nt
	s_nop 0
	global_load_dwordx4 v[108:111], v[112:113], off nt
	s_nop 0
	global_load_dwordx4 v[112:115], v[116:117], off nt
	s_nop 0
	global_load_dwordx4 v[116:119], v[120:121], off nt
	s_nop 0
	global_load_dwordx4 v[120:123], v[124:125], off nt
	v_lshl_add_u64 v[124:125], v[124:125], 0, s[0:1]
	global_load_dwordx4 v[124:127], v[124:125], off nt
	s_waitcnt vmcnt(16)
	s_branch .LcvwP0_a

; #define GAS __attribute__((address_space(1)))
; __device__ __forceinline__ void t64_finish(const f32x4 (&tv)[16], unsigned char* dst, int ldd, int f8, LAS unsigned char* scr, int lane) {
;     const int g = lane >> 4, i16 = lane & 15;
; #pragma unroll
;     for (int i = 0; i < 16; ++i) { v2u w; w.x = cvt_pk_bf16(tv[i].x, tv[i].y); w.y = cvt_pk_bf16(tv[i].z, tv[i].w); *(LAS v2u*)(scr + (8 * i + (lane >> 3)) * 64 + 8 * (lane & 7)) = w; }
;     LDS_WAIT(); asm volatile("" ::: "memory");
;     const int q = i16 >> 2, pp = i16 & 3;
;     bf16x8 o[8];
; #pragma unroll
;     for (int jj = 0; jj < 8; ++jj) { const int c = 4 * jj + g, nb = c & 1, kg = c >> 1;
;         LAS unsigned char* ra = scr + (8 * kg + q) * 64 + 32 * nb + 8 * pp;
;         const s16x4 lo = __builtin_bit_cast(s16x4, __builtin_amdgcn_ds_read_tr16_b64_v4i16((LAS s16x4*)ra));
;         const s16x4 hi = __builtin_bit_cast(s16x4, __builtin_amdgcn_ds_read_tr16_b64_v4i16((LAS s16x4*)(ra + 4 * 64)));
;         o[jj] = __builtin_shufflevector(lo, hi, 0, 1, 2, 3, 4, 5, 6, 7); }
;     LDS_WAIT(); asm volatile("" ::: "memory");
; #pragma unroll
;     for (int jj = 0; jj < 8; ++jj) { const int c = 4 * jj + g, nb = c & 1, kg = c >> 1; const int n = 16 * nb + i16;
;         *(LAS bf16x8*)(scr + n * 256 + 16 * (kg ^ (n & 15))) = o[jj]; }
;     LDS_WAIT(); asm volatile("" ::: "memory");
;     const int rr = lane >> 3, cc = lane & 7;
; #pragma unroll
;     for (int it = 0; it < 4; ++it) { const int n = 8 * it + rr;
;         const v4u v0 = *(const LAS v4u*)(scr + n * 256 + 16 * ((2 * cc) ^ (n & 15))), v1 = *(const LAS v4u*)(scr + n * 256 + 16 * ((2 * cc + 1) ^ (n & 15)));
;         if (f8) { v4u o4; o4.x = pk4_fp8(bf_lo(v0.x) * W8_SCALE, bf_hi(v0.x) * W8_SCALE, bf_lo(v0.y) * W8_SCALE, bf_hi(v0.y) * W8_SCALE);
;             o4.y = pk4_fp8(bf_lo(v0.z) * W8_SCALE, bf_hi(v0.z) * W8_SCALE, bf_lo(v0.w) * W8_SCALE, bf_hi(v0.w) * W8_SCALE);
;             o4.z = pk4_fp8(bf_lo(v1.x) * W8_SCALE, bf_hi(v1.x) * W8_SCALE, bf_lo(v1.y) * W8_SCALE, bf_hi(v1.y) * W8_SCALE);
;             o4.w = pk4_fp8(bf_lo(v1.z) * W8_SCALE, bf_hi(v1.z) * W8_SCALE, bf_lo(v1.w) * W8_SCALE, bf_hi(v1.w) * W8_SCALE);
;             __builtin_nontemporal_store(o4, (GAS v4u*)(dst + (size_t)n * ldd + 16 * cc)); }
;         else { *(GAS v4u*)(dst + (size_t)n * ldd + 32 * cc) = v0; *(GAS v4u*)(dst + (size_t)n * ldd + 32 * cc + 16) = v1; } }
.LcvwP0_a:
	v_cvt_pk_bf16_f32 v170, v0, v1
	v_cvt_pk_bf16_f32 v171, v2, v3
	ds_write_b64 v149, v[170:171]
	v_cvt_pk_bf16_f32 v170, v4, v5
	v_cvt_pk_bf16_f32 v171, v6, v7
	ds_write_b64 v149, v[170:171] offset:512
	v_cvt_pk_bf16_f32 v170, v8, v9
	v_cvt_pk_bf16_f32 v171, v10, v11
	ds_write_b64 v149, v[170:171] offset:1024
	v_cvt_pk_bf16_f32 v170, v12, v13
	v_cvt_pk_bf16_f32 v171, v14, v15
	ds_write_b64 v149, v[170:171] offset:1536
	v_cvt_pk_bf16_f32 v170, v16, v17
	v_cvt_pk_bf16_f32 v171, v18, v19
	ds_write_b64 v149, v[170:171] offset:2048
	v_cvt_pk_bf16_f32 v170, v20, v21
	v_cvt_pk_bf16_f32 v171, v22, v23
	ds_write_b64 v149, v[170:171] offset:2560
	v_cvt_pk_bf16_f32 v170, v24, v25
	v_cvt_pk_bf16_f32 v171, v26, v27
	ds_write_b64 v149, v[170:171] offset:3072
	v_cvt_pk_bf16_f32 v170, v28, v29
	v_cvt_pk_bf16_f32 v171, v30, v31
	ds_write_b64 v149, v[170:171] offset:3584
	v_cvt_pk_bf16_f32 v170, v32, v33
	v_cvt_pk_bf16_f32 v171, v34, v35
	ds_write_b64 v149, v[170:171] offset:4096
	v_cvt_pk_bf16_f32 v170, v36, v37
	v_cvt_pk_bf16_f32 v171, v38, v39
	ds_write_b64 v149, v[170:171] offset:4608
	v_cvt_pk_bf16_f32 v170, v40, v41
	v_cvt_pk_bf16_f32 v171, v42, v43
	ds_write_b64 v149, v[170:171] offset:5120
	v_cvt_pk_bf16_f32 v170, v44, v45
	v_cvt_pk_bf16_f32 v171, v46, v47
	ds_write_b64 v149, v[170:171] offset:5632
	v_cvt_pk_bf16_f32 v170, v48, v49
	v_cvt_pk_bf16_f32 v171, v50, v51
	ds_write_b64 v149, v[170:171] offset:6144
	v_cvt_pk_bf16_f32 v170, v52, v53
	v_cvt_pk_bf16_f32 v171, v54, v55
	ds_write_b64 v149, v[170:171] offset:6656
	v_cvt_pk_bf16_f32 v170, v56, v57
	v_cvt_pk_bf16_f32 v171, v58, v59
	ds_write_b64 v149, v[170:171] offset:7168
	v_cvt_pk_bf16_f32 v170, v60, v61
	v_cvt_pk_bf16_f32 v171, v62, v63
	ds_write_b64 v149, v[170:171] offset:7680
	s_waitcnt lgkmcnt(0)
	v_add_u32_e32 v131, v129, v133
	ds_read_b64_tr_b16 v[170:171], v131
	ds_read_b64_tr_b16 v[172:173], v131 offset:256
	ds_read_b64_tr_b16 v[174:175], v163
	ds_read_b64_tr_b16 v[176:177], v163 offset:256
	ds_read_b64_tr_b16 v[178:179], v164
	ds_read_b64_tr_b16 v[180:181], v164 offset:256
	ds_read_b64_tr_b16 v[182:183], v165
	ds_read_b64_tr_b16 v[184:185], v165 offset:256
	ds_read_b64_tr_b16 v[186:187], v166
	ds_read_b64_tr_b16 v[188:189], v166 offset:256
	ds_read_b64_tr_b16 v[190:191], v167
	ds_read_b64_tr_b16 v[192:193], v167 offset:256
	ds_read_b64_tr_b16 v[194:195], v168
	ds_read_b64_tr_b16 v[196:197], v168 offset:256
	ds_read_b64_tr_b16 v[198:199], v169
	ds_read_b64_tr_b16 v[200:201], v169 offset:256
	s_waitcnt lgkmcnt(0)
	s_waitcnt lgkmcnt(14)
	ds_write_b128 v150, v[170:173]
	s_waitcnt lgkmcnt(13)
	ds_write_b128 v151, v[174:177]
	s_waitcnt lgkmcnt(12)
	ds_write_b128 v152, v[178:181]
	s_waitcnt lgkmcnt(11)
	ds_write_b128 v153, v[182:185]
	s_waitcnt lgkmcnt(10)
	ds_write_b128 v154, v[186:189]
	s_waitcnt lgkmcnt(9)
	ds_write_b128 v155, v[190:193]
	s_waitcnt lgkmcnt(8)
	ds_write_b128 v156, v[194:197]
	s_waitcnt lgkmcnt(7)
	ds_write_b128 v157, v[198:201]
	s_waitcnt lgkmcnt(0)
	v_add_u32_e32 v170, v146, v147
	v_add_u32_e32 v171, v146, v148
	ds_read_b128 v[172:175], v170
	ds_read_b128 v[176:179], v171
	ds_read_b128 v[180:183], v158
	ds_read_b128 v[184:187], v159
	v_lshl_add_u64 v[190:191], s[20:21], 0, v[136:137]
	v_lshl_add_u64 v[188:189], v[190:191], 0, v[144:145]
	s_waitcnt lgkmcnt(3)
	global_store_dwordx4 v[188:189], v[172:175], off
	s_waitcnt lgkmcnt(2)
	global_store_dwordx4 v[188:189], v[176:179], off offset:16
	v_lshl_add_u64 v[172:173], v[190:191], 0, v[138:139]
	s_waitcnt lgkmcnt(1)
	global_store_dwordx4 v[172:173], v[180:183], off
	s_waitcnt lgkmcnt(0)
	global_store_dwordx4 v[172:173], v[184:187], off offset:16
	v_add_u32_e32 v172, v162, v147
	v_add_u32_e32 v173, v162, v148
	ds_read_b128 v[174:177], v172
	ds_read_b128 v[178:181], v173
	ds_read_b128 v[182:185], v160
	ds_read_b128 v[186:189], v161
	v_lshl_add_u64 v[192:193], v[190:191], 0, v[140:141]
	s_waitcnt lgkmcnt(3)
	global_store_dwordx4 v[192:193], v[174:177], off
	s_waitcnt lgkmcnt(2)
	global_store_dwordx4 v[192:193], v[178:181], off offset:16
	v_lshl_add_u64 v[174:175], v[190:191], 0, v[142:143]
	s_waitcnt lgkmcnt(1)
	global_store_dwordx4 v[174:175], v[182:185], off
	s_waitcnt lgkmcnt(0)
	global_store_dwordx4 v[174:175], v[186:189], off offset:16
	s_waitcnt lgkmcnt(0)
	s_andn2_b64 vcc, exec, s[60:61]
	s_add_i32 s33, s57, 2
	s_cbranch_vccnz .LBB0_22
	s_cmp_ge_i32 s33, s35
	s_cbranch_scc1 .LcvwP0_b
	s_cmpk_gt_i32 s57, 0x9fd
	s_mov_b64 s[64:65], -1
	s_cbranch_scc0 .LBB0_40
	s_and_b32 s0, s56, 0xffffff80
	s_addk_i32 s0, 0xec00
	s_lshl_b64 s[20:21], s[0:1], 13
	s_add_u32 s60, s8, s20
	s_addc_u32 s61, s9, s21
	s_and_b32 s20, s52, 0x7e0
	s_lshl_b32 s62, s20, 2
	s_add_u32 s60, s60, s62
	s_mov_b32 s21, s1
	s_addc_u32 s61, s61, 0
	s_mov_b64 s[64:65], 0
	s_mov_b64 s[62:63], s[0:1]

; #define LAS __attribute__((address_space(3)))
; __device__ __forceinline__ int lane_id_v() { int l; asm volatile("v_mbcnt_lo_u32_b32 %0, -1, 0\n\tv_mbcnt_hi_u32_b32 %0, -1, %0" : "=v"(l)); return l; }
; __device__ __forceinline__ XItem xitem(const float* w_gate, const float* w_up, const float* w_down, bf16* BTGU, bf16* BTD, int r) {
;     XItem it;
;     if (r < CV_GU) { const int per = (DM / 128) * (DFF / 32); const int e = r / (2 * per), r2 = r % (2 * per), which = r2 / per, r3 = r2 % per; const int nblk = DFF / 32, kb = r3 / nblk, nb = r3 % nblk;
;         const float* W = (which ? w_up : w_gate) + (size_t)e * DM * DFF;
;         const int f0 = 32 * nb, brow = 256 * (f0 >> 7) + 128 * which + (f0 & 127);
;         it.src = W + (size_t)(128 * kb) * DFF + f0; it.ldw = DFF; it.dst = (unsigned char*)BTGU + ((size_t)e * 2048 + brow) * DM + 128 * kb; it.ldd = DM; it.f8 = 1; return it; }
;     r -= CV_GU;
;     { const int per = (DFF / 128) * (DM / 32); const int e = r / per, r3 = r % per; const int nblk = DM / 32, kb = r3 / nblk, nb = r3 % nblk;
;         it.src = w_down + (size_t)e * DFF * DM + (size_t)(128 * kb) * DM + 32 * nb; it.ldw = DM; it.dst = (unsigned char*)BTD + ((size_t)e * DM + 32 * nb) * DFF + 128 * kb; it.ldd = DFF; it.f8 = 1; return it; }
; }
; __device__ __forceinline__ void convert_range(const float* w_gate, const float* w_up, const float* w_down, bf16* BTGU, bf16* BTD, int x0, int x1, LAS unsigned char* scr, int lane) {
;     if (x0 >= x1) return;
;     f32x4 ta[16], tc[16];
;     XItem A = xitem(w_gate, w_up, w_down, BTGU, BTD, x0), B = A;
;     t64_load(A.src, A.ldw, lane, ta);
; __global__ void __launch_bounds__(512, 2) hymba_fwd(Args args) {
;     ...
;         {   const int lane = lane_id_v();
;             const int nb = FB > 0 ? FB : G, ti = FB > 0 ? bx - GG : bx;
;             if (ti >= 0) { const int q = (CV_N1 + nb * 8 - 1) / (nb * 8), x0 = (ti * 8 + wave) * q, x1 = (x0 + q < CV_N1) ? x0 + q : CV_N1;
;                 convert_range(args.w_gate, args.w_up, args.w_down, BTGU, BTD, x0, x1, lds + wave * 8448, lane); }
.LBB0_140:
	s_sub_i32 s9, s3, s93
	s_cmp_gt_i32 s9, 0
	s_cselect_b64 s[0:1], -1, 0
	s_and_b64 s[20:21], s[0:1], exec
	s_cselect_b32 s8, s93, 0
	s_sub_i32 s8, s2, s8
	s_cmp_lt_i32 s8, 0
	v_readlane_b32 s93, v255, 4
	v_mbcnt_lo_u32_b32 v64, -1, 0
	v_mbcnt_hi_u32_b32 v64, -1, v64
	s_cbranch_scc1 .LBB0_150
	s_and_b64 s[0:1], s[0:1], exec
	s_cselect_b32 s0, s9, s3
	s_lshl_b32 s0, s0, 3
	s_abs_i32 s1, s0
	v_cvt_f32_u32_e32 v0, s1
	s_sub_i32 s20, 0, s1
	s_add_i32 s9, s0, 0x77ff
	s_xor_b32 s0, s9, s0
	v_rcp_iflag_f32_e32 v0, v0
	s_abs_i32 s9, s9
	s_ashr_i32 s0, s0, 31
	v_mul_f32_e32 v0, 0x4f7ffffe, v0
	v_cvt_u32_f32_e32 v0, v0
	s_nop 0
	v_readfirstlane_b32 s21, v0
	s_mul_i32 s20, s20, s21
	s_mul_hi_u32 s20, s21, s20
	s_add_i32 s21, s21, s20
	s_mul_hi_u32 s20, s9, s21
	s_mul_i32 s21, s20, s1
	s_sub_i32 s9, s9, s21
	s_add_i32 s22, s20, 1
	s_sub_i32 s21, s9, s1
	s_cmp_ge_u32 s9, s1
	s_cselect_b32 s20, s22, s20
	s_cselect_b32 s9, s21, s9
	s_add_i32 s21, s20, 1
	s_cmp_ge_u32 s9, s1
	s_cselect_b32 s1, s21, s20
	s_lshl_b32 s8, s8, 3
	s_xor_b32 s1, s1, s0
	s_sub_i32 s0, s1, s0
	s_add_i32 s8, s8, s92
	s_mul_i32 s56, s0, s8
	s_add_i32 s0, s56, s0
	s_min_i32 s52, s0, 0x7800
	s_cmp_ge_i32 s56, s52
	s_cbranch_scc1 .LBB0_150
	s_mul_i32 s0, s92, 0x2100
	s_add_i32 s8, s0, 0
	s_ashr_i32 s0, s56, 31
	s_lshr_b32 s0, s0, 22
	s_add_i32 s1, s56, s0
	s_ashr_i32 s0, s1, 10
	s_and_b32 s1, s1, 0xfffffc00
	s_sub_i32 s1, s56, s1
	s_lshr_b32 s9, s1, 22
	s_and_b32 s9, s9, 0x1ff
	s_add_i32 s9, s1, s9
	s_sext_i32_i16 s20, s9
	s_and_b32 s9, s9, 0xfe00
	s_sub_i32 s9, s1, s9
	s_ashr_i32 s22, s20, 9
	s_sext_i32_i16 s20, s9
	s_bfe_u32 s20, s20, 0x5001a
	s_add_i32 s20, s9, s20
	s_sext_i32_i16 s23, s20
	s_and_b32 s20, s20, 0xffe0
	s_sub_i32 s9, s9, s20
	s_addk_i32 s1, 0x1ff
	s_cmpk_lt_u32 s1, 0x3ff
	s_cselect_b32 s33, s29, s31
	s_cselect_b32 s40, s28, s30
	s_ashr_i32 s1, s0, 31
	s_lshl_b64 s[20:21], s[0:1], 23
	s_sext_i32_i16 s9, s9
	s_add_u32 s54, s40, s20
	s_addc_u32 s21, s33, s21
	s_lshl_b32 s20, s9, 5
	s_lshl_b32 s9, s9, 6
	s_and_b32 s9, s9, 0xffffff00
	s_lshl_b32 s22, s22, 7
	s_add_i32 s9, s9, s22
	s_and_b32 s22, s20, 0x60
	s_or_b32 s22, s9, s22
	s_lshl_b32 s9, s23, 2
	s_and_b32 s40, s9, 0xffffff80
	s_ashr_i32 s41, s40, 31
	s_lshl_b64 s[62:63], s[40:41], 12
	s_add_u32 s9, s54, s62
	s_addc_u32 s23, s21, s63
	s_ashr_i32 s21, s20, 31
	s_lshl_b64 s[20:21], s[20:21], 2
	v_ashrrev_i32_e32 v66, 3, v64
	s_add_u32 s20, s9, s20
	v_ashrrev_i32_e32 v67, 31, v66
	v_lshlrev_b32_e32 v0, 2, v64
	s_addc_u32 s21, s23, s21
	v_and_b32_e32 v128, 28, v0
	v_lshlrev_b64 v[132:133], 12, v[66:67]
	v_mov_b32_e32 v131, 0
	v_lshl_add_u64 v[0:1], s[20:21], 0, v[132:133]
	v_lshlrev_b32_e32 v130, 2, v128
	v_lshl_add_u64 v[0:1], v[0:1], 0, v[130:131]
	s_mov_b32 s9, 0x78000
	v_add_co_u32_e32 v2, vcc, s9, v0
	s_mov_b32 s9, 0x70000
	s_nop 0
	v_addc_co_u32_e32 v3, vcc, 0, v1, vcc
	s_waitcnt vmcnt(0)
	v_add_co_u32_e32 v4, vcc, s9, v0
	s_mov_b32 s9, 0x68000
	s_nop 0
	v_addc_co_u32_e32 v5, vcc, 0, v1, vcc
	v_add_co_u32_e32 v6, vcc, s9, v0
	s_mov_b32 s9, 0x60000
	s_nop 0
	v_addc_co_u32_e32 v7, vcc, 0, v1, vcc
	global_load_dwordx4 v[56:59], v[4:5], off nt
	global_load_dwordx4 v[28:31], v[6:7], off nt
	v_add_co_u32_e32 v4, vcc, s9, v0
	s_mov_b32 s9, 0x58000
	s_nop 0
	v_addc_co_u32_e32 v5, vcc, 0, v1, vcc
	v_add_co_u32_e32 v6, vcc, s9, v0
	s_mov_b32 s9, 0x50000
	s_nop 0
	v_addc_co_u32_e32 v7, vcc, 0, v1, vcc
	global_load_dwordx4 v[52:55], v[4:5], off nt
	global_load_dwordx4 v[24:27], v[6:7], off nt
	v_add_co_u32_e32 v4, vcc, s9, v0
	s_mov_b32 s9, 0x48000
	s_nop 0
	v_addc_co_u32_e32 v5, vcc, 0, v1, vcc
	v_add_co_u32_e32 v6, vcc, s9, v0
	s_mov_b32 s9, 0x40000
	s_nop 0
	v_addc_co_u32_e32 v7, vcc, 0, v1, vcc
	global_load_dwordx4 v[48:51], v[4:5], off nt
	global_load_dwordx4 v[20:23], v[6:7], off nt
	v_add_co_u32_e32 v4, vcc, s9, v0
	s_mov_b32 s9, 0x38000
	s_nop 0
	v_addc_co_u32_e32 v5, vcc, 0, v1, vcc
	v_add_co_u32_e32 v6, vcc, s9, v0
	s_mov_b32 s9, 0x30000
	s_nop 0
	v_addc_co_u32_e32 v7, vcc, 0, v1, vcc
	global_load_dwordx4 v[44:47], v[4:5], off nt
	global_load_dwordx4 v[16:19], v[6:7], off nt
	v_add_co_u32_e32 v4, vcc, s9, v0
	s_mov_b32 s9, 0x28000
	s_nop 0
	v_addc_co_u32_e32 v5, vcc, 0, v1, vcc
	v_add_co_u32_e32 v6, vcc, s9, v0
	s_mov_b32 s9, 0x20000
	s_nop 0
	v_addc_co_u32_e32 v7, vcc, 0, v1, vcc
	global_load_dwordx4 v[40:43], v[4:5], off nt
	global_load_dwordx4 v[12:15], v[6:7], off nt
	v_add_co_u32_e32 v4, vcc, s9, v0
	s_mov_b32 s9, 0x18000
	s_nop 0
	v_addc_co_u32_e32 v5, vcc, 0, v1, vcc
	v_add_co_u32_e32 v6, vcc, s9, v0
	s_mov_b32 s9, 0x10000
	s_nop 0
	v_addc_co_u32_e32 v7, vcc, 0, v1, vcc
	global_load_dwordx4 v[36:39], v[4:5], off nt
	global_load_dwordx4 v[8:11], v[6:7], off nt
	v_add_co_u32_e32 v4, vcc, s9, v0
	s_mov_b32 s9, 0x8000
	s_nop 0
	v_addc_co_u32_e32 v5, vcc, 0, v1, vcc
	v_add_co_u32_e32 v6, vcc, s9, v0
	v_lshlrev_b32_e32 v65, 3, v64
	s_nop 0
	v_addc_co_u32_e32 v7, vcc, 0, v1, vcc
	global_load_dwordx4 v[32:35], v[4:5], off nt
	s_nop 0
	global_load_dwordx4 v[4:7], v[6:7], off nt
	s_nop 0
	global_load_dwordx4 v[60:63], v[2:3], off nt
	s_nop 0
	global_load_dwordx4 v[0:3], v[0:1], off nt
	v_and_b32_e32 v68, 0xffffffc0, v65
	v_add_u32_e32 v72, s8, v68
	v_ashrrev_i32_e32 v68, 4, v64
	v_lshlrev_b32_e32 v71, 5, v68
	v_and_b32_e32 v73, 56, v65
	v_bfe_u32 v69, v64, 2, 2
	v_lshlrev_b32_e32 v70, 2, v68
	v_and_b32_e32 v71, 32, v71
	v_and_b32_e32 v65, 24, v65
	s_mov_b32 s9, 0x3fffff8
	v_add3_u32 v129, s8, v71, v65
	v_and_or_b32 v65, v70, s9, v69
	v_lshlrev_b32_e32 v146, 6, v65
	v_lshlrev_b32_e32 v65, 8, v64
	v_and_b32_e32 v65, 0x1f00, v65
	v_add_u32_e32 v81, s8, v65
	v_ashrrev_i32_e32 v65, 5, v64
; #define LAS __attribute__((address_space(3)))
; #define LDS_WAIT() asm volatile("s_waitcnt lgkmcnt(0)" ::: "memory")
; __device__ __forceinline__ unsigned cvt_pk_bf16(float lo, float hi) { unsigned r; asm volatile("v_cvt_pk_bf16_f32 %0, %1, %2" : "=v"(r) : "v"(lo), "v"(hi)); return r; }
; __device__ __forceinline__ void t64_finish(const f32x4 (&tv)[16], unsigned char* dst, int ldd, int f8, LAS unsigned char* scr, int lane) {
;     const int g = lane >> 4, i16 = lane & 15;
; #pragma unroll
;     for (int i = 0; i < 16; ++i) { v2u w; w.x = cvt_pk_bf16(tv[i].x, tv[i].y); w.y = cvt_pk_bf16(tv[i].z, tv[i].w); *(LAS v2u*)(scr + (8 * i + (lane >> 3)) * 64 + 8 * (lane & 7)) = w; }
;     LDS_WAIT(); asm volatile("" ::: "memory");
;     const int q = i16 >> 2, pp = i16 & 3;
;     bf16x8 o[8];
; #pragma unroll
;     for (int jj = 0; jj < 8; ++jj) { const int c = 4 * jj + g, nb = c & 1, kg = c >> 1;
;         LAS unsigned char* ra = scr + (8 * kg + q) * 64 + 32 * nb + 8 * pp;
;         const s16x4 lo = __builtin_bit_cast(s16x4, __builtin_amdgcn_ds_read_tr16_b64_v4i16((LAS s16x4*)ra));
;         const s16x4 hi = __builtin_bit_cast(s16x4, __builtin_amdgcn_ds_read_tr16_b64_v4i16((LAS s16x4*)(ra + 4 * 64)));
;         o[jj] = __builtin_shufflevector(lo, hi, 0, 1, 2, 3, 4, 5, 6, 7); }
;     LDS_WAIT(); asm volatile("" ::: "memory");
; #pragma unroll
;     for (int jj = 0; jj < 8; ++jj) { const int c = 4 * jj + g, nb = c & 1, kg = c >> 1; const int n = 16 * nb + i16;
;         *(LAS bf16x8*)(scr + n * 256 + 16 * (kg ^ (n & 15))) = o[jj]; }
	v_bitop3_b32 v65, v65, v64, 15 bitop3:0x78
	v_lshlrev_b32_e32 v82, 4, v65
	v_add_u32_e32 v65, 4, v68
	v_lshrrev_b32_e32 v65, 1, v65
	v_bitop3_b32 v65, v65, v64, 15 bitop3:0x78
	v_lshlrev_b32_e32 v83, 4, v65
	v_add_u32_e32 v65, 8, v68
	v_lshrrev_b32_e32 v65, 1, v65
	v_bitop3_b32 v65, v65, v64, 15 bitop3:0x78
	v_lshlrev_b32_e32 v84, 4, v65
	v_add_u32_e32 v65, 12, v68
	v_lshrrev_b32_e32 v65, 1, v65
	v_bitop3_b32 v65, v65, v64, 15 bitop3:0x78
	v_lshlrev_b32_e32 v85, 4, v65
	v_add_u32_e32 v65, 16, v68
	v_lshrrev_b32_e32 v65, 1, v65
	v_bitop3_b32 v65, v65, v64, 15 bitop3:0x78
	v_lshlrev_b32_e32 v86, 4, v65
	v_add_u32_e32 v65, 20, v68
	v_lshrrev_b32_e32 v65, 1, v65
	v_bitop3_b32 v65, v65, v64, 15 bitop3:0x78
	v_lshlrev_b32_e32 v87, 4, v65
	v_add_u32_e32 v65, 24, v68
	v_lshrrev_b32_e32 v65, 1, v65
	v_bitop3_b32 v65, v65, v64, 15 bitop3:0x78
	v_lshlrev_b32_e32 v88, 4, v65
	v_add_u32_e32 v65, 28, v68
	s_ashr_i32 s23, s22, 31
	v_lshrrev_b32_e32 v65, 1, v65
	s_lshl_b64 s[0:1], s[0:1], 22
	s_lshl_b64 s[22:23], s[22:23], 11
	v_bitop3_b32 v65, v65, v64, 15 bitop3:0x78
	v_and_b32_e32 v64, 7, v64
	s_add_u32 s0, s35, s0
	v_lshlrev_b32_e32 v71, 1, v64
	v_lshlrev_b32_e32 v134, 4, v64
	v_and_b32_e32 v64, 15, v66
	s_addc_u32 s1, s53, s1
	v_bitop3_b32 v64, v71, v64, 1 bitop3:0x36
	s_add_u32 s0, s0, s22
	v_lshlrev_b32_e32 v89, 4, v65
	v_bitop3_b32 v65, v66, v71, 15 bitop3:0x6c
	v_lshlrev_b32_e32 v149, 4, v64
	v_add_u32_e32 v64, 8, v66
	v_add_u32_e32 v70, 24, v66
	s_addc_u32 s1, s1, s23
	v_or_b32_e32 v90, 1, v71
	v_lshlrev_b32_e32 v148, 4, v65
	v_bitop3_b32 v65, v64, v71, 15 bitop3:0x6c
	v_bitop3_b32 v71, v70, v71, 15 bitop3:0x6c
	s_add_u32 s0, s0, s40
	v_lshlrev_b32_e32 v92, 4, v65
	v_bitop3_b32 v65, v64, v90, 15 bitop3:0x6c
	v_add_u32_e32 v68, 16, v66
	v_lshlrev_b32_e32 v95, 4, v71
	v_bitop3_b32 v71, v70, v90, 15 bitop3:0x6c
	s_addc_u32 s1, s1, s41
	v_add_u32_e32 v74, 0x400, v146
	v_add_u32_e32 v75, 0x800, v146
	v_add_u32_e32 v76, 0xc00, v146
	v_add_u32_e32 v77, 0x1000, v146
	v_add_u32_e32 v78, 0x1400, v146
	v_add_u32_e32 v79, 0x1800, v146
	v_add_u32_e32 v80, 0x1c00, v146
	v_lshl_add_u32 v91, v64, 8, s8
	v_lshlrev_b32_e32 v93, 4, v65
	v_ashrrev_i32_e32 v65, 31, v64
	v_ashrrev_i32_e32 v69, 31, v68
	v_lshl_add_u32 v94, v70, 8, s8
	v_lshlrev_b32_e32 v90, 4, v71
	v_ashrrev_i32_e32 v71, 31, v70
	v_mov_b32_e32 v135, v131
	v_lshl_add_u32 v147, v66, 8, s8
	v_lshl_add_u32 v150, v68, 8, s8
	v_lshlrev_b64 v[136:137], 11, v[66:67]
	v_lshlrev_b64 v[138:139], 11, v[64:65]
	v_lshlrev_b64 v[140:141], 11, v[68:69]
	v_lshlrev_b64 v[142:143], 11, v[70:71]
	v_add_u32_e32 v151, v72, v73
	v_add_u32_e32 v152, v129, v74
	v_add_u32_e32 v153, v129, v75
	v_add_u32_e32 v154, v129, v76
	v_add_u32_e32 v155, v129, v77
	v_add_u32_e32 v156, v129, v78
	v_add_u32_e32 v157, v129, v79
	v_add_u32_e32 v158, v129, v80
	v_add_u32_e32 v159, v81, v82
	v_add_u32_e32 v160, v81, v83
	v_add_u32_e32 v161, v81, v84
	v_add_u32_e32 v162, v81, v85
	v_add_u32_e32 v163, v81, v86
	v_add_u32_e32 v164, v81, v87
	v_add_u32_e32 v165, v81, v88
	v_add_u32_e32 v166, v81, v89
	v_add_u32_e32 v167, v91, v92
	v_add_u32_e32 v168, v91, v93
	v_add_u32_e32 v169, v94, v95
	v_add_u32_e32 v170, v94, v90
	s_mov_b64 s[8:9], s[0:1]
	s_branch .LBB0_145
.LcvwP1_b:
	s_waitcnt vmcnt(0)
.LBB0_143:
	v_cvt_pk_bf16_f32 v174, v64, v65
	v_cvt_pk_bf16_f32 v175, v66, v67
	ds_write_b64 v151, v[174:175]
	v_cvt_pk_bf16_f32 v174, v68, v69
	v_cvt_pk_bf16_f32 v175, v70, v71
	ds_write_b64 v151, v[174:175] offset:512
	v_cvt_pk_bf16_f32 v174, v72, v73
	v_cvt_pk_bf16_f32 v175, v74, v75
	ds_write_b64 v151, v[174:175] offset:1024
	v_cvt_pk_bf16_f32 v174, v76, v77
	v_cvt_pk_bf16_f32 v175, v78, v79
	ds_write_b64 v151, v[174:175] offset:1536
	v_cvt_pk_bf16_f32 v174, v80, v81
	v_cvt_pk_bf16_f32 v175, v82, v83
	ds_write_b64 v151, v[174:175] offset:2048
	v_cvt_pk_bf16_f32 v174, v84, v85
	v_cvt_pk_bf16_f32 v175, v86, v87
	ds_write_b64 v151, v[174:175] offset:2560
	v_cvt_pk_bf16_f32 v174, v88, v89
	v_cvt_pk_bf16_f32 v175, v90, v91
	ds_write_b64 v151, v[174:175] offset:3072
	v_cvt_pk_bf16_f32 v174, v92, v93
	v_cvt_pk_bf16_f32 v175, v94, v95
	ds_write_b64 v151, v[174:175] offset:3584
	v_cvt_pk_bf16_f32 v174, v96, v97
	v_cvt_pk_bf16_f32 v175, v98, v99
	ds_write_b64 v151, v[174:175] offset:4096
	v_cvt_pk_bf16_f32 v174, v100, v101
	v_cvt_pk_bf16_f32 v175, v102, v103
	ds_write_b64 v151, v[174:175] offset:4608
	v_cvt_pk_bf16_f32 v174, v104, v105
	v_cvt_pk_bf16_f32 v175, v106, v107
	ds_write_b64 v151, v[174:175] offset:5120
	v_cvt_pk_bf16_f32 v174, v108, v109
	v_cvt_pk_bf16_f32 v175, v110, v111
	ds_write_b64 v151, v[174:175] offset:5632
	v_cvt_pk_bf16_f32 v174, v112, v113
	v_cvt_pk_bf16_f32 v175, v114, v115
	ds_write_b64 v151, v[174:175] offset:6144
	v_cvt_pk_bf16_f32 v174, v116, v117
	v_cvt_pk_bf16_f32 v175, v118, v119
	ds_write_b64 v151, v[174:175] offset:6656
	v_cvt_pk_bf16_f32 v174, v120, v121
	v_cvt_pk_bf16_f32 v175, v122, v123
	ds_write_b64 v151, v[174:175] offset:7168
	v_cvt_pk_bf16_f32 v174, v124, v125
	v_cvt_pk_bf16_f32 v175, v126, v127
	ds_write_b64 v151, v[174:175] offset:7680
	s_waitcnt lgkmcnt(0)
	ds_read_b64_tr_b16 v[174:175], v144
	ds_read_b64_tr_b16 v[176:177], v144 offset:256
	ds_read_b64_tr_b16 v[178:179], v152
	ds_read_b64_tr_b16 v[180:181], v152 offset:256
	ds_read_b64_tr_b16 v[182:183], v153
	ds_read_b64_tr_b16 v[184:185], v153 offset:256
	ds_read_b64_tr_b16 v[186:187], v154
	ds_read_b64_tr_b16 v[188:189], v154 offset:256
	ds_read_b64_tr_b16 v[190:191], v155
	ds_read_b64_tr_b16 v[192:193], v155 offset:256
	ds_read_b64_tr_b16 v[194:195], v156
	ds_read_b64_tr_b16 v[196:197], v156 offset:256
	ds_read_b64_tr_b16 v[198:199], v157
	ds_read_b64_tr_b16 v[200:201], v157 offset:256
	ds_read_b64_tr_b16 v[202:203], v158
	ds_read_b64_tr_b16 v[204:205], v158 offset:256
	s_waitcnt lgkmcnt(0)
; #define GAS __attribute__((address_space(1)))
; #define LAS __attribute__((address_space(3)))
; #define LDS_WAIT() asm volatile("s_waitcnt lgkmcnt(0)" ::: "memory")
; __device__ __forceinline__ unsigned pk4_fp8(float a, float b, float c, float d) { int p = 0; p = __builtin_amdgcn_cvt_pk_fp8_f32(a, b, p, false); p = __builtin_amdgcn_cvt_pk_fp8_f32(c, d, p, true); return (unsigned)p; }
; __device__ __forceinline__ void t64_finish(const f32x4 (&tv)[16], unsigned char* dst, int ldd, int f8, LAS unsigned char* scr, int lane) {
;     ...
;     for (int jj = 0; jj < 8; ++jj) { const int c = 4 * jj + g, nb = c & 1, kg = c >> 1; const int n = 16 * nb + i16;
;         *(LAS bf16x8*)(scr + n * 256 + 16 * (kg ^ (n & 15))) = o[jj]; }
;     LDS_WAIT(); asm volatile("" ::: "memory");
;     const int rr = lane >> 3, cc = lane & 7;
; #pragma unroll
;     for (int it = 0; it < 4; ++it) { const int n = 8 * it + rr;
;         const v4u v0 = *(const LAS v4u*)(scr + n * 256 + 16 * ((2 * cc) ^ (n & 15))), v1 = *(const LAS v4u*)(scr + n * 256 + 16 * ((2 * cc + 1) ^ (n & 15)));
;         if (f8) { v4u o4; o4.x = pk4_fp8(bf_lo(v0.x) * W8_SCALE, bf_hi(v0.x) * W8_SCALE, bf_lo(v0.y) * W8_SCALE, bf_hi(v0.y) * W8_SCALE);
;             o4.y = pk4_fp8(bf_lo(v0.z) * W8_SCALE, bf_hi(v0.z) * W8_SCALE, bf_lo(v0.w) * W8_SCALE, bf_hi(v0.w) * W8_SCALE);
;             o4.z = pk4_fp8(bf_lo(v1.x) * W8_SCALE, bf_hi(v1.x) * W8_SCALE, bf_lo(v1.y) * W8_SCALE, bf_hi(v1.y) * W8_SCALE);
;             o4.w = pk4_fp8(bf_lo(v1.z) * W8_SCALE, bf_hi(v1.z) * W8_SCALE, bf_lo(v1.w) * W8_SCALE, bf_hi(v1.w) * W8_SCALE);
;             __builtin_nontemporal_store(o4, (GAS v4u*)(dst + (size_t)n * ldd + 16 * cc)); }
	s_waitcnt lgkmcnt(14)
	ds_write_b128 v159, v[174:177]
	s_waitcnt lgkmcnt(13)
	ds_write_b128 v160, v[178:181]
	s_waitcnt lgkmcnt(12)
	ds_write_b128 v161, v[182:185]
	s_waitcnt lgkmcnt(11)
	ds_write_b128 v162, v[186:189]
	s_waitcnt lgkmcnt(10)
	ds_write_b128 v163, v[190:193]
	s_waitcnt lgkmcnt(9)
	ds_write_b128 v164, v[194:197]
	s_waitcnt lgkmcnt(8)
	ds_write_b128 v165, v[198:201]
	s_waitcnt lgkmcnt(7)
	ds_write_b128 v166, v[202:205]
	s_waitcnt lgkmcnt(0)
	ds_read_b128 v[174:177], v145
	ds_read_b128 v[178:181], v171
	v_lshl_add_u64 v[144:145], s[8:9], 0, v[134:135]
	v_lshl_add_u64 v[186:187], v[144:145], 0, v[136:137]
	s_waitcnt lgkmcnt(1)
	v_lshlrev_b32_e32 v130, 16, v174
	v_and_b32_e32 v171, 0xffff0000, v174
	v_mul_f32_e32 v130, 0x42800000, v130
	v_mul_f32_e32 v171, 0x42800000, v171
	v_mov_b32_e32 v174, 0
	v_cvt_pk_fp8_f32 v174, v130, v171
	v_lshlrev_b32_e32 v182, 16, v175
	v_and_b32_e32 v171, 0xffff0000, v175
	v_mul_f32_e32 v130, 0x42800000, v182
	v_mul_f32_e32 v171, 0x42800000, v171
	v_cvt_pk_fp8_f32 v174, v130, v171 op_sel:[0,0,1]
	v_lshlrev_b32_e32 v130, 16, v176
	v_and_b32_e32 v171, 0xffff0000, v176
	v_mul_f32_e32 v130, 0x42800000, v130
	v_mul_f32_e32 v171, 0x42800000, v171
	v_mov_b32_e32 v175, 0
	v_cvt_pk_fp8_f32 v175, v130, v171
	v_lshlrev_b32_e32 v176, 16, v177
	v_and_b32_e32 v171, 0xffff0000, v177
	v_mul_f32_e32 v130, 0x42800000, v176
	v_mul_f32_e32 v171, 0x42800000, v171
	v_cvt_pk_fp8_f32 v175, v130, v171 op_sel:[0,0,1]
	s_waitcnt lgkmcnt(0)
	v_lshlrev_b32_e32 v130, 16, v178
	v_and_b32_e32 v171, 0xffff0000, v178
	v_mul_f32_e32 v130, 0x42800000, v130
	v_mul_f32_e32 v171, 0x42800000, v171
	v_mov_b32_e32 v176, 0
	v_cvt_pk_fp8_f32 v176, v130, v171
	v_lshlrev_b32_e32 v177, 16, v179
	v_and_b32_e32 v171, 0xffff0000, v179
	v_mul_f32_e32 v130, 0x42800000, v177
	v_mul_f32_e32 v171, 0x42800000, v171
	v_cvt_pk_fp8_f32 v176, v130, v171 op_sel:[0,0,1]
	v_lshlrev_b32_e32 v130, 16, v180
	v_and_b32_e32 v171, 0xffff0000, v180
	v_lshlrev_b32_e32 v177, 16, v181
	v_mul_f32_e32 v130, 0x42800000, v130
	v_mul_f32_e32 v171, 0x42800000, v171
	v_mul_f32_e32 v182, 0x42800000, v177
	v_mov_b32_e32 v177, 0
	v_cvt_pk_fp8_f32 v177, v130, v171
	v_and_b32_e32 v130, 0xffff0000, v181
	ds_read_b128 v[178:181], v167
	v_mul_f32_e32 v130, 0x42800000, v130
	v_cvt_pk_fp8_f32 v177, v182, v130 op_sel:[0,0,1]
	ds_read_b128 v[182:185], v168
	s_waitcnt lgkmcnt(1)
	v_lshlrev_b32_e32 v130, 16, v178
	v_and_b32_e32 v171, 0xffff0000, v178
	v_mul_f32_e32 v130, 0x42800000, v130
	v_mul_f32_e32 v171, 0x42800000, v171
	v_mov_b32_e32 v178, 0
	v_cvt_pk_fp8_f32 v178, v130, v171
	v_lshlrev_b32_e32 v188, 16, v179
	v_and_b32_e32 v171, 0xffff0000, v179
	v_mul_f32_e32 v130, 0x42800000, v188
	v_mul_f32_e32 v171, 0x42800000, v171
	v_cvt_pk_fp8_f32 v178, v130, v171 op_sel:[0,0,1]
	v_lshlrev_b32_e32 v130, 16, v180
	v_and_b32_e32 v171, 0xffff0000, v180
	v_mul_f32_e32 v130, 0x42800000, v130
	v_mul_f32_e32 v171, 0x42800000, v171
	v_mov_b32_e32 v179, 0
	v_cvt_pk_fp8_f32 v179, v130, v171
	v_lshlrev_b32_e32 v180, 16, v181
	v_and_b32_e32 v171, 0xffff0000, v181
	v_mul_f32_e32 v130, 0x42800000, v180
	v_mul_f32_e32 v171, 0x42800000, v171
	v_cvt_pk_fp8_f32 v179, v130, v171 op_sel:[0,0,1]
	s_waitcnt lgkmcnt(0)
	v_lshlrev_b32_e32 v130, 16, v182
	v_and_b32_e32 v171, 0xffff0000, v182
	v_mul_f32_e32 v130, 0x42800000, v130
	v_mul_f32_e32 v171, 0x42800000, v171
	v_mov_b32_e32 v180, 0
	v_cvt_pk_fp8_f32 v180, v130, v171
	v_lshlrev_b32_e32 v181, 16, v183
	v_and_b32_e32 v171, 0xffff0000, v183
	v_mul_f32_e32 v130, 0x42800000, v181
	v_mul_f32_e32 v171, 0x42800000, v171
	v_cvt_pk_fp8_f32 v180, v130, v171 op_sel:[0,0,1]
	v_lshlrev_b32_e32 v130, 16, v184
	v_and_b32_e32 v171, 0xffff0000, v184
	v_mul_f32_e32 v130, 0x42800000, v130
	v_mul_f32_e32 v171, 0x42800000, v171
	v_lshlrev_b32_e32 v182, 16, v185
	v_mov_b32_e32 v181, 0
	v_cvt_pk_fp8_f32 v181, v130, v171
	v_mul_f32_e32 v130, 0x42800000, v182
	v_and_b32_e32 v171, 0xffff0000, v185
	ds_read_b128 v[182:185], v172
	v_mul_f32_e32 v171, 0x42800000, v171
	v_cvt_pk_fp8_f32 v181, v130, v171 op_sel:[0,0,1]
	global_store_dwordx4 v[186:187], v[174:177], off
	s_waitcnt lgkmcnt(0)
; #define GAS __attribute__((address_space(1)))
; #define LAS __attribute__((address_space(3)))
; __device__ __forceinline__ unsigned pk4_fp8(float a, float b, float c, float d) { int p = 0; p = __builtin_amdgcn_cvt_pk_fp8_f32(a, b, p, false); p = __builtin_amdgcn_cvt_pk_fp8_f32(c, d, p, true); return (unsigned)p; }
; __device__ __forceinline__ void t64_finish(const f32x4 (&tv)[16], unsigned char* dst, int ldd, int f8, LAS unsigned char* scr, int lane) {
;     ...
;     const int rr = lane >> 3, cc = lane & 7;
; #pragma unroll
;     for (int it = 0; it < 4; ++it) { const int n = 8 * it + rr;
;         const v4u v0 = *(const LAS v4u*)(scr + n * 256 + 16 * ((2 * cc) ^ (n & 15))), v1 = *(const LAS v4u*)(scr + n * 256 + 16 * ((2 * cc + 1) ^ (n & 15)));
;         if (f8) { v4u o4; o4.x = pk4_fp8(bf_lo(v0.x) * W8_SCALE, bf_hi(v0.x) * W8_SCALE, bf_lo(v0.y) * W8_SCALE, bf_hi(v0.y) * W8_SCALE);
;             o4.y = pk4_fp8(bf_lo(v0.z) * W8_SCALE, bf_hi(v0.z) * W8_SCALE, bf_lo(v0.w) * W8_SCALE, bf_hi(v0.w) * W8_SCALE);
;             o4.z = pk4_fp8(bf_lo(v1.x) * W8_SCALE, bf_hi(v1.x) * W8_SCALE, bf_lo(v1.y) * W8_SCALE, bf_hi(v1.y) * W8_SCALE);
;             o4.w = pk4_fp8(bf_lo(v1.z) * W8_SCALE, bf_hi(v1.z) * W8_SCALE, bf_lo(v1.w) * W8_SCALE, bf_hi(v1.w) * W8_SCALE);
;             __builtin_nontemporal_store(o4, (GAS v4u*)(dst + (size_t)n * ldd + 16 * cc)); }
	v_lshlrev_b32_e32 v130, 16, v182
	v_and_b32_e32 v171, 0xffff0000, v182
	v_mul_f32_e32 v130, 0x42800000, v130
	v_mul_f32_e32 v171, 0x42800000, v171
	v_mov_b32_e32 v176, 0
	v_cvt_pk_fp8_f32 v176, v130, v171
	v_lshlrev_b32_e32 v177, 16, v183
	v_and_b32_e32 v171, 0xffff0000, v183
	v_mul_f32_e32 v130, 0x42800000, v177
	v_mul_f32_e32 v171, 0x42800000, v171
	v_lshl_add_u64 v[174:175], v[144:145], 0, v[138:139]
	v_cvt_pk_fp8_f32 v176, v130, v171 op_sel:[0,0,1]
	v_lshlrev_b32_e32 v130, 16, v184
	v_and_b32_e32 v171, 0xffff0000, v184
	global_store_dwordx4 v[174:175], v[178:181], off
	ds_read_b128 v[172:175], v173
	v_mul_f32_e32 v130, 0x42800000, v130
	v_mul_f32_e32 v171, 0x42800000, v171
	v_mov_b32_e32 v177, 0
	v_cvt_pk_fp8_f32 v177, v130, v171
	v_lshlrev_b32_e32 v178, 16, v185
	v_and_b32_e32 v171, 0xffff0000, v185
	v_mul_f32_e32 v130, 0x42800000, v178
	v_mul_f32_e32 v171, 0x42800000, v171
	v_cvt_pk_fp8_f32 v177, v130, v171 op_sel:[0,0,1]
	s_waitcnt lgkmcnt(0)
	v_lshlrev_b32_e32 v130, 16, v172
	v_and_b32_e32 v171, 0xffff0000, v172
	v_mul_f32_e32 v130, 0x42800000, v130
	v_mul_f32_e32 v171, 0x42800000, v171
	v_mov_b32_e32 v178, 0
	v_cvt_pk_fp8_f32 v178, v130, v171
	v_lshlrev_b32_e32 v172, 16, v173
	v_and_b32_e32 v171, 0xffff0000, v173
	v_mul_f32_e32 v130, 0x42800000, v172
	v_mul_f32_e32 v171, 0x42800000, v171
	v_cvt_pk_fp8_f32 v178, v130, v171 op_sel:[0,0,1]
	v_lshlrev_b32_e32 v130, 16, v174
	v_and_b32_e32 v171, 0xffff0000, v174
	v_mul_f32_e32 v130, 0x42800000, v130
	v_mul_f32_e32 v171, 0x42800000, v171
	v_mov_b32_e32 v179, 0
	ds_read_b128 v[180:183], v169
	v_cvt_pk_fp8_f32 v179, v130, v171
	v_lshlrev_b32_e32 v172, 16, v175
	v_and_b32_e32 v130, 0xffff0000, v175
	v_mul_f32_e32 v172, 0x42800000, v172
	v_mul_f32_e32 v130, 0x42800000, v130
	v_cvt_pk_fp8_f32 v179, v172, v130 op_sel:[0,0,1]
	ds_read_b128 v[172:175], v170
	s_waitcnt lgkmcnt(1)
	v_lshlrev_b32_e32 v130, 16, v180
	v_and_b32_e32 v171, 0xffff0000, v180
	v_mul_f32_e32 v130, 0x42800000, v130
	v_mul_f32_e32 v171, 0x42800000, v171
	v_mov_b32_e32 v180, 0
	v_cvt_pk_fp8_f32 v180, v130, v171
	v_lshlrev_b32_e32 v184, 16, v181
	v_and_b32_e32 v171, 0xffff0000, v181
	v_mul_f32_e32 v130, 0x42800000, v184
	v_mul_f32_e32 v171, 0x42800000, v171
	v_cvt_pk_fp8_f32 v180, v130, v171 op_sel:[0,0,1]
	v_lshlrev_b32_e32 v130, 16, v182
	v_and_b32_e32 v171, 0xffff0000, v182
	v_mul_f32_e32 v130, 0x42800000, v130
	v_mul_f32_e32 v171, 0x42800000, v171
	v_mov_b32_e32 v181, 0
	v_cvt_pk_fp8_f32 v181, v130, v171
	v_lshlrev_b32_e32 v182, 16, v183
	v_and_b32_e32 v171, 0xffff0000, v183
	v_mul_f32_e32 v130, 0x42800000, v182
	v_mul_f32_e32 v171, 0x42800000, v171
	v_cvt_pk_fp8_f32 v181, v130, v171 op_sel:[0,0,1]
	s_waitcnt lgkmcnt(0)
	v_lshlrev_b32_e32 v130, 16, v172
	v_and_b32_e32 v171, 0xffff0000, v172
	v_mul_f32_e32 v130, 0x42800000, v130
	v_mul_f32_e32 v171, 0x42800000, v171
	v_mov_b32_e32 v182, 0
	v_cvt_pk_fp8_f32 v182, v130, v171
	v_lshlrev_b32_e32 v172, 16, v173
	v_and_b32_e32 v171, 0xffff0000, v173
	v_mul_f32_e32 v130, 0x42800000, v172
	v_mul_f32_e32 v171, 0x42800000, v171
	v_cvt_pk_fp8_f32 v182, v130, v171 op_sel:[0,0,1]
	v_lshlrev_b32_e32 v130, 16, v174
	v_and_b32_e32 v171, 0xffff0000, v174
	v_mul_f32_e32 v130, 0x42800000, v130
	v_mul_f32_e32 v171, 0x42800000, v171
	v_mov_b32_e32 v183, 0
	v_cvt_pk_fp8_f32 v183, v130, v171
	v_lshlrev_b32_e32 v172, 16, v175
	v_and_b32_e32 v171, 0xffff0000, v175
	v_mul_f32_e32 v130, 0x42800000, v172
	v_mul_f32_e32 v171, 0x42800000, v171
	v_cvt_pk_fp8_f32 v183, v130, v171 op_sel:[0,0,1]
	v_lshl_add_u64 v[172:173], v[144:145], 0, v[140:141]
	v_lshl_add_u64 v[144:145], v[144:145], 0, v[142:143]
	global_store_dwordx4 v[172:173], v[176:179], off
	global_store_dwordx4 v[144:145], v[180:183], off
	s_waitcnt lgkmcnt(0)

; #define LAS __attribute__((address_space(3)))
; __device__ __forceinline__ XItem xitem(const float* w_gate, const float* w_up, const float* w_down, bf16* BTGU, bf16* BTD, int r) {
;     XItem it;
;     if (r < CV_GU) { const int per = (DM / 128) * (DFF / 32); const int e = r / (2 * per), r2 = r % (2 * per), which = r2 / per, r3 = r2 % per; const int nblk = DFF / 32, kb = r3 / nblk, nb = r3 % nblk;
;         const float* W = (which ? w_up : w_gate) + (size_t)e * DM * DFF;
;         const int f0 = 32 * nb, brow = 256 * (f0 >> 7) + 128 * which + (f0 & 127);
;         it.src = W + (size_t)(128 * kb) * DFF + f0; it.ldw = DFF; it.dst = (unsigned char*)BTGU + ((size_t)e * 2048 + brow) * DM + 128 * kb; it.ldd = DM; it.f8 = 1; return it; }
;     r -= CV_GU;
;     { const int per = (DFF / 128) * (DM / 32); const int e = r / per, r3 = r % per; const int nblk = DM / 32, kb = r3 / nblk, nb = r3 % nblk;
;         it.src = w_down + (size_t)e * DFF * DM + (size_t)(128 * kb) * DM + 32 * nb; it.ldw = DM; it.dst = (unsigned char*)BTD + ((size_t)e * DM + 32 * nb) * DFF + 128 * kb; it.ldd = DFF; it.f8 = 1; return it; }
; }
; __device__ __forceinline__ void convert_range(const float* w_gate, const float* w_up, const float* w_down, bf16* BTGU, bf16* BTD, int x0, int x1, LAS unsigned char* scr, int lane) {
;     if (x0 >= x1) return;
;     f32x4 ta[16], tc[16];
;     XItem A = xitem(w_gate, w_up, w_down, BTGU, BTD, x0), B = A;
;     t64_load(A.src, A.ldw, lane, ta);
; #pragma unroll 1
;     for (int x = x0; x < x1; x += 2) {
;         const bool hasB = x + 1 < x1;
;         if (hasB) { B = xitem(w_gate, w_up, w_down, BTGU, BTD, x + 1); t64_load(B.src, B.ldw, lane, tc); }
;         t64_finish(ta, A.dst, A.ldd, A.f8, scr, lane);
;         if (hasB) {
;             if (x + 2 < x1) { A = xitem(w_gate, w_up, w_down, BTGU, BTD, x + 2); t64_load(A.src, A.ldw, lane, ta); }
.LBB0_145:
	s_add_i32 s22, s56, 1
	s_cmp_lt_i32 s22, s52
	s_cselect_b64 s[20:21], -1, 0
	s_cmp_ge_i32 s22, s52
	s_cbranch_scc1 .LBB0_147
	s_ashr_i32 s8, s22, 31
	s_lshr_b32 s8, s8, 22
	s_add_i32 s9, s22, s8
	s_ashr_i32 s8, s9, 10
	s_and_b32 s9, s9, 0xfffffc00
	s_sub_i32 s9, s22, s9
	s_lshr_b32 s22, s9, 22
	s_and_b32 s22, s22, 0x1ff
	s_add_i32 s22, s9, s22
	s_sext_i32_i16 s23, s22
	s_and_b32 s22, s22, 0xfe00
	s_sub_i32 s22, s9, s22
	s_ashr_i32 s33, s23, 9
	s_sext_i32_i16 s23, s22
	s_bfe_u32 s23, s23, 0x5001a
	s_add_i32 s23, s22, s23
	s_sext_i32_i16 s41, s23
	s_and_b32 s23, s23, 0xffe0
	s_sub_i32 s22, s22, s23
	s_addk_i32 s9, 0x1ff
	s_cmpk_lt_u32 s9, 0x3ff
	s_cselect_b32 s54, s29, s31
	s_cselect_b32 s55, s28, s30
	s_ashr_i32 s9, s8, 31
	s_sext_i32_i16 s40, s22
	s_lshl_b64 s[22:23], s[8:9], 23
	s_add_u32 s55, s55, s22
	s_addc_u32 s54, s54, s23
	s_lshl_b32 s22, s40, 6
	s_lshl_b32 s62, s40, 5
	s_and_b32 s22, s22, 0xffffff00
	s_lshl_b32 s23, s33, 7
	s_add_i32 s22, s22, s23
	s_and_b32 s23, s62, 0x60
	s_or_b32 s40, s22, s23
	s_lshl_b32 s22, s41, 2
	s_and_b32 s22, s22, 0xffffff80
	s_ashr_i32 s23, s22, 31
	s_lshl_b64 s[64:65], s[22:23], 12
	s_add_u32 s33, s55, s64
	s_addc_u32 s41, s54, s65
	s_ashr_i32 s63, s62, 31
	s_lshl_b64 s[62:63], s[62:63], 2
	s_add_u32 s62, s33, s62
	s_addc_u32 s63, s41, s63
	v_lshl_add_u64 v[64:65], s[62:63], 0, v[132:133]
	v_lshlrev_b32_e32 v130, 2, v128
	v_lshl_add_u64 v[120:121], v[64:65], 0, v[130:131]
	v_add_co_u32_e32 v68, vcc, 0x8000, v120
	s_ashr_i32 s41, s40, 31
	s_nop 0
	v_addc_co_u32_e32 v69, vcc, 0, v121, vcc
	v_add_co_u32_e32 v72, vcc, 0x10000, v120
	global_load_dwordx4 v[64:67], v[120:121], off nt
	s_nop 0
	global_load_dwordx4 v[68:71], v[68:69], off nt
	v_addc_co_u32_e32 v73, vcc, 0, v121, vcc
	v_add_co_u32_e32 v76, vcc, 0x18000, v120
	s_lshl_b64 s[8:9], s[8:9], 22
	s_nop 0
	v_addc_co_u32_e32 v77, vcc, 0, v121, vcc
	v_add_co_u32_e32 v80, vcc, 0x20000, v120
	global_load_dwordx4 v[72:75], v[72:73], off nt
	s_nop 0
	global_load_dwordx4 v[76:79], v[76:77], off nt
	v_addc_co_u32_e32 v81, vcc, 0, v121, vcc
	v_add_co_u32_e32 v84, vcc, 0x28000, v120
	s_lshl_b64 s[40:41], s[40:41], 11
	s_nop 0
	v_addc_co_u32_e32 v85, vcc, 0, v121, vcc
	v_add_co_u32_e32 v88, vcc, 0x30000, v120
	global_load_dwordx4 v[80:83], v[80:81], off nt
	s_nop 0
	global_load_dwordx4 v[84:87], v[84:85], off nt
	v_addc_co_u32_e32 v89, vcc, 0, v121, vcc
	v_add_co_u32_e32 v92, vcc, 0x38000, v120
	s_add_u32 s8, s35, s8
	s_nop 0
	v_addc_co_u32_e32 v93, vcc, 0, v121, vcc
	v_add_co_u32_e32 v96, vcc, 0x40000, v120
	global_load_dwordx4 v[88:91], v[88:89], off nt
	s_nop 0
	global_load_dwordx4 v[92:95], v[92:93], off nt
	v_addc_co_u32_e32 v97, vcc, 0, v121, vcc
	v_add_co_u32_e32 v100, vcc, 0x48000, v120
	s_addc_u32 s9, s53, s9
	s_nop 0
	v_addc_co_u32_e32 v101, vcc, 0, v121, vcc
	v_add_co_u32_e32 v104, vcc, 0x50000, v120
	global_load_dwordx4 v[96:99], v[96:97], off nt
	s_nop 0
	global_load_dwordx4 v[100:103], v[100:101], off nt
	v_addc_co_u32_e32 v105, vcc, 0, v121, vcc
	v_add_co_u32_e32 v108, vcc, 0x58000, v120
	s_add_u32 s8, s8, s40
	s_nop 0
	v_addc_co_u32_e32 v109, vcc, 0, v121, vcc
	v_add_co_u32_e32 v112, vcc, 0x60000, v120
	global_load_dwordx4 v[104:107], v[104:105], off nt
	s_nop 0
	global_load_dwordx4 v[108:111], v[108:109], off nt
	v_addc_co_u32_e32 v113, vcc, 0, v121, vcc
	v_add_co_u32_e32 v116, vcc, 0x68000, v120
	s_addc_u32 s9, s9, s41
	s_nop 0
	v_addc_co_u32_e32 v117, vcc, 0, v121, vcc
	v_add_co_u32_e32 v122, vcc, 0x70000, v120
	global_load_dwordx4 v[112:115], v[112:113], off nt
	s_nop 0
	global_load_dwordx4 v[116:119], v[116:117], off nt
	v_addc_co_u32_e32 v123, vcc, 0, v121, vcc
	v_add_co_u32_e32 v124, vcc, 0x78000, v120
	s_add_u32 s8, s8, s22
	s_nop 0
	v_addc_co_u32_e32 v125, vcc, 0, v121, vcc
	global_load_dwordx4 v[120:123], v[122:123], off nt
	s_nop 0
	global_load_dwordx4 v[124:127], v[124:125], off nt
	s_addc_u32 s9, s9, s23
	s_waitcnt vmcnt(16)
	s_branch .LcvwP1_a

; #define GAS __attribute__((address_space(1)))
; #define LAS __attribute__((address_space(3)))
; #define LDS_WAIT() asm volatile("s_waitcnt lgkmcnt(0)" ::: "memory")
; __device__ __forceinline__ void t64_finish(const f32x4 (&tv)[16], unsigned char* dst, int ldd, int f8, LAS unsigned char* scr, int lane) {
;     const int g = lane >> 4, i16 = lane & 15;
; #pragma unroll
;     for (int i = 0; i < 16; ++i) { v2u w; w.x = cvt_pk_bf16(tv[i].x, tv[i].y); w.y = cvt_pk_bf16(tv[i].z, tv[i].w); *(LAS v2u*)(scr + (8 * i + (lane >> 3)) * 64 + 8 * (lane & 7)) = w; }
;     LDS_WAIT(); asm volatile("" ::: "memory");
;     const int q = i16 >> 2, pp = i16 & 3;
;     bf16x8 o[8];
; #pragma unroll
;     for (int jj = 0; jj < 8; ++jj) { const int c = 4 * jj + g, nb = c & 1, kg = c >> 1;
;         LAS unsigned char* ra = scr + (8 * kg + q) * 64 + 32 * nb + 8 * pp;
;         const s16x4 lo = __builtin_bit_cast(s16x4, __builtin_amdgcn_ds_read_tr16_b64_v4i16((LAS s16x4*)ra));
;         const s16x4 hi = __builtin_bit_cast(s16x4, __builtin_amdgcn_ds_read_tr16_b64_v4i16((LAS s16x4*)(ra + 4 * 64)));
;         o[jj] = __builtin_shufflevector(lo, hi, 0, 1, 2, 3, 4, 5, 6, 7); }
;     LDS_WAIT(); asm volatile("" ::: "memory");
; #pragma unroll
;     for (int jj = 0; jj < 8; ++jj) { const int c = 4 * jj + g, nb = c & 1, kg = c >> 1; const int n = 16 * nb + i16;
;         *(LAS bf16x8*)(scr + n * 256 + 16 * (kg ^ (n & 15))) = o[jj]; }
;     LDS_WAIT(); asm volatile("" ::: "memory");
;     const int rr = lane >> 3, cc = lane & 7;
; #pragma unroll
;     for (int it = 0; it < 4; ++it) { const int n = 8 * it + rr;
;         const v4u v0 = *(const LAS v4u*)(scr + n * 256 + 16 * ((2 * cc) ^ (n & 15))), v1 = *(const LAS v4u*)(scr + n * 256 + 16 * ((2 * cc + 1) ^ (n & 15)));
;         if (f8) { v4u o4; o4.x = pk4_fp8(bf_lo(v0.x) * W8_SCALE, bf_hi(v0.x) * W8_SCALE, bf_lo(v0.y) * W8_SCALE, bf_hi(v0.y) * W8_SCALE);
;             o4.y = pk4_fp8(bf_lo(v0.z) * W8_SCALE, bf_hi(v0.z) * W8_SCALE, bf_lo(v0.w) * W8_SCALE, bf_hi(v0.w) * W8_SCALE);
;             o4.z = pk4_fp8(bf_lo(v1.x) * W8_SCALE, bf_hi(v1.x) * W8_SCALE, bf_lo(v1.y) * W8_SCALE, bf_hi(v1.y) * W8_SCALE);
;             o4.w = pk4_fp8(bf_lo(v1.z) * W8_SCALE, bf_hi(v1.z) * W8_SCALE, bf_lo(v1.w) * W8_SCALE, bf_hi(v1.w) * W8_SCALE);
;             __builtin_nontemporal_store(o4, (GAS v4u*)(dst + (size_t)n * ldd + 16 * cc)); }
.LcvwP1_a:
	v_cvt_pk_bf16_f32 v144, v0, v1
	v_cvt_pk_bf16_f32 v145, v2, v3
	ds_write_b64 v151, v[144:145]
	v_cvt_pk_bf16_f32 v144, v4, v5
	v_cvt_pk_bf16_f32 v145, v6, v7
	ds_write_b64 v151, v[144:145] offset:512
	v_cvt_pk_bf16_f32 v144, v32, v33
	v_cvt_pk_bf16_f32 v145, v34, v35
	ds_write_b64 v151, v[144:145] offset:1024
	v_cvt_pk_bf16_f32 v144, v8, v9
	v_cvt_pk_bf16_f32 v145, v10, v11
	ds_write_b64 v151, v[144:145] offset:1536
	v_cvt_pk_bf16_f32 v144, v36, v37
	v_cvt_pk_bf16_f32 v145, v38, v39
	ds_write_b64 v151, v[144:145] offset:2048
	v_cvt_pk_bf16_f32 v144, v12, v13
	v_cvt_pk_bf16_f32 v145, v14, v15
	ds_write_b64 v151, v[144:145] offset:2560
	v_cvt_pk_bf16_f32 v144, v40, v41
	v_cvt_pk_bf16_f32 v145, v42, v43
	ds_write_b64 v151, v[144:145] offset:3072
	v_cvt_pk_bf16_f32 v144, v16, v17
	v_cvt_pk_bf16_f32 v145, v18, v19
	ds_write_b64 v151, v[144:145] offset:3584
	v_cvt_pk_bf16_f32 v144, v44, v45
	v_cvt_pk_bf16_f32 v145, v46, v47
	ds_write_b64 v151, v[144:145] offset:4096
	v_cvt_pk_bf16_f32 v144, v20, v21
	v_cvt_pk_bf16_f32 v145, v22, v23
	ds_write_b64 v151, v[144:145] offset:4608
	v_cvt_pk_bf16_f32 v144, v48, v49
	v_cvt_pk_bf16_f32 v145, v50, v51
	ds_write_b64 v151, v[144:145] offset:5120
	v_cvt_pk_bf16_f32 v144, v24, v25
	v_cvt_pk_bf16_f32 v145, v26, v27
	ds_write_b64 v151, v[144:145] offset:5632
	v_cvt_pk_bf16_f32 v144, v52, v53
	v_cvt_pk_bf16_f32 v145, v54, v55
	ds_write_b64 v151, v[144:145] offset:6144
	v_cvt_pk_bf16_f32 v144, v28, v29
	v_cvt_pk_bf16_f32 v145, v30, v31
	ds_write_b64 v151, v[144:145] offset:6656
	v_cvt_pk_bf16_f32 v144, v56, v57
	v_cvt_pk_bf16_f32 v145, v58, v59
	ds_write_b64 v151, v[144:145] offset:7168
	v_cvt_pk_bf16_f32 v144, v60, v61
	v_cvt_pk_bf16_f32 v145, v62, v63
	ds_write_b64 v151, v[144:145] offset:7680
	s_waitcnt lgkmcnt(0)
	v_add_u32_e32 v144, v129, v146
	ds_read_b64_tr_b16 v[172:173], v144
	ds_read_b64_tr_b16 v[174:175], v144 offset:256
	ds_read_b64_tr_b16 v[176:177], v152
	ds_read_b64_tr_b16 v[178:179], v152 offset:256
	ds_read_b64_tr_b16 v[180:181], v153
	ds_read_b64_tr_b16 v[182:183], v153 offset:256
	ds_read_b64_tr_b16 v[184:185], v154
	ds_read_b64_tr_b16 v[186:187], v154 offset:256
	ds_read_b64_tr_b16 v[188:189], v155
	ds_read_b64_tr_b16 v[190:191], v155 offset:256
	ds_read_b64_tr_b16 v[192:193], v156
	ds_read_b64_tr_b16 v[194:195], v156 offset:256
	ds_read_b64_tr_b16 v[196:197], v157
	ds_read_b64_tr_b16 v[198:199], v157 offset:256
	ds_read_b64_tr_b16 v[200:201], v158
	ds_read_b64_tr_b16 v[202:203], v158 offset:256
	s_waitcnt lgkmcnt(0)
	s_waitcnt lgkmcnt(14)
	ds_write_b128 v159, v[172:175]
	s_waitcnt lgkmcnt(13)
	ds_write_b128 v160, v[176:179]
	s_waitcnt lgkmcnt(12)
	ds_write_b128 v161, v[180:183]
	s_waitcnt lgkmcnt(11)
	ds_write_b128 v162, v[184:187]
	s_waitcnt lgkmcnt(10)
	ds_write_b128 v163, v[188:191]
	s_waitcnt lgkmcnt(9)
	ds_write_b128 v164, v[192:195]
	s_waitcnt lgkmcnt(8)
	ds_write_b128 v165, v[196:199]
	s_waitcnt lgkmcnt(7)
	ds_write_b128 v166, v[200:203]
	s_waitcnt lgkmcnt(0)
	v_add_u32_e32 v145, v147, v148
	ds_read_b128 v[172:175], v145
	v_add_u32_e32 v171, v147, v149
	ds_read_b128 v[176:179], v171
	v_lshl_add_u64 v[186:187], s[0:1], 0, v[134:135]
	s_andn2_b64 vcc, exec, s[20:21]
	s_waitcnt lgkmcnt(1)
	v_lshlrev_b32_e32 v130, 16, v172
	v_and_b32_e32 v172, 0xffff0000, v172
	v_mul_f32_e32 v130, 0x42800000, v130
	v_mul_f32_e32 v180, 0x42800000, v172
	v_mov_b32_e32 v172, 0
	v_cvt_pk_fp8_f32 v172, v130, v180
	v_lshlrev_b32_e32 v181, 16, v173
	v_and_b32_e32 v173, 0xffff0000, v173
	v_mul_f32_e32 v130, 0x42800000, v181
	v_mul_f32_e32 v173, 0x42800000, v173
	v_cvt_pk_fp8_f32 v172, v130, v173 op_sel:[0,0,1]
	v_lshlrev_b32_e32 v130, 16, v174
	v_and_b32_e32 v173, 0xffff0000, v174
	v_mul_f32_e32 v130, 0x42800000, v130
	v_mul_f32_e32 v174, 0x42800000, v173
	v_mov_b32_e32 v173, 0
	v_cvt_pk_fp8_f32 v173, v130, v174
	v_lshlrev_b32_e32 v180, 16, v175
	v_and_b32_e32 v174, 0xffff0000, v175
	v_mul_f32_e32 v130, 0x42800000, v180
	v_mul_f32_e32 v174, 0x42800000, v174
	v_cvt_pk_fp8_f32 v173, v130, v174 op_sel:[0,0,1]
	s_waitcnt lgkmcnt(0)
	v_lshlrev_b32_e32 v130, 16, v176
	v_and_b32_e32 v174, 0xffff0000, v176
	v_mul_f32_e32 v130, 0x42800000, v130
	v_mul_f32_e32 v175, 0x42800000, v174
	v_mov_b32_e32 v174, 0
	v_cvt_pk_fp8_f32 v174, v130, v175
	v_lshlrev_b32_e32 v176, 16, v177
	v_and_b32_e32 v175, 0xffff0000, v177
	v_mul_f32_e32 v130, 0x42800000, v176
	v_mul_f32_e32 v175, 0x42800000, v175
	v_cvt_pk_fp8_f32 v174, v130, v175 op_sel:[0,0,1]
	v_lshlrev_b32_e32 v130, 16, v178
	v_and_b32_e32 v175, 0xffff0000, v178
	v_mul_f32_e32 v130, 0x42800000, v130
	v_mul_f32_e32 v176, 0x42800000, v175
	v_mov_b32_e32 v175, 0
	v_cvt_pk_fp8_f32 v175, v130, v176
	v_lshlrev_b32_e32 v177, 16, v179
	v_and_b32_e32 v176, 0xffff0000, v179
	v_mul_f32_e32 v130, 0x42800000, v177
	v_mul_f32_e32 v176, 0x42800000, v176
	v_cvt_pk_fp8_f32 v175, v130, v176 op_sel:[0,0,1]
	ds_read_b128 v[176:179], v167
	v_lshl_add_u64 v[180:181], v[186:187], 0, v[136:137]
	s_add_i32 s33, s56, 2
	global_store_dwordx4 v[180:181], v[172:175], off
	ds_read_b128 v[172:175], v168
	s_waitcnt lgkmcnt(1)
	v_lshlrev_b32_e32 v130, 16, v176
	v_and_b32_e32 v176, 0xffff0000, v176
	v_mul_f32_e32 v130, 0x42800000, v130
	v_mul_f32_e32 v180, 0x42800000, v176
	v_mov_b32_e32 v176, 0
	v_cvt_pk_fp8_f32 v176, v130, v180
	v_lshlrev_b32_e32 v181, 16, v177
	v_and_b32_e32 v177, 0xffff0000, v177
	v_mul_f32_e32 v130, 0x42800000, v181
	v_mul_f32_e32 v177, 0x42800000, v177
	v_cvt_pk_fp8_f32 v176, v130, v177 op_sel:[0,0,1]
	v_lshlrev_b32_e32 v130, 16, v178
	v_and_b32_e32 v177, 0xffff0000, v178
	v_mul_f32_e32 v130, 0x42800000, v130
	v_mul_f32_e32 v178, 0x42800000, v177
	v_mov_b32_e32 v177, 0
	v_cvt_pk_fp8_f32 v177, v130, v178
	v_lshlrev_b32_e32 v180, 16, v179
	v_and_b32_e32 v178, 0xffff0000, v179
	v_mul_f32_e32 v130, 0x42800000, v180
	v_mul_f32_e32 v178, 0x42800000, v178
	v_cvt_pk_fp8_f32 v177, v130, v178 op_sel:[0,0,1]
	s_waitcnt lgkmcnt(0)
; #define GAS __attribute__((address_space(1)))
; #define LAS __attribute__((address_space(3)))
; __device__ __forceinline__ unsigned pk4_fp8(float a, float b, float c, float d) { int p = 0; p = __builtin_amdgcn_cvt_pk_fp8_f32(a, b, p, false); p = __builtin_amdgcn_cvt_pk_fp8_f32(c, d, p, true); return (unsigned)p; }
; __device__ __forceinline__ void t64_finish(const f32x4 (&tv)[16], unsigned char* dst, int ldd, int f8, LAS unsigned char* scr, int lane) {
;     ...
;     const int rr = lane >> 3, cc = lane & 7;
; #pragma unroll
;     for (int it = 0; it < 4; ++it) { const int n = 8 * it + rr;
;         const v4u v0 = *(const LAS v4u*)(scr + n * 256 + 16 * ((2 * cc) ^ (n & 15))), v1 = *(const LAS v4u*)(scr + n * 256 + 16 * ((2 * cc + 1) ^ (n & 15)));
;         if (f8) { v4u o4; o4.x = pk4_fp8(bf_lo(v0.x) * W8_SCALE, bf_hi(v0.x) * W8_SCALE, bf_lo(v0.y) * W8_SCALE, bf_hi(v0.y) * W8_SCALE);
;             o4.y = pk4_fp8(bf_lo(v0.z) * W8_SCALE, bf_hi(v0.z) * W8_SCALE, bf_lo(v0.w) * W8_SCALE, bf_hi(v0.w) * W8_SCALE);
;             o4.z = pk4_fp8(bf_lo(v1.x) * W8_SCALE, bf_hi(v1.x) * W8_SCALE, bf_lo(v1.y) * W8_SCALE, bf_hi(v1.y) * W8_SCALE);
;             o4.w = pk4_fp8(bf_lo(v1.z) * W8_SCALE, bf_hi(v1.z) * W8_SCALE, bf_lo(v1.w) * W8_SCALE, bf_hi(v1.w) * W8_SCALE);
;             __builtin_nontemporal_store(o4, (GAS v4u*)(dst + (size_t)n * ldd + 16 * cc)); }
;         else { *(GAS v4u*)(dst + (size_t)n * ldd + 32 * cc) = v0; *(GAS v4u*)(dst + (size_t)n * ldd + 32 * cc + 16) = v1; } }
	v_lshlrev_b32_e32 v130, 16, v172
	v_and_b32_e32 v172, 0xffff0000, v172
	v_mul_f32_e32 v130, 0x42800000, v130
	v_mul_f32_e32 v172, 0x42800000, v172
	v_mov_b32_e32 v178, 0
	v_cvt_pk_fp8_f32 v178, v130, v172
	v_lshlrev_b32_e32 v179, 16, v173
	v_and_b32_e32 v172, 0xffff0000, v173
	v_mul_f32_e32 v130, 0x42800000, v179
	v_mul_f32_e32 v172, 0x42800000, v172
	v_cvt_pk_fp8_f32 v178, v130, v172 op_sel:[0,0,1]
	v_lshlrev_b32_e32 v130, 16, v174
	v_and_b32_e32 v172, 0xffff0000, v174
	v_mul_f32_e32 v130, 0x42800000, v130
	v_mul_f32_e32 v172, 0x42800000, v172
	v_mov_b32_e32 v179, 0
	v_cvt_pk_fp8_f32 v179, v130, v172
	v_lshlrev_b32_e32 v173, 16, v175
	v_and_b32_e32 v172, 0xffff0000, v175
	v_mul_f32_e32 v130, 0x42800000, v173
	v_mul_f32_e32 v172, 0x42800000, v172
	v_cvt_pk_fp8_f32 v179, v130, v172 op_sel:[0,0,1]
	v_add_u32_e32 v172, v150, v148
	ds_read_b128 v[180:183], v172
	v_lshl_add_u64 v[174:175], v[186:187], 0, v[138:139]
	v_add_u32_e32 v173, v150, v149
	global_store_dwordx4 v[174:175], v[176:179], off
	ds_read_b128 v[174:177], v173
	s_waitcnt lgkmcnt(1)
	v_lshlrev_b32_e32 v130, 16, v180
	v_and_b32_e32 v178, 0xffff0000, v180
	v_mul_f32_e32 v130, 0x42800000, v130
	v_mul_f32_e32 v179, 0x42800000, v178
	v_mov_b32_e32 v178, 0
	v_cvt_pk_fp8_f32 v178, v130, v179
	v_lshlrev_b32_e32 v180, 16, v181
	v_and_b32_e32 v179, 0xffff0000, v181
	v_mul_f32_e32 v130, 0x42800000, v180
	v_mul_f32_e32 v179, 0x42800000, v179
	v_cvt_pk_fp8_f32 v178, v130, v179 op_sel:[0,0,1]
	v_lshlrev_b32_e32 v130, 16, v182
	v_and_b32_e32 v179, 0xffff0000, v182
	v_mul_f32_e32 v130, 0x42800000, v130
	v_mul_f32_e32 v180, 0x42800000, v179
	v_mov_b32_e32 v179, 0
	v_cvt_pk_fp8_f32 v179, v130, v180
	v_lshlrev_b32_e32 v181, 16, v183
	v_and_b32_e32 v180, 0xffff0000, v183
	v_mul_f32_e32 v130, 0x42800000, v181
	v_mul_f32_e32 v180, 0x42800000, v180
	v_cvt_pk_fp8_f32 v179, v130, v180 op_sel:[0,0,1]
	s_waitcnt lgkmcnt(0)
	v_lshlrev_b32_e32 v130, 16, v174
	v_and_b32_e32 v174, 0xffff0000, v174
	v_mul_f32_e32 v130, 0x42800000, v130
	v_mul_f32_e32 v174, 0x42800000, v174
	v_mov_b32_e32 v180, 0
	v_cvt_pk_fp8_f32 v180, v130, v174
	v_lshlrev_b32_e32 v181, 16, v175
	v_and_b32_e32 v174, 0xffff0000, v175
	v_mul_f32_e32 v130, 0x42800000, v181
	v_mul_f32_e32 v174, 0x42800000, v174
	v_cvt_pk_fp8_f32 v180, v130, v174 op_sel:[0,0,1]
	v_lshlrev_b32_e32 v130, 16, v176
	v_and_b32_e32 v174, 0xffff0000, v176
	v_mul_f32_e32 v130, 0x42800000, v130
	v_mul_f32_e32 v174, 0x42800000, v174
	v_mov_b32_e32 v181, 0
	ds_read_b128 v[182:185], v169
	v_cvt_pk_fp8_f32 v181, v130, v174
	v_lshlrev_b32_e32 v175, 16, v177
	v_and_b32_e32 v130, 0xffff0000, v177
	v_mul_f32_e32 v175, 0x42800000, v175
	v_mul_f32_e32 v130, 0x42800000, v130
	v_cvt_pk_fp8_f32 v181, v175, v130 op_sel:[0,0,1]
	ds_read_b128 v[174:177], v170
	s_waitcnt lgkmcnt(1)
	v_lshlrev_b32_e32 v130, 16, v182
	v_and_b32_e32 v182, 0xffff0000, v182
	v_mul_f32_e32 v130, 0x42800000, v130
	v_mul_f32_e32 v188, 0x42800000, v182
	v_mov_b32_e32 v182, 0
	v_cvt_pk_fp8_f32 v182, v130, v188
	v_lshlrev_b32_e32 v189, 16, v183
	v_and_b32_e32 v183, 0xffff0000, v183
	v_mul_f32_e32 v130, 0x42800000, v189
	v_mul_f32_e32 v183, 0x42800000, v183
	v_cvt_pk_fp8_f32 v182, v130, v183 op_sel:[0,0,1]
	v_lshlrev_b32_e32 v130, 16, v184
	v_and_b32_e32 v183, 0xffff0000, v184
	v_mul_f32_e32 v130, 0x42800000, v130
	v_mul_f32_e32 v184, 0x42800000, v183
	v_mov_b32_e32 v183, 0
	v_cvt_pk_fp8_f32 v183, v130, v184
	v_lshlrev_b32_e32 v188, 16, v185
	v_and_b32_e32 v184, 0xffff0000, v185
	v_mul_f32_e32 v130, 0x42800000, v188
	v_mul_f32_e32 v184, 0x42800000, v184
	v_cvt_pk_fp8_f32 v183, v130, v184 op_sel:[0,0,1]
	s_waitcnt lgkmcnt(0)
	v_lshlrev_b32_e32 v130, 16, v174
	v_and_b32_e32 v174, 0xffff0000, v174
	v_mul_f32_e32 v130, 0x42800000, v130
	v_mul_f32_e32 v174, 0x42800000, v174
	v_mov_b32_e32 v184, 0
	v_cvt_pk_fp8_f32 v184, v130, v174
	v_lshlrev_b32_e32 v185, 16, v175
	v_and_b32_e32 v174, 0xffff0000, v175
	v_mul_f32_e32 v130, 0x42800000, v185
	v_mul_f32_e32 v174, 0x42800000, v174
	v_cvt_pk_fp8_f32 v184, v130, v174 op_sel:[0,0,1]
	v_lshlrev_b32_e32 v130, 16, v176
	v_and_b32_e32 v174, 0xffff0000, v176
	v_mul_f32_e32 v130, 0x42800000, v130
	v_mul_f32_e32 v174, 0x42800000, v174
	v_mov_b32_e32 v185, 0
	v_cvt_pk_fp8_f32 v185, v130, v174
	v_lshlrev_b32_e32 v175, 16, v177
	v_and_b32_e32 v174, 0xffff0000, v177
	v_mul_f32_e32 v130, 0x42800000, v175
	v_mul_f32_e32 v174, 0x42800000, v174
	v_cvt_pk_fp8_f32 v185, v130, v174 op_sel:[0,0,1]
	v_lshl_add_u64 v[174:175], v[186:187], 0, v[140:141]
	global_store_dwordx4 v[174:175], v[178:181], off
	v_lshl_add_u64 v[174:175], v[186:187], 0, v[142:143]
	global_store_dwordx4 v[174:175], v[182:185], off
	s_waitcnt lgkmcnt(0)
	s_cbranch_vccnz .LBB0_144
; #define LAS __attribute__((address_space(3)))
; __device__ __forceinline__ XItem xitem(const float* w_gate, const float* w_up, const float* w_down, bf16* BTGU, bf16* BTD, int r) {
;     XItem it;
;     if (r < CV_GU) { const int per = (DM / 128) * (DFF / 32); const int e = r / (2 * per), r2 = r % (2 * per), which = r2 / per, r3 = r2 % per; const int nblk = DFF / 32, kb = r3 / nblk, nb = r3 % nblk;
;         const float* W = (which ? w_up : w_gate) + (size_t)e * DM * DFF;
;         const int f0 = 32 * nb, brow = 256 * (f0 >> 7) + 128 * which + (f0 & 127);
;         it.src = W + (size_t)(128 * kb) * DFF + f0; it.ldw = DFF; it.dst = (unsigned char*)BTGU + ((size_t)e * 2048 + brow) * DM + 128 * kb; it.ldd = DM; it.f8 = 1; return it; }
;     r -= CV_GU;
;     { const int per = (DFF / 128) * (DM / 32); const int e = r / per, r3 = r % per; const int nblk = DM / 32, kb = r3 / nblk, nb = r3 % nblk;
;         it.src = w_down + (size_t)e * DFF * DM + (size_t)(128 * kb) * DM + 32 * nb; it.ldw = DM; it.dst = (unsigned char*)BTD + ((size_t)e * DM + 32 * nb) * DFF + 128 * kb; it.ldd = DFF; it.f8 = 1; return it; }
; }
; __device__ __forceinline__ void convert_range(const float* w_gate, const float* w_up, const float* w_down, bf16* BTGU, bf16* BTD, int x0, int x1, LAS unsigned char* scr, int lane) {
;     if (x0 >= x1) return;
;     f32x4 ta[16], tc[16];
;     XItem A = xitem(w_gate, w_up, w_down, BTGU, BTD, x0), B = A;
;     t64_load(A.src, A.ldw, lane, ta);
; #pragma unroll 1
;     for (int x = x0; x < x1; x += 2) {
;         const bool hasB = x + 1 < x1;
;         if (hasB) { B = xitem(w_gate, w_up, w_down, BTGU, BTD, x + 1); t64_load(B.src, B.ldw, lane, tc); }
;         t64_finish(ta, A.dst, A.ldd, A.f8, scr, lane);
;         if (hasB) {
;             if (x + 2 < x1) { A = xitem(w_gate, w_up, w_down, BTGU, BTD, x + 2); t64_load(A.src, A.ldw, lane, ta); }
;             t64_finish(tc, B.dst, B.ldd, B.f8, scr, lane);
	s_cmp_ge_i32 s33, s52
	s_cbranch_scc1 .LcvwP1_b
	s_ashr_i32 s0, s33, 31
	s_lshr_b32 s0, s0, 22
	s_add_i32 s1, s33, s0
	s_ashr_i32 s0, s1, 10
	s_and_b32 s1, s1, 0xfffffc00
	s_sub_i32 s1, s56, s1
	s_add_i32 s20, s1, 2
	s_sext_i32_i16 s21, s20
	s_bfe_u32 s21, s21, 0x90016
	s_add_i32 s21, s20, s21
	s_sext_i32_i16 s22, s21
	s_and_b32 s21, s21, 0xfe00
	s_sub_i32 s20, s20, s21
	s_sext_i32_i16 s21, s20
	s_bfe_u32 s21, s21, 0x5001a
	s_add_i32 s21, s20, s21
	s_sext_i32_i16 s23, s21
	s_and_b32 s21, s21, 0xffe0
	s_ashr_i32 s22, s22, 9
	s_sub_i32 s20, s20, s21
	s_addk_i32 s1, 0x201
	s_cmpk_lt_u32 s1, 0x3ff
	s_cselect_b32 s40, s29, s31
	s_cselect_b32 s54, s28, s30
	s_ashr_i32 s1, s0, 31
	s_sext_i32_i16 s41, s20
	s_lshl_b64 s[20:21], s[0:1], 23
	s_add_u32 s54, s54, s20
	s_addc_u32 s55, s40, s21
	s_lshl_b32 s20, s41, 6
	s_lshl_b32 s40, s41, 5
	s_and_b32 s20, s20, 0xffffff00
	s_lshl_b32 s21, s22, 7
	s_add_i32 s20, s20, s21
	s_and_b32 s21, s40, 0x60
	s_or_b32 s22, s20, s21
	s_lshl_b32 s20, s23, 2
	s_and_b32 s20, s20, 0xffffff80
	s_ashr_i32 s21, s20, 31
	s_lshl_b64 s[56:57], s[20:21], 12
	s_add_u32 s23, s54, s56
	s_addc_u32 s54, s55, s57
	s_ashr_i32 s41, s40, 31
	s_lshl_b64 s[40:41], s[40:41], 2
	s_add_u32 s40, s23, s40
	s_addc_u32 s41, s54, s41
	v_lshl_add_u64 v[0:1], s[40:41], 0, v[132:133]
	v_lshlrev_b32_e32 v130, 2, v128
	v_lshl_add_u64 v[56:57], v[0:1], 0, v[130:131]
	v_add_co_u32_e32 v4, vcc, 0x8000, v56
	s_ashr_i32 s23, s22, 31
	s_nop 0
	v_addc_co_u32_e32 v5, vcc, 0, v57, vcc
	v_add_co_u32_e32 v8, vcc, 0x10000, v56
	global_load_dwordx4 v[0:3], v[56:57], off nt
	s_nop 0
	global_load_dwordx4 v[4:7], v[4:5], off nt
	v_addc_co_u32_e32 v9, vcc, 0, v57, vcc
	v_add_co_u32_e32 v10, vcc, 0x18000, v56
	s_lshl_b64 s[0:1], s[0:1], 22
	s_nop 0
	v_addc_co_u32_e32 v11, vcc, 0, v57, vcc
	v_add_co_u32_e32 v12, vcc, 0x20000, v56
	global_load_dwordx4 v[32:35], v[8:9], off nt
	s_nop 0
	global_load_dwordx4 v[8:11], v[10:11], off nt
	v_addc_co_u32_e32 v13, vcc, 0, v57, vcc
	v_add_co_u32_e32 v14, vcc, 0x28000, v56
	s_lshl_b64 s[22:23], s[22:23], 11
	s_nop 0
	v_addc_co_u32_e32 v15, vcc, 0, v57, vcc
	v_add_co_u32_e32 v16, vcc, 0x30000, v56
	global_load_dwordx4 v[36:39], v[12:13], off nt
	s_nop 0
	global_load_dwordx4 v[12:15], v[14:15], off nt
	v_addc_co_u32_e32 v17, vcc, 0, v57, vcc
	v_add_co_u32_e32 v18, vcc, 0x38000, v56
	s_add_u32 s0, s35, s0
	s_nop 0
	v_addc_co_u32_e32 v19, vcc, 0, v57, vcc
	v_add_co_u32_e32 v20, vcc, 0x40000, v56
	global_load_dwordx4 v[40:43], v[16:17], off nt
	s_nop 0
	global_load_dwordx4 v[16:19], v[18:19], off nt
	v_addc_co_u32_e32 v21, vcc, 0, v57, vcc
	v_add_co_u32_e32 v22, vcc, 0x48000, v56
	s_addc_u32 s1, s53, s1
	s_nop 0
	v_addc_co_u32_e32 v23, vcc, 0, v57, vcc
	v_add_co_u32_e32 v24, vcc, 0x50000, v56
	global_load_dwordx4 v[44:47], v[20:21], off nt
	s_nop 0
	global_load_dwordx4 v[20:23], v[22:23], off nt
	v_addc_co_u32_e32 v25, vcc, 0, v57, vcc
	v_add_co_u32_e32 v26, vcc, 0x58000, v56
	s_add_u32 s0, s0, s22
	s_nop 0
	v_addc_co_u32_e32 v27, vcc, 0, v57, vcc
	v_add_co_u32_e32 v28, vcc, 0x60000, v56
	global_load_dwordx4 v[48:51], v[24:25], off nt
	s_nop 0
	global_load_dwordx4 v[24:27], v[26:27], off nt
	v_addc_co_u32_e32 v29, vcc, 0, v57, vcc
	v_add_co_u32_e32 v30, vcc, 0x68000, v56
	s_addc_u32 s1, s1, s23
	s_nop 0
	v_addc_co_u32_e32 v31, vcc, 0, v57, vcc
	v_add_co_u32_e32 v58, vcc, 0x70000, v56
	global_load_dwordx4 v[52:55], v[28:29], off nt
	s_nop 0
	global_load_dwordx4 v[28:31], v[30:31], off nt
	v_addc_co_u32_e32 v59, vcc, 0, v57, vcc
	v_add_co_u32_e32 v60, vcc, 0x78000, v56
	s_add_u32 s0, s0, s20
	s_nop 0
	v_addc_co_u32_e32 v61, vcc, 0, v57, vcc
	global_load_dwordx4 v[56:59], v[58:59], off nt
	s_nop 0
	global_load_dwordx4 v[60:63], v[60:61], off nt
	s_addc_u32 s1, s1, s21
	s_waitcnt vmcnt(16)
	s_branch .LBB0_143

; #define LAS __attribute__((address_space(3)))
; __device__ __forceinline__ unsigned cvt_pk_bf16(float lo, float hi) { unsigned r; asm volatile("v_cvt_pk_bf16_f32 %0, %1, %2" : "=v"(r) : "v"(lo), "v"(hi)); return r; }
; __device__ __forceinline__ void t64_load(const float* Wsrc, int ldw, int lane, f32x4 (&tv)[16]) {
;     const float* p = Wsrc + (size_t)(lane >> 3) * ldw + 4 * (lane & 7);
; #pragma unroll
;     for (int i = 0; i < 16; ++i) { tv[i] = __builtin_nontemporal_load((const f32x4*)p); p += 8 * ldw; }
; }
; __device__ __forceinline__ void t64_finish(const f32x4 (&tv)[16], unsigned char* dst, int ldd, int f8, LAS unsigned char* scr, int lane) {
;     const int g = lane >> 4, i16 = lane & 15;
; #pragma unroll
;     for (int i = 0; i < 16; ++i) { v2u w; w.x = cvt_pk_bf16(tv[i].x, tv[i].y); w.y = cvt_pk_bf16(tv[i].z, tv[i].w); *(LAS v2u*)(scr + (8 * i + (lane >> 3)) * 64 + 8 * (lane & 7)) = w; }
; __device__ __forceinline__ void convert_range(const float* w_gate, const float* w_up, const float* w_down, bf16* BTGU, bf16* BTD, int x0, int x1, LAS unsigned char* scr, int lane) {
;     ...
; #pragma unroll 1
;     for (int x = x0; x < x1; x += 2) {
;         const bool hasB = x + 1 < x1;
;         if (hasB) { B = xitem(w_gate, w_up, w_down, BTGU, BTD, x + 1); t64_load(B.src, B.ldw, lane, tc); }
;         t64_finish(ta, A.dst, A.ldd, A.f8, scr, lane);
.LBB0_244:
	v_mul_u32_u24_e32 v2, s0, v158
	v_lshlrev_b32_e32 v170, 2, v2
	v_lshl_add_u64 v[2:3], s[44:45], 0, v[170:171]
	v_mov_b32_e32 v131, v171
	v_lshl_add_u64 v[2:3], v[2:3], 0, v[130:131]
	s_lshl_b32 s0, s0, 5
	v_lshl_add_u64 v[10:11], v[2:3], 0, s[0:1]
	global_load_dwordx4 v[2:5], v[2:3], off nt
	s_nop 0
	global_load_dwordx4 v[6:9], v[10:11], off nt
	v_lshl_add_u64 v[10:11], v[10:11], 0, s[0:1]
	v_lshl_add_u64 v[18:19], v[10:11], 0, s[0:1]
	global_load_dwordx4 v[10:13], v[10:11], off nt
	s_nop 0
	global_load_dwordx4 v[14:17], v[18:19], off nt
	v_lshl_add_u64 v[18:19], v[18:19], 0, s[0:1]
	v_lshl_add_u64 v[26:27], v[18:19], 0, s[0:1]
	global_load_dwordx4 v[18:21], v[18:19], off nt
	s_nop 0
	global_load_dwordx4 v[22:25], v[26:27], off nt
	v_lshl_add_u64 v[26:27], v[26:27], 0, s[0:1]
	v_lshl_add_u64 v[34:35], v[26:27], 0, s[0:1]
	v_lshl_add_u64 v[38:39], v[34:35], 0, s[0:1]
	v_lshl_add_u64 v[42:43], v[38:39], 0, s[0:1]
	v_lshl_add_u64 v[46:47], v[42:43], 0, s[0:1]
	v_lshl_add_u64 v[54:55], v[46:47], 0, s[0:1]
	v_lshl_add_u64 v[58:59], v[54:55], 0, s[0:1]
	v_lshl_add_u64 v[66:67], v[58:59], 0, s[0:1]
	v_lshl_add_u64 v[70:71], v[66:67], 0, s[0:1]
	global_load_dwordx4 v[26:29], v[26:27], off nt
	s_nop 0
	global_load_dwordx4 v[30:33], v[34:35], off nt
	s_nop 0
	global_load_dwordx4 v[34:37], v[38:39], off nt
	s_nop 0
	global_load_dwordx4 v[38:41], v[42:43], off nt
	s_nop 0
	global_load_dwordx4 v[42:45], v[46:47], off nt
	s_nop 0
	global_load_dwordx4 v[46:49], v[54:55], off nt
	s_nop 0
	global_load_dwordx4 v[54:57], v[58:59], off nt
	s_nop 0
	global_load_dwordx4 v[58:61], v[66:67], off nt
	s_nop 0
	global_load_dwordx4 v[66:69], v[70:71], off nt
	v_lshl_add_u64 v[70:71], v[70:71], 0, s[0:1]
	global_load_dwordx4 v[70:73], v[70:71], off nt
	s_waitcnt vmcnt(16)
	s_branch .LBB0_245
.LcvwP2a_b:
	s_waitcnt vmcnt(0)
.LBB0_245:
	v_cvt_pk_bf16_f32 v132, v50, v51
	v_cvt_pk_bf16_f32 v133, v52, v53
	ds_write_b64 v1, v[132:133]
	v_cvt_pk_bf16_f32 v132, v62, v63
	v_cvt_pk_bf16_f32 v133, v64, v65
	ds_write_b64 v1, v[132:133] offset:512
	v_cvt_pk_bf16_f32 v132, v74, v75
	v_cvt_pk_bf16_f32 v133, v76, v77
	ds_write_b64 v1, v[132:133] offset:1024
	v_cvt_pk_bf16_f32 v132, v78, v79
	v_cvt_pk_bf16_f32 v133, v80, v81
	ds_write_b64 v1, v[132:133] offset:1536
	v_cvt_pk_bf16_f32 v132, v82, v83
	v_cvt_pk_bf16_f32 v133, v84, v85
	ds_write_b64 v1, v[132:133] offset:2048
	v_cvt_pk_bf16_f32 v132, v86, v87
	v_cvt_pk_bf16_f32 v133, v88, v89
	ds_write_b64 v1, v[132:133] offset:2560
	v_cvt_pk_bf16_f32 v132, v90, v91
	v_cvt_pk_bf16_f32 v133, v92, v93
	ds_write_b64 v1, v[132:133] offset:3072
	v_cvt_pk_bf16_f32 v132, v94, v95
	v_cvt_pk_bf16_f32 v133, v96, v97
	ds_write_b64 v1, v[132:133] offset:3584
	v_cvt_pk_bf16_f32 v132, v98, v99
	v_cvt_pk_bf16_f32 v133, v100, v101
	ds_write_b64 v1, v[132:133] offset:4096
	v_cvt_pk_bf16_f32 v132, v102, v103
	v_cvt_pk_bf16_f32 v133, v104, v105
	ds_write_b64 v1, v[132:133] offset:4608
	v_cvt_pk_bf16_f32 v132, v106, v107
	v_cvt_pk_bf16_f32 v133, v108, v109
	ds_write_b64 v1, v[132:133] offset:5120
	v_cvt_pk_bf16_f32 v132, v110, v111
	v_cvt_pk_bf16_f32 v133, v112, v113
	ds_write_b64 v1, v[132:133] offset:5632
	v_cvt_pk_bf16_f32 v132, v114, v115
	v_cvt_pk_bf16_f32 v133, v116, v117
	ds_write_b64 v1, v[132:133] offset:6144
	v_cvt_pk_bf16_f32 v132, v118, v119
	v_cvt_pk_bf16_f32 v133, v120, v121
	ds_write_b64 v1, v[132:133] offset:6656
	v_cvt_pk_bf16_f32 v132, v122, v123
	v_cvt_pk_bf16_f32 v133, v124, v125
	ds_write_b64 v1, v[132:133] offset:7168
	v_cvt_pk_bf16_f32 v132, v126, v127
	v_cvt_pk_bf16_f32 v133, v128, v129
	ds_write_b64 v1, v[132:133] offset:7680
	s_waitcnt lgkmcnt(0)
	ds_read_b64_tr_b16 v[152:153], v134
	ds_read_b64_tr_b16 v[154:155], v134 offset:256
	ds_read_b64_tr_b16 v[172:173], v134 offset:1024
	ds_read_b64_tr_b16 v[174:175], v134 offset:1280
	ds_read_b64_tr_b16 v[176:177], v134 offset:2048
	ds_read_b64_tr_b16 v[178:179], v134 offset:2304
	ds_read_b64_tr_b16 v[180:181], v134 offset:3072
	ds_read_b64_tr_b16 v[182:183], v134 offset:3328
	ds_read_b64_tr_b16 v[184:185], v134 offset:4096
	ds_read_b64_tr_b16 v[186:187], v134 offset:4352
	ds_read_b64_tr_b16 v[188:189], v134 offset:5120
	ds_read_b64_tr_b16 v[190:191], v134 offset:5376
	ds_read_b64_tr_b16 v[192:193], v134 offset:6144
	ds_read_b64_tr_b16 v[194:195], v134 offset:6400
	ds_read_b64_tr_b16 v[224:225], v134 offset:7168
	ds_read_b64_tr_b16 v[226:227], v134 offset:7424
	s_waitcnt lgkmcnt(0)
	s_waitcnt lgkmcnt(14)
	ds_write_b128 v135, v[152:155]
	s_waitcnt lgkmcnt(13)
	ds_write_b128 v136, v[172:175]
	s_waitcnt lgkmcnt(12)
	ds_write_b128 v137, v[176:179]
	s_waitcnt lgkmcnt(11)
	ds_write_b128 v138, v[180:183]
	s_waitcnt lgkmcnt(10)
	ds_write_b128 v139, v[184:187]
	s_waitcnt lgkmcnt(9)
	ds_write_b128 v140, v[188:191]
	s_waitcnt lgkmcnt(8)
	ds_write_b128 v141, v[192:195]
	s_waitcnt lgkmcnt(7)
	ds_write_b128 v142, v[224:227]
	s_waitcnt lgkmcnt(0)
	ds_read_b128 v[134:137], v143
	ds_read_b128 v[138:141], v144
	v_lshl_add_u64 v[132:133], s[22:23], 0, v[160:161]
	s_waitcnt lgkmcnt(1)
	v_lshlrev_b32_e32 v1, 16, v134
	v_and_b32_e32 v131, 0xffff0000, v134
	v_mul_f32_e32 v1, 0x42800000, v1
	v_mul_f32_e32 v131, 0x42800000, v131
	v_mov_b32_e32 v134, v171
	v_cvt_pk_fp8_f32 v134, v1, v131
	v_lshlrev_b32_e32 v142, 16, v135
	v_and_b32_e32 v131, 0xffff0000, v135
	v_mul_f32_e32 v1, 0x42800000, v142
	v_mul_f32_e32 v131, 0x42800000, v131
	v_cvt_pk_fp8_f32 v134, v1, v131 op_sel:[0,0,1]
	v_lshlrev_b32_e32 v1, 16, v136
	v_and_b32_e32 v131, 0xffff0000, v136
	v_mul_f32_e32 v1, 0x42800000, v1
	v_mul_f32_e32 v131, 0x42800000, v131
	v_mov_b32_e32 v135, v171
	v_cvt_pk_fp8_f32 v135, v1, v131
	v_lshlrev_b32_e32 v136, 16, v137
	v_and_b32_e32 v131, 0xffff0000, v137
	v_mul_f32_e32 v1, 0x42800000, v136
	v_mul_f32_e32 v131, 0x42800000, v131
	v_cvt_pk_fp8_f32 v135, v1, v131 op_sel:[0,0,1]
	s_waitcnt lgkmcnt(0)
; #define GAS __attribute__((address_space(1)))
; #define LAS __attribute__((address_space(3)))
; __device__ __forceinline__ unsigned pk4_fp8(float a, float b, float c, float d) { int p = 0; p = __builtin_amdgcn_cvt_pk_fp8_f32(a, b, p, false); p = __builtin_amdgcn_cvt_pk_fp8_f32(c, d, p, true); return (unsigned)p; }
; __device__ __forceinline__ void t64_finish(const f32x4 (&tv)[16], unsigned char* dst, int ldd, int f8, LAS unsigned char* scr, int lane) {
;     ...
;     for (int it = 0; it < 4; ++it) { const int n = 8 * it + rr;
;         const v4u v0 = *(const LAS v4u*)(scr + n * 256 + 16 * ((2 * cc) ^ (n & 15))), v1 = *(const LAS v4u*)(scr + n * 256 + 16 * ((2 * cc + 1) ^ (n & 15)));
;         if (f8) { v4u o4; o4.x = pk4_fp8(bf_lo(v0.x) * W8_SCALE, bf_hi(v0.x) * W8_SCALE, bf_lo(v0.y) * W8_SCALE, bf_hi(v0.y) * W8_SCALE);
;             o4.y = pk4_fp8(bf_lo(v0.z) * W8_SCALE, bf_hi(v0.z) * W8_SCALE, bf_lo(v0.w) * W8_SCALE, bf_hi(v0.w) * W8_SCALE);
;             o4.z = pk4_fp8(bf_lo(v1.x) * W8_SCALE, bf_hi(v1.x) * W8_SCALE, bf_lo(v1.y) * W8_SCALE, bf_hi(v1.y) * W8_SCALE);
;             o4.w = pk4_fp8(bf_lo(v1.z) * W8_SCALE, bf_hi(v1.z) * W8_SCALE, bf_lo(v1.w) * W8_SCALE, bf_hi(v1.w) * W8_SCALE);
;             __builtin_nontemporal_store(o4, (GAS v4u*)(dst + (size_t)n * ldd + 16 * cc)); }
;         else { *(GAS v4u*)(dst + (size_t)n * ldd + 32 * cc) = v0; *(GAS v4u*)(dst + (size_t)n * ldd + 32 * cc + 16) = v1; } }
	v_lshlrev_b32_e32 v1, 16, v138
	v_and_b32_e32 v131, 0xffff0000, v138
	v_mul_f32_e32 v1, 0x42800000, v1
	v_mul_f32_e32 v131, 0x42800000, v131
	v_mov_b32_e32 v136, v171
	v_cvt_pk_fp8_f32 v136, v1, v131
	v_lshlrev_b32_e32 v137, 16, v139
	v_and_b32_e32 v131, 0xffff0000, v139
	v_mul_f32_e32 v1, 0x42800000, v137
	v_mul_f32_e32 v131, 0x42800000, v131
	v_cvt_pk_fp8_f32 v136, v1, v131 op_sel:[0,0,1]
	v_lshlrev_b32_e32 v1, 16, v140
	v_and_b32_e32 v131, 0xffff0000, v140
	v_mul_f32_e32 v1, 0x42800000, v1
	v_mul_f32_e32 v131, 0x42800000, v131
	v_mov_b32_e32 v137, v171
	v_cvt_pk_fp8_f32 v137, v1, v131
	v_lshlrev_b32_e32 v138, 16, v141
	v_and_b32_e32 v131, 0xffff0000, v141
	v_mul_f32_e32 v1, 0x42800000, v138
	v_mul_f32_e32 v131, 0x42800000, v131
	ds_read_b128 v[138:141], v145
	v_cvt_pk_fp8_f32 v137, v1, v131 op_sel:[0,0,1]
	v_mad_u64_u32 v[142:143], s[44:45], s64, v158, v[132:133]
	global_store_dwordx4 v[142:143], v[134:137], off
	ds_read_b128 v[134:137], v146
	s_waitcnt lgkmcnt(1)
	v_lshlrev_b32_e32 v1, 16, v138
	v_and_b32_e32 v131, 0xffff0000, v138
	v_mul_f32_e32 v1, 0x42800000, v1
	v_mul_f32_e32 v131, 0x42800000, v131
	v_mov_b32_e32 v138, v171
	v_cvt_pk_fp8_f32 v138, v1, v131
	v_lshlrev_b32_e32 v142, 16, v139
	v_and_b32_e32 v131, 0xffff0000, v139
	v_mul_f32_e32 v1, 0x42800000, v142
	v_mul_f32_e32 v131, 0x42800000, v131
	v_cvt_pk_fp8_f32 v138, v1, v131 op_sel:[0,0,1]
	v_lshlrev_b32_e32 v1, 16, v140
	v_and_b32_e32 v131, 0xffff0000, v140
	v_mul_f32_e32 v1, 0x42800000, v1
	v_mul_f32_e32 v131, 0x42800000, v131
	v_mov_b32_e32 v139, v171
	v_cvt_pk_fp8_f32 v139, v1, v131
	v_lshlrev_b32_e32 v140, 16, v141
	v_and_b32_e32 v131, 0xffff0000, v141
	v_mul_f32_e32 v1, 0x42800000, v140
	v_mul_f32_e32 v131, 0x42800000, v131
	v_cvt_pk_fp8_f32 v139, v1, v131 op_sel:[0,0,1]
	s_waitcnt lgkmcnt(0)
	v_lshlrev_b32_e32 v1, 16, v134
	v_and_b32_e32 v131, 0xffff0000, v134
	v_mul_f32_e32 v1, 0x42800000, v1
	v_mul_f32_e32 v131, 0x42800000, v131
	v_mov_b32_e32 v140, v171
	v_cvt_pk_fp8_f32 v140, v1, v131
	v_lshlrev_b32_e32 v134, 16, v135
	v_and_b32_e32 v131, 0xffff0000, v135
	v_mul_f32_e32 v1, 0x42800000, v134
	v_mul_f32_e32 v131, 0x42800000, v131
	v_cvt_pk_fp8_f32 v140, v1, v131 op_sel:[0,0,1]
	v_lshlrev_b32_e32 v1, 16, v136
	v_and_b32_e32 v131, 0xffff0000, v136
	v_mul_f32_e32 v1, 0x42800000, v1
	v_mul_f32_e32 v131, 0x42800000, v131
	v_mov_b32_e32 v141, v171
	v_cvt_pk_fp8_f32 v141, v1, v131
	v_lshlrev_b32_e32 v134, 16, v137
	v_and_b32_e32 v131, 0xffff0000, v137
	v_mul_f32_e32 v1, 0x42800000, v134
	v_mul_f32_e32 v131, 0x42800000, v131
	ds_read_b128 v[134:137], v147
	v_cvt_pk_fp8_f32 v141, v1, v131 op_sel:[0,0,1]
	v_mad_u64_u32 v[142:143], s[44:45], s64, v162, v[132:133]
	global_store_dwordx4 v[142:143], v[138:141], off
	ds_read_b128 v[138:141], v148
	s_waitcnt lgkmcnt(1)
	v_lshlrev_b32_e32 v1, 16, v134
	v_and_b32_e32 v131, 0xffff0000, v134
	v_mul_f32_e32 v1, 0x42800000, v1
	v_mul_f32_e32 v131, 0x42800000, v131
	v_mov_b32_e32 v134, v171
	v_cvt_pk_fp8_f32 v134, v1, v131
	v_lshlrev_b32_e32 v142, 16, v135
	v_and_b32_e32 v131, 0xffff0000, v135
	v_mul_f32_e32 v1, 0x42800000, v142
	v_mul_f32_e32 v131, 0x42800000, v131
	v_cvt_pk_fp8_f32 v134, v1, v131 op_sel:[0,0,1]
	v_lshlrev_b32_e32 v1, 16, v136
	v_and_b32_e32 v131, 0xffff0000, v136
	v_mul_f32_e32 v1, 0x42800000, v1
	v_mul_f32_e32 v131, 0x42800000, v131
	v_mov_b32_e32 v135, v171
	v_cvt_pk_fp8_f32 v135, v1, v131
	v_lshlrev_b32_e32 v136, 16, v137
	v_and_b32_e32 v131, 0xffff0000, v137
	v_mul_f32_e32 v1, 0x42800000, v136
	v_mul_f32_e32 v131, 0x42800000, v131
	v_cvt_pk_fp8_f32 v135, v1, v131 op_sel:[0,0,1]
	s_waitcnt lgkmcnt(0)
	v_lshlrev_b32_e32 v1, 16, v138
	v_and_b32_e32 v131, 0xffff0000, v138
	v_mul_f32_e32 v1, 0x42800000, v1
	v_mul_f32_e32 v131, 0x42800000, v131
	v_mov_b32_e32 v136, v171
	v_cvt_pk_fp8_f32 v136, v1, v131
	v_lshlrev_b32_e32 v137, 16, v139
	v_and_b32_e32 v131, 0xffff0000, v139
	v_mul_f32_e32 v1, 0x42800000, v137
	v_mul_f32_e32 v131, 0x42800000, v131
	v_cvt_pk_fp8_f32 v136, v1, v131 op_sel:[0,0,1]
	v_lshlrev_b32_e32 v1, 16, v140
	v_and_b32_e32 v131, 0xffff0000, v140
	v_lshlrev_b32_e32 v137, 16, v141
	v_mul_f32_e32 v1, 0x42800000, v1
	v_mul_f32_e32 v131, 0x42800000, v131
	v_mul_f32_e32 v142, 0x42800000, v137
	v_mov_b32_e32 v137, v171
	v_cvt_pk_fp8_f32 v137, v1, v131
	v_and_b32_e32 v1, 0xffff0000, v141
	ds_read_b128 v[138:141], v149
	v_mul_f32_e32 v1, 0x42800000, v1
	v_cvt_pk_fp8_f32 v137, v142, v1 op_sel:[0,0,1]
	ds_read_b128 v[142:145], v150
	v_mad_u64_u32 v[146:147], s[44:45], s64, v164, v[132:133]
	s_waitcnt lgkmcnt(1)
	v_lshlrev_b32_e32 v1, 16, v138
	v_and_b32_e32 v131, 0xffff0000, v138
	v_mul_f32_e32 v1, 0x42800000, v1
	v_mul_f32_e32 v131, 0x42800000, v131
	v_mov_b32_e32 v138, v171
	v_cvt_pk_fp8_f32 v138, v1, v131
	v_lshlrev_b32_e32 v148, 16, v139
	v_and_b32_e32 v131, 0xffff0000, v139
	v_mul_f32_e32 v1, 0x42800000, v148
	v_mul_f32_e32 v131, 0x42800000, v131
	v_cvt_pk_fp8_f32 v138, v1, v131 op_sel:[0,0,1]
	v_lshlrev_b32_e32 v1, 16, v140
	v_and_b32_e32 v131, 0xffff0000, v140
	v_mul_f32_e32 v1, 0x42800000, v1
	v_mul_f32_e32 v131, 0x42800000, v131
	v_mov_b32_e32 v139, v171
	v_cvt_pk_fp8_f32 v139, v1, v131
	v_lshlrev_b32_e32 v140, 16, v141
	v_and_b32_e32 v131, 0xffff0000, v141
	v_mul_f32_e32 v1, 0x42800000, v140
	v_mul_f32_e32 v131, 0x42800000, v131
	v_cvt_pk_fp8_f32 v139, v1, v131 op_sel:[0,0,1]
	s_waitcnt lgkmcnt(0)
	v_lshlrev_b32_e32 v1, 16, v142
	v_and_b32_e32 v131, 0xffff0000, v142
	v_mul_f32_e32 v1, 0x42800000, v1
	v_mul_f32_e32 v131, 0x42800000, v131
	v_mov_b32_e32 v140, v171
	v_cvt_pk_fp8_f32 v140, v1, v131
	v_lshlrev_b32_e32 v141, 16, v143
	v_and_b32_e32 v131, 0xffff0000, v143
	v_mul_f32_e32 v1, 0x42800000, v141
	v_mul_f32_e32 v131, 0x42800000, v131
	v_cvt_pk_fp8_f32 v140, v1, v131 op_sel:[0,0,1]
	v_lshlrev_b32_e32 v1, 16, v144
	v_and_b32_e32 v131, 0xffff0000, v144
	v_mul_f32_e32 v1, 0x42800000, v1
	v_mul_f32_e32 v131, 0x42800000, v131
	v_mov_b32_e32 v141, v171
	v_cvt_pk_fp8_f32 v141, v1, v131
	v_lshlrev_b32_e32 v142, 16, v145
	v_and_b32_e32 v131, 0xffff0000, v145
	v_mul_f32_e32 v1, 0x42800000, v142
	v_mul_f32_e32 v131, 0x42800000, v131
	v_cvt_pk_fp8_f32 v141, v1, v131 op_sel:[0,0,1]
	v_mad_u64_u32 v[132:133], s[44:45], s64, v166, v[132:133]
	global_store_dwordx4 v[146:147], v[134:137], off
	global_store_dwordx4 v[132:133], v[138:141], off
	s_waitcnt lgkmcnt(0)

; __device__ __forceinline__ void t64_load(const float* Wsrc, int ldw, int lane, f32x4 (&tv)[16]) {
;     const float* p = Wsrc + (size_t)(lane >> 3) * ldw + 4 * (lane & 7);
; #pragma unroll
;     for (int i = 0; i < 16; ++i) { tv[i] = __builtin_nontemporal_load((const f32x4*)p); p += 8 * ldw; }
; }
; __device__ __forceinline__ void convert_range(const float* w_gate, const float* w_up, const float* w_down, bf16* BTGU, bf16* BTD, int x0, int x1, LAS unsigned char* scr, int lane) {
;     ...
;             if (x + 2 < x1) { A = xitem(w_gate, w_up, w_down, BTGU, BTD, x + 2); t64_load(A.src, A.ldw, lane, ta); }
.LBB0_253:
	v_mul_u32_u24_e32 v1, s0, v158
	v_lshlrev_b32_e32 v170, 2, v1
	v_lshl_add_u64 v[50:51], s[62:63], 0, v[170:171]
	v_mov_b32_e32 v131, v171
	v_lshl_add_u64 v[50:51], v[50:51], 0, v[130:131]
	s_lshl_b32 s0, s0, 5
	v_lshl_add_u64 v[74:75], v[50:51], 0, s[0:1]
	global_load_dwordx4 v[50:53], v[50:51], off nt
	s_nop 0
	global_load_dwordx4 v[62:65], v[74:75], off nt
	v_lshl_add_u64 v[74:75], v[74:75], 0, s[0:1]
	v_lshl_add_u64 v[82:83], v[74:75], 0, s[0:1]
	global_load_dwordx4 v[74:77], v[74:75], off nt
	s_nop 0
	global_load_dwordx4 v[78:81], v[82:83], off nt
	v_lshl_add_u64 v[82:83], v[82:83], 0, s[0:1]
	v_lshl_add_u64 v[90:91], v[82:83], 0, s[0:1]
	global_load_dwordx4 v[82:85], v[82:83], off nt
	s_nop 0
	global_load_dwordx4 v[86:89], v[90:91], off nt
	v_lshl_add_u64 v[90:91], v[90:91], 0, s[0:1]
	v_lshl_add_u64 v[98:99], v[90:91], 0, s[0:1]
	v_lshl_add_u64 v[102:103], v[98:99], 0, s[0:1]
	v_lshl_add_u64 v[106:107], v[102:103], 0, s[0:1]
	v_lshl_add_u64 v[110:111], v[106:107], 0, s[0:1]
	v_lshl_add_u64 v[114:115], v[110:111], 0, s[0:1]
	v_lshl_add_u64 v[118:119], v[114:115], 0, s[0:1]
	v_lshl_add_u64 v[122:123], v[118:119], 0, s[0:1]
	v_lshl_add_u64 v[126:127], v[122:123], 0, s[0:1]
	global_load_dwordx4 v[90:93], v[90:91], off nt
	s_nop 0
	global_load_dwordx4 v[94:97], v[98:99], off nt
	s_nop 0
	global_load_dwordx4 v[98:101], v[102:103], off nt
	s_nop 0
	global_load_dwordx4 v[102:105], v[106:107], off nt
	s_nop 0
	global_load_dwordx4 v[106:109], v[110:111], off nt
	s_nop 0
	global_load_dwordx4 v[110:113], v[114:115], off nt
	s_nop 0
	global_load_dwordx4 v[114:117], v[118:119], off nt
	s_nop 0
	global_load_dwordx4 v[118:121], v[122:123], off nt
	s_nop 0
	global_load_dwordx4 v[122:125], v[126:127], off nt
	v_lshl_add_u64 v[126:127], v[126:127], 0, s[0:1]
	global_load_dwordx4 v[126:129], v[126:127], off nt
	s_waitcnt vmcnt(16)
	s_branch .LcvwP2a_a

; #define LAS __attribute__((address_space(3)))
; #define LDS_WAIT() asm volatile("s_waitcnt lgkmcnt(0)" ::: "memory")
; __device__ __forceinline__ unsigned cvt_pk_bf16(float lo, float hi) { unsigned r; asm volatile("v_cvt_pk_bf16_f32 %0, %1, %2" : "=v"(r) : "v"(lo), "v"(hi)); return r; }
; __device__ __forceinline__ void t64_finish(const f32x4 (&tv)[16], unsigned char* dst, int ldd, int f8, LAS unsigned char* scr, int lane) {
;     const int g = lane >> 4, i16 = lane & 15;
; #pragma unroll
;     for (int i = 0; i < 16; ++i) { v2u w; w.x = cvt_pk_bf16(tv[i].x, tv[i].y); w.y = cvt_pk_bf16(tv[i].z, tv[i].w); *(LAS v2u*)(scr + (8 * i + (lane >> 3)) * 64 + 8 * (lane & 7)) = w; }
;     LDS_WAIT(); asm volatile("" ::: "memory");
;     const int q = i16 >> 2, pp = i16 & 3;
;     bf16x8 o[8];
; #pragma unroll
;     for (int jj = 0; jj < 8; ++jj) { const int c = 4 * jj + g, nb = c & 1, kg = c >> 1;
;         LAS unsigned char* ra = scr + (8 * kg + q) * 64 + 32 * nb + 8 * pp;
;         const s16x4 lo = __builtin_bit_cast(s16x4, __builtin_amdgcn_ds_read_tr16_b64_v4i16((LAS s16x4*)ra));
;         const s16x4 hi = __builtin_bit_cast(s16x4, __builtin_amdgcn_ds_read_tr16_b64_v4i16((LAS s16x4*)(ra + 4 * 64)));
;         o[jj] = __builtin_shufflevector(lo, hi, 0, 1, 2, 3, 4, 5, 6, 7); }
;     LDS_WAIT(); asm volatile("" ::: "memory");
; #pragma unroll
;     for (int jj = 0; jj < 8; ++jj) { const int c = 4 * jj + g, nb = c & 1, kg = c >> 1; const int n = 16 * nb + i16;
;         *(LAS bf16x8*)(scr + n * 256 + 16 * (kg ^ (n & 15))) = o[jj]; }
;     LDS_WAIT(); asm volatile("" ::: "memory");
; __device__ __forceinline__ void convert_range(const float* w_gate, const float* w_up, const float* w_down, bf16* BTGU, bf16* BTD, int x0, int x1, LAS unsigned char* scr, int lane) {
;     ...
;             t64_finish(tc, B.dst, B.ldd, B.f8, scr, lane);
.LcvwP2a_a:
	v_cvt_pk_bf16_f32 v132, v2, v3
	v_cvt_pk_bf16_f32 v133, v4, v5
	v_add_u32_e32 v1, v163, v165
	ds_write_b64 v1, v[132:133]
	v_cvt_pk_bf16_f32 v132, v6, v7
	v_cvt_pk_bf16_f32 v133, v8, v9
	ds_write_b64 v1, v[132:133] offset:512
	v_cvt_pk_bf16_f32 v132, v10, v11
	v_cvt_pk_bf16_f32 v133, v12, v13
	ds_write_b64 v1, v[132:133] offset:1024
	v_cvt_pk_bf16_f32 v132, v14, v15
	v_cvt_pk_bf16_f32 v133, v16, v17
	ds_write_b64 v1, v[132:133] offset:1536
	v_cvt_pk_bf16_f32 v132, v18, v19
	v_cvt_pk_bf16_f32 v133, v20, v21
	ds_write_b64 v1, v[132:133] offset:2048
	v_cvt_pk_bf16_f32 v132, v22, v23
	v_cvt_pk_bf16_f32 v133, v24, v25
	ds_write_b64 v1, v[132:133] offset:2560
	v_cvt_pk_bf16_f32 v132, v26, v27
	v_cvt_pk_bf16_f32 v133, v28, v29
	ds_write_b64 v1, v[132:133] offset:3072
	v_cvt_pk_bf16_f32 v132, v30, v31
	v_cvt_pk_bf16_f32 v133, v32, v33
	ds_write_b64 v1, v[132:133] offset:3584
	v_cvt_pk_bf16_f32 v132, v34, v35
	v_cvt_pk_bf16_f32 v133, v36, v37
	ds_write_b64 v1, v[132:133] offset:4096
	v_cvt_pk_bf16_f32 v132, v38, v39
	v_cvt_pk_bf16_f32 v133, v40, v41
	ds_write_b64 v1, v[132:133] offset:4608
	v_cvt_pk_bf16_f32 v132, v42, v43
	v_cvt_pk_bf16_f32 v133, v44, v45
	ds_write_b64 v1, v[132:133] offset:5120
	v_cvt_pk_bf16_f32 v132, v46, v47
	v_cvt_pk_bf16_f32 v133, v48, v49
	ds_write_b64 v1, v[132:133] offset:5632
	v_cvt_pk_bf16_f32 v132, v54, v55
	v_cvt_pk_bf16_f32 v133, v56, v57
	ds_write_b64 v1, v[132:133] offset:6144
	v_cvt_pk_bf16_f32 v132, v58, v59
	v_cvt_pk_bf16_f32 v133, v60, v61
	ds_write_b64 v1, v[132:133] offset:6656
	v_cvt_pk_bf16_f32 v132, v66, v67
	v_cvt_pk_bf16_f32 v133, v68, v69
	ds_write_b64 v1, v[132:133] offset:7168
	v_cvt_pk_bf16_f32 v132, v70, v71
	v_cvt_pk_bf16_f32 v133, v72, v73
	ds_write_b64 v1, v[132:133] offset:7680
	s_waitcnt lgkmcnt(0)
	v_add_u32_e32 v134, v167, v169
	ds_read_b64_tr_b16 v[136:137], v134
	ds_read_b64_tr_b16 v[138:139], v134 offset:256
	ds_read_b64_tr_b16 v[140:141], v134 offset:1024
	ds_read_b64_tr_b16 v[142:143], v134 offset:1280
	ds_read_b64_tr_b16 v[144:145], v134 offset:2048
	ds_read_b64_tr_b16 v[146:147], v134 offset:2304
	ds_read_b64_tr_b16 v[148:149], v134 offset:3072
	ds_read_b64_tr_b16 v[150:151], v134 offset:3328
	ds_read_b64_tr_b16 v[152:153], v134 offset:4096
	ds_read_b64_tr_b16 v[154:155], v134 offset:4352
	ds_read_b64_tr_b16 v[172:173], v134 offset:5120
	ds_read_b64_tr_b16 v[174:175], v134 offset:5376
	ds_read_b64_tr_b16 v[176:177], v134 offset:6144
	ds_read_b64_tr_b16 v[178:179], v134 offset:6400
	ds_read_b64_tr_b16 v[180:181], v134 offset:7168
	ds_read_b64_tr_b16 v[182:183], v134 offset:7424
	s_waitcnt lgkmcnt(0)
	v_add_u32_e32 v135, v204, v205
	s_waitcnt lgkmcnt(14)
	ds_write_b128 v135, v[136:139]
	v_add_u32_e32 v136, v204, v206
	s_waitcnt lgkmcnt(13)
	ds_write_b128 v136, v[140:143]
	v_add_u32_e32 v137, v204, v207
	v_add_u32_e32 v138, v204, v208
	v_add_u32_e32 v139, v204, v209
	v_add_u32_e32 v140, v204, v210
	v_add_u32_e32 v141, v204, v211
	v_add_u32_e32 v142, v204, v212
	s_waitcnt lgkmcnt(12)
	ds_write_b128 v137, v[144:147]
	s_waitcnt lgkmcnt(11)
	ds_write_b128 v138, v[148:151]
	s_waitcnt lgkmcnt(10)
	ds_write_b128 v139, v[152:155]
	s_waitcnt lgkmcnt(9)
	ds_write_b128 v140, v[172:175]
	s_waitcnt lgkmcnt(8)
	ds_write_b128 v141, v[176:179]
	s_waitcnt lgkmcnt(7)
	ds_write_b128 v142, v[180:183]
	s_waitcnt lgkmcnt(0)
	v_add_u32_e32 v143, v213, v214
	ds_read_b128 v[146:149], v143
	v_add_u32_e32 v144, v213, v215
	ds_read_b128 v[150:153], v144
	v_lshl_add_u64 v[132:133], s[6:7], 0, v[160:161]
	v_mad_u64_u32 v[180:181], s[62:63], s84, v164, v[132:133]
	s_waitcnt lgkmcnt(1)
	v_lshlrev_b32_e32 v131, 16, v146
	v_and_b32_e32 v145, 0xffff0000, v146
	v_mul_f32_e32 v131, 0x42800000, v131
	v_mul_f32_e32 v145, 0x42800000, v145
	v_mov_b32_e32 v146, v171
	v_cvt_pk_fp8_f32 v146, v131, v145
	v_lshlrev_b32_e32 v154, 16, v147
	v_and_b32_e32 v145, 0xffff0000, v147
	v_mul_f32_e32 v131, 0x42800000, v154
	v_mul_f32_e32 v145, 0x42800000, v145
	v_cvt_pk_fp8_f32 v146, v131, v145 op_sel:[0,0,1]
	v_lshlrev_b32_e32 v131, 16, v148
	v_and_b32_e32 v145, 0xffff0000, v148
	v_mul_f32_e32 v131, 0x42800000, v131
	v_mul_f32_e32 v145, 0x42800000, v145
	v_mov_b32_e32 v147, v171
	v_cvt_pk_fp8_f32 v147, v131, v145
	v_lshlrev_b32_e32 v148, 16, v149
	v_and_b32_e32 v145, 0xffff0000, v149
	v_mul_f32_e32 v131, 0x42800000, v148
	v_mul_f32_e32 v145, 0x42800000, v145
	v_cvt_pk_fp8_f32 v147, v131, v145 op_sel:[0,0,1]
	s_waitcnt lgkmcnt(0)
	v_lshlrev_b32_e32 v131, 16, v150
	v_and_b32_e32 v145, 0xffff0000, v150
	v_mul_f32_e32 v131, 0x42800000, v131
	v_mul_f32_e32 v145, 0x42800000, v145
	v_mov_b32_e32 v148, v171
	v_cvt_pk_fp8_f32 v148, v131, v145
	v_lshlrev_b32_e32 v149, 16, v151
	v_and_b32_e32 v145, 0xffff0000, v151
	v_mul_f32_e32 v131, 0x42800000, v149
	v_mul_f32_e32 v145, 0x42800000, v145
	v_cvt_pk_fp8_f32 v148, v131, v145 op_sel:[0,0,1]
	v_lshlrev_b32_e32 v131, 16, v152
	v_and_b32_e32 v145, 0xffff0000, v152
	v_mul_f32_e32 v131, 0x42800000, v131
	v_mul_f32_e32 v145, 0x42800000, v145
	v_mov_b32_e32 v149, v171
	v_cvt_pk_fp8_f32 v149, v131, v145
	v_lshlrev_b32_e32 v150, 16, v153
	v_and_b32_e32 v145, 0xffff0000, v153
	v_mul_f32_e32 v131, 0x42800000, v150
	v_mul_f32_e32 v145, 0x42800000, v145
	v_cvt_pk_fp8_f32 v149, v131, v145 op_sel:[0,0,1]
	v_add_u32_e32 v145, v216, v217
	ds_read_b128 v[150:153], v145
	v_mad_u64_u32 v[154:155], s[62:63], s84, v158, v[132:133]
	global_store_dwordx4 v[154:155], v[146:149], off
	s_andn2_b64 vcc, exec, s[44:45]
	s_nop 0
	v_add_u32_e32 v146, v216, v218
	ds_read_b128 v[172:175], v146
	s_waitcnt lgkmcnt(1)
; #define GAS __attribute__((address_space(1)))
; #define LAS __attribute__((address_space(3)))
; __device__ __forceinline__ unsigned pk4_fp8(float a, float b, float c, float d) { int p = 0; p = __builtin_amdgcn_cvt_pk_fp8_f32(a, b, p, false); p = __builtin_amdgcn_cvt_pk_fp8_f32(c, d, p, true); return (unsigned)p; }
; __device__ __forceinline__ void t64_finish(const f32x4 (&tv)[16], unsigned char* dst, int ldd, int f8, LAS unsigned char* scr, int lane) {
;     ...
;     for (int it = 0; it < 4; ++it) { const int n = 8 * it + rr;
;         const v4u v0 = *(const LAS v4u*)(scr + n * 256 + 16 * ((2 * cc) ^ (n & 15))), v1 = *(const LAS v4u*)(scr + n * 256 + 16 * ((2 * cc + 1) ^ (n & 15)));
;         if (f8) { v4u o4; o4.x = pk4_fp8(bf_lo(v0.x) * W8_SCALE, bf_hi(v0.x) * W8_SCALE, bf_lo(v0.y) * W8_SCALE, bf_hi(v0.y) * W8_SCALE);
;             o4.y = pk4_fp8(bf_lo(v0.z) * W8_SCALE, bf_hi(v0.z) * W8_SCALE, bf_lo(v0.w) * W8_SCALE, bf_hi(v0.w) * W8_SCALE);
;             o4.z = pk4_fp8(bf_lo(v1.x) * W8_SCALE, bf_hi(v1.x) * W8_SCALE, bf_lo(v1.y) * W8_SCALE, bf_hi(v1.y) * W8_SCALE);
;             o4.w = pk4_fp8(bf_lo(v1.z) * W8_SCALE, bf_hi(v1.z) * W8_SCALE, bf_lo(v1.w) * W8_SCALE, bf_hi(v1.w) * W8_SCALE);
;             __builtin_nontemporal_store(o4, (GAS v4u*)(dst + (size_t)n * ldd + 16 * cc)); }
;         else { *(GAS v4u*)(dst + (size_t)n * ldd + 32 * cc) = v0; *(GAS v4u*)(dst + (size_t)n * ldd + 32 * cc + 16) = v1; } }
; __device__ __forceinline__ XItem xitem(const float* w_gate, const float* w_up, const float* w_down, bf16* BTGU, bf16* BTD, int r) {
;     ...
;     { const int per = (DFF / 128) * (DM / 32); const int e = r / per, r3 = r % per; const int nblk = DM / 32, kb = r3 / nblk, nb = r3 % nblk;
;         it.src = w_down + (size_t)e * DFF * DM + (size_t)(128 * kb) * DM + 32 * nb; it.ldw = DM; it.dst = (unsigned char*)BTD + ((size_t)e * DM + 32 * nb) * DFF + 128 * kb; it.ldd = DFF; it.f8 = 1; return it; }
; __device__ __forceinline__ void convert_range(const float* w_gate, const float* w_up, const float* w_down, bf16* BTGU, bf16* BTD, int x0, int x1, LAS unsigned char* scr, int lane) {
;     ...
;         if (hasB) {
;             if (x + 2 < x1) { A = xitem(w_gate, w_up, w_down, BTGU, BTD, x + 2); t64_load(A.src, A.ldw, lane, ta); }
;             t64_finish(tc, B.dst, B.ldd, B.f8, scr, lane);
;         }
;     }
	v_lshlrev_b32_e32 v131, 16, v150
	v_and_b32_e32 v147, 0xffff0000, v150
	v_mul_f32_e32 v131, 0x42800000, v131
	v_mul_f32_e32 v147, 0x42800000, v147
	v_mov_b32_e32 v148, v171
	v_cvt_pk_fp8_f32 v148, v131, v147
	v_lshlrev_b32_e32 v149, 16, v151
	v_and_b32_e32 v147, 0xffff0000, v151
	v_mul_f32_e32 v131, 0x42800000, v149
	v_mul_f32_e32 v147, 0x42800000, v147
	v_cvt_pk_fp8_f32 v148, v131, v147 op_sel:[0,0,1]
	v_lshlrev_b32_e32 v131, 16, v152
	v_and_b32_e32 v147, 0xffff0000, v152
	v_mul_f32_e32 v131, 0x42800000, v131
	v_mul_f32_e32 v147, 0x42800000, v147
	v_mov_b32_e32 v149, v171
	v_cvt_pk_fp8_f32 v149, v131, v147
	v_lshlrev_b32_e32 v150, 16, v153
	v_and_b32_e32 v147, 0xffff0000, v153
	v_mul_f32_e32 v131, 0x42800000, v150
	v_mul_f32_e32 v147, 0x42800000, v147
	v_cvt_pk_fp8_f32 v149, v131, v147 op_sel:[0,0,1]
	s_waitcnt lgkmcnt(0)
	v_lshlrev_b32_e32 v131, 16, v172
	v_and_b32_e32 v147, 0xffff0000, v172
	v_mul_f32_e32 v131, 0x42800000, v131
	v_mul_f32_e32 v147, 0x42800000, v147
	v_mov_b32_e32 v150, v171
	v_cvt_pk_fp8_f32 v150, v131, v147
	v_lshlrev_b32_e32 v151, 16, v173
	v_and_b32_e32 v147, 0xffff0000, v173
	v_mul_f32_e32 v131, 0x42800000, v151
	v_mul_f32_e32 v147, 0x42800000, v147
	v_cvt_pk_fp8_f32 v150, v131, v147 op_sel:[0,0,1]
	v_lshlrev_b32_e32 v131, 16, v174
	v_and_b32_e32 v147, 0xffff0000, v174
	v_mul_f32_e32 v131, 0x42800000, v131
	v_mul_f32_e32 v147, 0x42800000, v147
	v_mov_b32_e32 v151, v171
	v_cvt_pk_fp8_f32 v151, v131, v147
	v_lshlrev_b32_e32 v152, 16, v175
	v_and_b32_e32 v147, 0xffff0000, v175
	v_mul_f32_e32 v131, 0x42800000, v152
	v_mul_f32_e32 v147, 0x42800000, v147
	v_cvt_pk_fp8_f32 v151, v131, v147 op_sel:[0,0,1]
	v_add_u32_e32 v147, v219, v214
	ds_read_b128 v[152:155], v147
	v_mad_u64_u32 v[172:173], s[62:63], s84, v162, v[132:133]
	global_store_dwordx4 v[172:173], v[148:151], off
	v_mad_u64_u32 v[132:133], s[62:63], s84, v166, v[132:133]
	s_nop 0
	v_add_u32_e32 v148, v219, v215
	ds_read_b128 v[172:175], v148
	s_waitcnt lgkmcnt(1)
	v_lshlrev_b32_e32 v131, 16, v152
	v_and_b32_e32 v149, 0xffff0000, v152
	v_mul_f32_e32 v131, 0x42800000, v131
	v_mul_f32_e32 v149, 0x42800000, v149
	v_mov_b32_e32 v152, v171
	v_cvt_pk_fp8_f32 v152, v131, v149
	v_lshlrev_b32_e32 v150, 16, v153
	v_and_b32_e32 v149, 0xffff0000, v153
	v_mul_f32_e32 v131, 0x42800000, v150
	v_mul_f32_e32 v149, 0x42800000, v149
	v_cvt_pk_fp8_f32 v152, v131, v149 op_sel:[0,0,1]
	v_lshlrev_b32_e32 v131, 16, v154
	v_and_b32_e32 v149, 0xffff0000, v154
	v_mul_f32_e32 v131, 0x42800000, v131
	v_mul_f32_e32 v149, 0x42800000, v149
	v_mov_b32_e32 v153, v171
	v_cvt_pk_fp8_f32 v153, v131, v149
	v_lshlrev_b32_e32 v150, 16, v155
	v_and_b32_e32 v149, 0xffff0000, v155
	v_mul_f32_e32 v131, 0x42800000, v150
	v_mul_f32_e32 v149, 0x42800000, v149
	v_cvt_pk_fp8_f32 v153, v131, v149 op_sel:[0,0,1]
	s_waitcnt lgkmcnt(0)
	v_lshlrev_b32_e32 v131, 16, v172
	v_and_b32_e32 v149, 0xffff0000, v172
	v_mul_f32_e32 v131, 0x42800000, v131
	v_mul_f32_e32 v149, 0x42800000, v149
	v_mov_b32_e32 v154, v171
	v_cvt_pk_fp8_f32 v154, v131, v149
	v_lshlrev_b32_e32 v150, 16, v173
	v_and_b32_e32 v149, 0xffff0000, v173
	v_mul_f32_e32 v131, 0x42800000, v150
	v_mul_f32_e32 v149, 0x42800000, v149
	v_cvt_pk_fp8_f32 v154, v131, v149 op_sel:[0,0,1]
	v_lshlrev_b32_e32 v131, 16, v174
	v_and_b32_e32 v149, 0xffff0000, v174
	v_mul_f32_e32 v131, 0x42800000, v131
	v_mul_f32_e32 v149, 0x42800000, v149
	v_mov_b32_e32 v155, v171
	v_cvt_pk_fp8_f32 v155, v131, v149
	v_lshlrev_b32_e32 v150, 16, v175
	v_and_b32_e32 v149, 0xffff0000, v175
	v_mul_f32_e32 v131, 0x42800000, v150
	v_mul_f32_e32 v149, 0x42800000, v149
	v_cvt_pk_fp8_f32 v155, v131, v149 op_sel:[0,0,1]
	v_add_u32_e32 v149, v220, v221
	ds_read_b128 v[172:175], v149
	v_add_u32_e32 v150, v220, v222
	ds_read_b128 v[176:179], v150
	global_store_dwordx4 v[180:181], v[152:155], off
	s_waitcnt lgkmcnt(1)
	v_lshlrev_b32_e32 v131, 16, v172
	v_and_b32_e32 v151, 0xffff0000, v172
	v_mul_f32_e32 v131, 0x42800000, v131
	v_mul_f32_e32 v151, 0x42800000, v151
	v_mov_b32_e32 v172, v171
	v_cvt_pk_fp8_f32 v172, v131, v151
	v_lshlrev_b32_e32 v170, 16, v173
	v_and_b32_e32 v151, 0xffff0000, v173
	v_mul_f32_e32 v131, 0x42800000, v170
	v_mul_f32_e32 v151, 0x42800000, v151
	v_cvt_pk_fp8_f32 v172, v131, v151 op_sel:[0,0,1]
	v_lshlrev_b32_e32 v131, 16, v174
	v_and_b32_e32 v151, 0xffff0000, v174
	v_mul_f32_e32 v131, 0x42800000, v131
	v_mul_f32_e32 v151, 0x42800000, v151
	v_mov_b32_e32 v173, v171
	v_cvt_pk_fp8_f32 v173, v131, v151
	v_lshlrev_b32_e32 v170, 16, v175
	v_and_b32_e32 v151, 0xffff0000, v175
	v_mul_f32_e32 v131, 0x42800000, v170
	v_mul_f32_e32 v151, 0x42800000, v151
	v_cvt_pk_fp8_f32 v173, v131, v151 op_sel:[0,0,1]
	s_waitcnt lgkmcnt(0)
	v_lshlrev_b32_e32 v131, 16, v176
	v_and_b32_e32 v151, 0xffff0000, v176
	v_mul_f32_e32 v131, 0x42800000, v131
	v_mul_f32_e32 v151, 0x42800000, v151
	v_mov_b32_e32 v174, v171
	v_cvt_pk_fp8_f32 v174, v131, v151
	v_lshlrev_b32_e32 v170, 16, v177
	v_and_b32_e32 v151, 0xffff0000, v177
	v_mul_f32_e32 v131, 0x42800000, v170
	v_mul_f32_e32 v151, 0x42800000, v151
	v_cvt_pk_fp8_f32 v174, v131, v151 op_sel:[0,0,1]
	v_lshlrev_b32_e32 v131, 16, v178
	v_and_b32_e32 v151, 0xffff0000, v178
	v_mul_f32_e32 v131, 0x42800000, v131
	v_mul_f32_e32 v151, 0x42800000, v151
	v_mov_b32_e32 v175, v171
	v_cvt_pk_fp8_f32 v175, v131, v151
	v_lshlrev_b32_e32 v170, 16, v179
	v_and_b32_e32 v151, 0xffff0000, v179
	v_mul_f32_e32 v131, 0x42800000, v170
	v_mul_f32_e32 v151, 0x42800000, v151
	v_cvt_pk_fp8_f32 v175, v131, v151 op_sel:[0,0,1]
	global_store_dwordx4 v[132:133], v[172:175], off
	s_waitcnt lgkmcnt(0)
	s_cbranch_vccnz .LBB0_246
	s_add_i32 s65, s57, 0x8001
	s_cmp_ge_i32 s65, s21
	s_cbranch_scc1 .LcvwP2a_b
	s_cmpk_gt_i32 s33, 0x7ffd
	s_mov_b64 s[62:63], -1
	s_cbranch_scc0 .LBB0_258
	s_add_i32 s0, s57, 1
	s_lshr_b32 s0, s0, 9
	s_lshl_b64 s[6:7], s[0:1], 23
	s_add_u32 s6, s58, s6
	s_addc_u32 s7, s59, s7
	s_and_b32 s33, s52, 0x380
	s_lshl_b32 s44, s33, 13
	s_add_u32 s6, s6, s44
	s_addc_u32 s7, s7, 0
	s_and_b32 s54, s56, 0x7e0
	s_lshl_b32 s44, s54, 2
	s_add_u32 s44, s6, s44
	s_addc_u32 s45, s7, 0
	s_lshl_b64 s[6:7], s[0:1], 21
	s_lshl_b32 s0, s54, 10
	s_add_u32 s6, s70, s6
	s_addc_u32 s7, s71, s7
	s_add_u32 s0, s6, s0
	s_addc_u32 s7, s7, 0
	s_add_u32 s6, s0, s33
	s_addc_u32 s7, s7, 0
	s_mov_b64 s[62:63], 0

; #define LAS __attribute__((address_space(3)))
; __device__ __forceinline__ unsigned cvt_pk_bf16(float lo, float hi) { unsigned r; asm volatile("v_cvt_pk_bf16_f32 %0, %1, %2" : "=v"(r) : "v"(lo), "v"(hi)); return r; }
; __device__ __forceinline__ void t64_load(const float* Wsrc, int ldw, int lane, f32x4 (&tv)[16]) {
;     const float* p = Wsrc + (size_t)(lane >> 3) * ldw + 4 * (lane & 7);
; #pragma unroll
;     for (int i = 0; i < 16; ++i) { tv[i] = __builtin_nontemporal_load((const f32x4*)p); p += 8 * ldw; }
; }
; __device__ __forceinline__ void t64_finish(const f32x4 (&tv)[16], unsigned char* dst, int ldd, int f8, LAS unsigned char* scr, int lane) {
;     const int g = lane >> 4, i16 = lane & 15;
; #pragma unroll
;     for (int i = 0; i < 16; ++i) { v2u w; w.x = cvt_pk_bf16(tv[i].x, tv[i].y); w.y = cvt_pk_bf16(tv[i].z, tv[i].w); *(LAS v2u*)(scr + (8 * i + (lane >> 3)) * 64 + 8 * (lane & 7)) = w; }
; __device__ __forceinline__ void convert_range(const float* w_gate, const float* w_up, const float* w_down, bf16* BTGU, bf16* BTD, int x0, int x1, LAS unsigned char* scr, int lane) {
;     ...
; #pragma unroll 1
;     for (int x = x0; x < x1; x += 2) {
;         const bool hasB = x + 1 < x1;
;         if (hasB) { B = xitem(w_gate, w_up, w_down, BTGU, BTD, x + 1); t64_load(B.src, B.ldw, lane, tc); }
;         t64_finish(ta, A.dst, A.ldd, A.f8, scr, lane);
.LBB0_268:
	v_mul_u32_u24_e32 v0, s0, v158
	v_lshlrev_b32_e32 v128, 2, v0
	v_lshl_add_u64 v[0:1], s[20:21], 0, v[128:129]
	v_mov_b32_e32 v131, v129
	v_lshl_add_u64 v[0:1], v[0:1], 0, v[130:131]
	s_lshl_b32 s0, s0, 5
	v_lshl_add_u64 v[8:9], v[0:1], 0, s[0:1]
	global_load_dwordx4 v[0:3], v[0:1], off nt
	s_nop 0
	global_load_dwordx4 v[4:7], v[8:9], off nt
	v_lshl_add_u64 v[8:9], v[8:9], 0, s[0:1]
	v_lshl_add_u64 v[16:17], v[8:9], 0, s[0:1]
	global_load_dwordx4 v[8:11], v[8:9], off nt
	s_nop 0
	global_load_dwordx4 v[12:15], v[16:17], off nt
	v_lshl_add_u64 v[16:17], v[16:17], 0, s[0:1]
	v_lshl_add_u64 v[24:25], v[16:17], 0, s[0:1]
	global_load_dwordx4 v[16:19], v[16:17], off nt
	s_nop 0
	global_load_dwordx4 v[20:23], v[24:25], off nt
	v_lshl_add_u64 v[24:25], v[24:25], 0, s[0:1]
	v_lshl_add_u64 v[32:33], v[24:25], 0, s[0:1]
	v_lshl_add_u64 v[36:37], v[32:33], 0, s[0:1]
	v_lshl_add_u64 v[40:41], v[36:37], 0, s[0:1]
	v_lshl_add_u64 v[44:45], v[40:41], 0, s[0:1]
	v_lshl_add_u64 v[52:53], v[44:45], 0, s[0:1]
	v_lshl_add_u64 v[56:57], v[52:53], 0, s[0:1]
	v_lshl_add_u64 v[64:65], v[56:57], 0, s[0:1]
	v_lshl_add_u64 v[68:69], v[64:65], 0, s[0:1]
	global_load_dwordx4 v[24:27], v[24:25], off nt
	s_nop 0
	global_load_dwordx4 v[28:31], v[32:33], off nt
	s_nop 0
	global_load_dwordx4 v[32:35], v[36:37], off nt
	s_nop 0
	global_load_dwordx4 v[36:39], v[40:41], off nt
	s_nop 0
	global_load_dwordx4 v[40:43], v[44:45], off nt
	s_nop 0
	global_load_dwordx4 v[44:47], v[52:53], off nt
	s_nop 0
	global_load_dwordx4 v[52:55], v[56:57], off nt
	s_nop 0
	global_load_dwordx4 v[56:59], v[64:65], off nt
	s_nop 0
	global_load_dwordx4 v[64:67], v[68:69], off nt
	v_lshl_add_u64 v[68:69], v[68:69], 0, s[0:1]
	global_load_dwordx4 v[68:71], v[68:69], off nt
	s_waitcnt vmcnt(16)
	s_branch .LBB0_269
.LcvwP2b_b:
	s_waitcnt vmcnt(0)
.LBB0_269:
	v_cvt_pk_bf16_f32 v132, v48, v49
	v_cvt_pk_bf16_f32 v133, v50, v51
	ds_write_b64 v134, v[132:133]
	v_cvt_pk_bf16_f32 v132, v60, v61
	v_cvt_pk_bf16_f32 v133, v62, v63
	ds_write_b64 v134, v[132:133] offset:512
	v_cvt_pk_bf16_f32 v132, v72, v73
	v_cvt_pk_bf16_f32 v133, v74, v75
	ds_write_b64 v134, v[132:133] offset:1024
	v_cvt_pk_bf16_f32 v132, v76, v77
	v_cvt_pk_bf16_f32 v133, v78, v79
	ds_write_b64 v134, v[132:133] offset:1536
	v_cvt_pk_bf16_f32 v132, v80, v81
	v_cvt_pk_bf16_f32 v133, v82, v83
	ds_write_b64 v134, v[132:133] offset:2048
	v_cvt_pk_bf16_f32 v132, v84, v85
	v_cvt_pk_bf16_f32 v133, v86, v87
	ds_write_b64 v134, v[132:133] offset:2560
	v_cvt_pk_bf16_f32 v132, v88, v89
	v_cvt_pk_bf16_f32 v133, v90, v91
	ds_write_b64 v134, v[132:133] offset:3072
	v_cvt_pk_bf16_f32 v132, v92, v93
	v_cvt_pk_bf16_f32 v133, v94, v95
	ds_write_b64 v134, v[132:133] offset:3584
	v_cvt_pk_bf16_f32 v132, v96, v97
	v_cvt_pk_bf16_f32 v133, v98, v99
	ds_write_b64 v134, v[132:133] offset:4096
	v_cvt_pk_bf16_f32 v132, v100, v101
	v_cvt_pk_bf16_f32 v133, v102, v103
	ds_write_b64 v134, v[132:133] offset:4608
	v_cvt_pk_bf16_f32 v132, v104, v105
	v_cvt_pk_bf16_f32 v133, v106, v107
	ds_write_b64 v134, v[132:133] offset:5120
	v_cvt_pk_bf16_f32 v132, v108, v109
	v_cvt_pk_bf16_f32 v133, v110, v111
	ds_write_b64 v134, v[132:133] offset:5632
	v_cvt_pk_bf16_f32 v132, v112, v113
	v_cvt_pk_bf16_f32 v133, v114, v115
	ds_write_b64 v134, v[132:133] offset:6144
	v_cvt_pk_bf16_f32 v132, v116, v117
	v_cvt_pk_bf16_f32 v133, v118, v119
	ds_write_b64 v134, v[132:133] offset:6656
	v_cvt_pk_bf16_f32 v132, v120, v121
	v_cvt_pk_bf16_f32 v133, v122, v123
	ds_write_b64 v134, v[132:133] offset:7168
	v_cvt_pk_bf16_f32 v132, v124, v125
	v_cvt_pk_bf16_f32 v133, v126, v127
	ds_write_b64 v134, v[132:133] offset:7680
	s_waitcnt lgkmcnt(0)
	ds_read_b64_tr_b16 v[152:153], v135
	ds_read_b64_tr_b16 v[154:155], v135 offset:256
	ds_read_b64_tr_b16 v[170:171], v135 offset:1024
	ds_read_b64_tr_b16 v[172:173], v135 offset:1280
	ds_read_b64_tr_b16 v[174:175], v135 offset:2048
	ds_read_b64_tr_b16 v[176:177], v135 offset:2304
	ds_read_b64_tr_b16 v[178:179], v135 offset:3072
	ds_read_b64_tr_b16 v[180:181], v135 offset:3328
	ds_read_b64_tr_b16 v[182:183], v135 offset:4096
	ds_read_b64_tr_b16 v[184:185], v135 offset:4352
	ds_read_b64_tr_b16 v[186:187], v135 offset:5120
	ds_read_b64_tr_b16 v[188:189], v135 offset:5376
	ds_read_b64_tr_b16 v[190:191], v135 offset:6144
	ds_read_b64_tr_b16 v[192:193], v135 offset:6400
	ds_read_b64_tr_b16 v[132:133], v135 offset:7168
	ds_read_b64_tr_b16 v[134:135], v135 offset:7424
	s_waitcnt lgkmcnt(0)
	s_waitcnt lgkmcnt(14)
	ds_write_b128 v136, v[152:155]
	s_waitcnt lgkmcnt(13)
	ds_write_b128 v137, v[170:173]
	s_waitcnt lgkmcnt(12)
	ds_write_b128 v138, v[174:177]
	s_waitcnt lgkmcnt(11)
	ds_write_b128 v139, v[178:181]
	s_waitcnt lgkmcnt(10)
	ds_write_b128 v140, v[182:185]
	s_waitcnt lgkmcnt(9)
	ds_write_b128 v141, v[186:189]
	s_waitcnt lgkmcnt(8)
	ds_write_b128 v142, v[190:193]
	s_waitcnt lgkmcnt(7)
	ds_write_b128 v143, v[132:135]
	s_waitcnt lgkmcnt(0)
	ds_read_b128 v[134:137], v144
	ds_read_b128 v[138:141], v145
	v_lshl_add_u64 v[132:133], s[16:17], 0, v[160:161]
	s_waitcnt lgkmcnt(1)
	v_lshlrev_b32_e32 v128, 16, v134
	v_and_b32_e32 v131, 0xffff0000, v134
	v_mul_f32_e32 v128, 0x42800000, v128
	v_mul_f32_e32 v131, 0x42800000, v131
	v_mov_b32_e32 v134, v129
	v_cvt_pk_fp8_f32 v134, v128, v131
	v_lshlrev_b32_e32 v142, 16, v135
	v_and_b32_e32 v131, 0xffff0000, v135
	v_mul_f32_e32 v128, 0x42800000, v142
	v_mul_f32_e32 v131, 0x42800000, v131
	v_cvt_pk_fp8_f32 v134, v128, v131 op_sel:[0,0,1]
	v_lshlrev_b32_e32 v128, 16, v136
	v_and_b32_e32 v131, 0xffff0000, v136
	v_mul_f32_e32 v128, 0x42800000, v128
	v_mul_f32_e32 v131, 0x42800000, v131
	v_mov_b32_e32 v135, v129
	v_cvt_pk_fp8_f32 v135, v128, v131
	v_lshlrev_b32_e32 v136, 16, v137
	v_and_b32_e32 v131, 0xffff0000, v137
	v_mul_f32_e32 v128, 0x42800000, v136
	v_mul_f32_e32 v131, 0x42800000, v131
	v_cvt_pk_fp8_f32 v135, v128, v131 op_sel:[0,0,1]
	s_waitcnt lgkmcnt(0)
; #define GAS __attribute__((address_space(1)))
; #define LAS __attribute__((address_space(3)))
; __device__ __forceinline__ unsigned pk4_fp8(float a, float b, float c, float d) { int p = 0; p = __builtin_amdgcn_cvt_pk_fp8_f32(a, b, p, false); p = __builtin_amdgcn_cvt_pk_fp8_f32(c, d, p, true); return (unsigned)p; }
; __device__ __forceinline__ void t64_finish(const f32x4 (&tv)[16], unsigned char* dst, int ldd, int f8, LAS unsigned char* scr, int lane) {
;     ...
;     for (int it = 0; it < 4; ++it) { const int n = 8 * it + rr;
;         const v4u v0 = *(const LAS v4u*)(scr + n * 256 + 16 * ((2 * cc) ^ (n & 15))), v1 = *(const LAS v4u*)(scr + n * 256 + 16 * ((2 * cc + 1) ^ (n & 15)));
;         if (f8) { v4u o4; o4.x = pk4_fp8(bf_lo(v0.x) * W8_SCALE, bf_hi(v0.x) * W8_SCALE, bf_lo(v0.y) * W8_SCALE, bf_hi(v0.y) * W8_SCALE);
;             o4.y = pk4_fp8(bf_lo(v0.z) * W8_SCALE, bf_hi(v0.z) * W8_SCALE, bf_lo(v0.w) * W8_SCALE, bf_hi(v0.w) * W8_SCALE);
;             o4.z = pk4_fp8(bf_lo(v1.x) * W8_SCALE, bf_hi(v1.x) * W8_SCALE, bf_lo(v1.y) * W8_SCALE, bf_hi(v1.y) * W8_SCALE);
;             o4.w = pk4_fp8(bf_lo(v1.z) * W8_SCALE, bf_hi(v1.z) * W8_SCALE, bf_lo(v1.w) * W8_SCALE, bf_hi(v1.w) * W8_SCALE);
;             __builtin_nontemporal_store(o4, (GAS v4u*)(dst + (size_t)n * ldd + 16 * cc)); }
;         else { *(GAS v4u*)(dst + (size_t)n * ldd + 32 * cc) = v0; *(GAS v4u*)(dst + (size_t)n * ldd + 32 * cc + 16) = v1; } }
	v_lshlrev_b32_e32 v128, 16, v138
	v_and_b32_e32 v131, 0xffff0000, v138
	v_mul_f32_e32 v128, 0x42800000, v128
	v_mul_f32_e32 v131, 0x42800000, v131
	v_mov_b32_e32 v136, v129
	v_cvt_pk_fp8_f32 v136, v128, v131
	v_lshlrev_b32_e32 v137, 16, v139
	v_and_b32_e32 v131, 0xffff0000, v139
	v_mul_f32_e32 v128, 0x42800000, v137
	v_mul_f32_e32 v131, 0x42800000, v131
	v_cvt_pk_fp8_f32 v136, v128, v131 op_sel:[0,0,1]
	v_lshlrev_b32_e32 v128, 16, v140
	v_and_b32_e32 v131, 0xffff0000, v140
	v_mul_f32_e32 v128, 0x42800000, v128
	v_mul_f32_e32 v131, 0x42800000, v131
	v_mov_b32_e32 v137, v129
	v_cvt_pk_fp8_f32 v137, v128, v131
	v_lshlrev_b32_e32 v138, 16, v141
	v_and_b32_e32 v131, 0xffff0000, v141
	v_mul_f32_e32 v128, 0x42800000, v138
	v_mul_f32_e32 v131, 0x42800000, v131
	ds_read_b128 v[138:141], v146
	v_cvt_pk_fp8_f32 v137, v128, v131 op_sel:[0,0,1]
	v_mad_u64_u32 v[142:143], s[20:21], s40, v158, v[132:133]
	global_store_dwordx4 v[142:143], v[134:137], off
	ds_read_b128 v[134:137], v147
	s_waitcnt lgkmcnt(1)
	v_lshlrev_b32_e32 v128, 16, v138
	v_and_b32_e32 v131, 0xffff0000, v138
	v_mul_f32_e32 v128, 0x42800000, v128
	v_mul_f32_e32 v131, 0x42800000, v131
	v_mov_b32_e32 v138, v129
	v_cvt_pk_fp8_f32 v138, v128, v131
	v_lshlrev_b32_e32 v142, 16, v139
	v_and_b32_e32 v131, 0xffff0000, v139
	v_mul_f32_e32 v128, 0x42800000, v142
	v_mul_f32_e32 v131, 0x42800000, v131
	v_cvt_pk_fp8_f32 v138, v128, v131 op_sel:[0,0,1]
	v_lshlrev_b32_e32 v128, 16, v140
	v_and_b32_e32 v131, 0xffff0000, v140
	v_mul_f32_e32 v128, 0x42800000, v128
	v_mul_f32_e32 v131, 0x42800000, v131
	v_mov_b32_e32 v139, v129
	v_cvt_pk_fp8_f32 v139, v128, v131
	v_lshlrev_b32_e32 v140, 16, v141
	v_and_b32_e32 v131, 0xffff0000, v141
	v_mul_f32_e32 v128, 0x42800000, v140
	v_mul_f32_e32 v131, 0x42800000, v131
	v_cvt_pk_fp8_f32 v139, v128, v131 op_sel:[0,0,1]
	s_waitcnt lgkmcnt(0)
	v_lshlrev_b32_e32 v128, 16, v134
	v_and_b32_e32 v131, 0xffff0000, v134
	v_mul_f32_e32 v128, 0x42800000, v128
	v_mul_f32_e32 v131, 0x42800000, v131
	v_mov_b32_e32 v140, v129
	v_cvt_pk_fp8_f32 v140, v128, v131
	v_lshlrev_b32_e32 v134, 16, v135
	v_and_b32_e32 v131, 0xffff0000, v135
	v_mul_f32_e32 v128, 0x42800000, v134
	v_mul_f32_e32 v131, 0x42800000, v131
	v_cvt_pk_fp8_f32 v140, v128, v131 op_sel:[0,0,1]
	v_lshlrev_b32_e32 v128, 16, v136
	v_and_b32_e32 v131, 0xffff0000, v136
	v_mul_f32_e32 v128, 0x42800000, v128
	v_mul_f32_e32 v131, 0x42800000, v131
	v_mov_b32_e32 v141, v129
	v_cvt_pk_fp8_f32 v141, v128, v131
	v_lshlrev_b32_e32 v134, 16, v137
	v_and_b32_e32 v131, 0xffff0000, v137
	v_mul_f32_e32 v128, 0x42800000, v134
	v_mul_f32_e32 v131, 0x42800000, v131
	ds_read_b128 v[134:137], v148
	v_cvt_pk_fp8_f32 v141, v128, v131 op_sel:[0,0,1]
	v_mad_u64_u32 v[142:143], s[20:21], s40, v162, v[132:133]
	v_mad_u64_u32 v[146:147], s[20:21], s40, v164, v[132:133]
	global_store_dwordx4 v[142:143], v[138:141], off
	ds_read_b128 v[138:141], v149
	s_waitcnt lgkmcnt(1)
	v_lshlrev_b32_e32 v128, 16, v134
	v_and_b32_e32 v131, 0xffff0000, v134
	v_mul_f32_e32 v128, 0x42800000, v128
	v_mul_f32_e32 v131, 0x42800000, v131
	v_mov_b32_e32 v134, v129
	v_cvt_pk_fp8_f32 v134, v128, v131
	v_lshlrev_b32_e32 v142, 16, v135
	v_and_b32_e32 v131, 0xffff0000, v135
	v_mul_f32_e32 v128, 0x42800000, v142
	v_mul_f32_e32 v131, 0x42800000, v131
	v_cvt_pk_fp8_f32 v134, v128, v131 op_sel:[0,0,1]
	v_lshlrev_b32_e32 v128, 16, v136
	v_and_b32_e32 v131, 0xffff0000, v136
	v_mul_f32_e32 v128, 0x42800000, v128
	v_mul_f32_e32 v131, 0x42800000, v131
	v_mov_b32_e32 v135, v129
	v_cvt_pk_fp8_f32 v135, v128, v131
	v_lshlrev_b32_e32 v136, 16, v137
	v_and_b32_e32 v131, 0xffff0000, v137
	v_mul_f32_e32 v128, 0x42800000, v136
	v_mul_f32_e32 v131, 0x42800000, v131
	v_cvt_pk_fp8_f32 v135, v128, v131 op_sel:[0,0,1]
	s_waitcnt lgkmcnt(0)
	v_lshlrev_b32_e32 v128, 16, v138
	v_and_b32_e32 v131, 0xffff0000, v138
	v_mul_f32_e32 v128, 0x42800000, v128
	v_mul_f32_e32 v131, 0x42800000, v131
	v_mov_b32_e32 v136, v129
	v_cvt_pk_fp8_f32 v136, v128, v131
	v_lshlrev_b32_e32 v137, 16, v139
	v_and_b32_e32 v131, 0xffff0000, v139
	v_mul_f32_e32 v128, 0x42800000, v137
	v_mul_f32_e32 v131, 0x42800000, v131
	v_cvt_pk_fp8_f32 v136, v128, v131 op_sel:[0,0,1]
	v_lshlrev_b32_e32 v128, 16, v140
	v_and_b32_e32 v131, 0xffff0000, v140
	v_lshlrev_b32_e32 v137, 16, v141
	v_mul_f32_e32 v128, 0x42800000, v128
	v_mul_f32_e32 v131, 0x42800000, v131
	v_mul_f32_e32 v142, 0x42800000, v137
	v_mov_b32_e32 v137, v129
	v_cvt_pk_fp8_f32 v137, v128, v131
	v_and_b32_e32 v128, 0xffff0000, v141
	ds_read_b128 v[138:141], v150
	v_mul_f32_e32 v128, 0x42800000, v128
	v_cvt_pk_fp8_f32 v137, v142, v128 op_sel:[0,0,1]
	ds_read_b128 v[142:145], v151
	v_mad_u64_u32 v[132:133], s[20:21], s40, v166, v[132:133]
	s_waitcnt lgkmcnt(1)
	v_lshlrev_b32_e32 v128, 16, v138
	v_and_b32_e32 v131, 0xffff0000, v138
	v_mul_f32_e32 v128, 0x42800000, v128
	v_mul_f32_e32 v131, 0x42800000, v131
	v_mov_b32_e32 v138, v129
	v_cvt_pk_fp8_f32 v138, v128, v131
	v_lshlrev_b32_e32 v148, 16, v139
	v_and_b32_e32 v131, 0xffff0000, v139
	v_mul_f32_e32 v128, 0x42800000, v148
	v_mul_f32_e32 v131, 0x42800000, v131
	v_cvt_pk_fp8_f32 v138, v128, v131 op_sel:[0,0,1]
	v_lshlrev_b32_e32 v128, 16, v140
	v_and_b32_e32 v131, 0xffff0000, v140
	v_mul_f32_e32 v128, 0x42800000, v128
	v_mul_f32_e32 v131, 0x42800000, v131
	v_mov_b32_e32 v139, v129
	v_cvt_pk_fp8_f32 v139, v128, v131
	v_lshlrev_b32_e32 v140, 16, v141
	v_and_b32_e32 v131, 0xffff0000, v141
	v_mul_f32_e32 v128, 0x42800000, v140
	v_mul_f32_e32 v131, 0x42800000, v131
	v_cvt_pk_fp8_f32 v139, v128, v131 op_sel:[0,0,1]
	s_waitcnt lgkmcnt(0)
	v_lshlrev_b32_e32 v128, 16, v142
	v_and_b32_e32 v131, 0xffff0000, v142
	v_mul_f32_e32 v128, 0x42800000, v128
	v_mul_f32_e32 v131, 0x42800000, v131
	v_mov_b32_e32 v140, v129
	v_cvt_pk_fp8_f32 v140, v128, v131
	v_lshlrev_b32_e32 v141, 16, v143
	v_and_b32_e32 v131, 0xffff0000, v143
	v_mul_f32_e32 v128, 0x42800000, v141
	v_mul_f32_e32 v131, 0x42800000, v131
	v_cvt_pk_fp8_f32 v140, v128, v131 op_sel:[0,0,1]
	v_lshlrev_b32_e32 v128, 16, v144
	v_and_b32_e32 v131, 0xffff0000, v144
	v_mul_f32_e32 v128, 0x42800000, v128
	v_mul_f32_e32 v131, 0x42800000, v131
	v_mov_b32_e32 v141, v129
	v_cvt_pk_fp8_f32 v141, v128, v131
	v_lshlrev_b32_e32 v142, 16, v145
	v_and_b32_e32 v131, 0xffff0000, v145
	v_mul_f32_e32 v128, 0x42800000, v142
	v_mul_f32_e32 v131, 0x42800000, v131
	v_cvt_pk_fp8_f32 v141, v128, v131 op_sel:[0,0,1]
	global_store_dwordx4 v[146:147], v[134:137], off
	global_store_dwordx4 v[132:133], v[138:141], off
	s_waitcnt lgkmcnt(0)

; __device__ __forceinline__ void t64_load(const float* Wsrc, int ldw, int lane, f32x4 (&tv)[16]) {
;     const float* p = Wsrc + (size_t)(lane >> 3) * ldw + 4 * (lane & 7);
; #pragma unroll
;     for (int i = 0; i < 16; ++i) { tv[i] = __builtin_nontemporal_load((const f32x4*)p); p += 8 * ldw; }
; }
; __device__ __forceinline__ void convert_range(const float* w_gate, const float* w_up, const float* w_down, bf16* BTGU, bf16* BTD, int x0, int x1, LAS unsigned char* scr, int lane) {
;     ...
;             if (x + 2 < x1) { A = xitem(w_gate, w_up, w_down, BTGU, BTD, x + 2); t64_load(A.src, A.ldw, lane, ta); }
.LBB0_277:
	s_waitcnt vmcnt(24)
	v_mul_u32_u24_e32 v48, s0, v158
	v_lshlrev_b32_e32 v128, 2, v48
	v_lshl_add_u64 v[48:49], s[22:23], 0, v[128:129]
	v_mov_b32_e32 v131, v129
	v_lshl_add_u64 v[48:49], v[48:49], 0, v[130:131]
	s_lshl_b32 s0, s0, 5
	s_waitcnt vmcnt(20)
	v_lshl_add_u64 v[72:73], v[48:49], 0, s[0:1]
	global_load_dwordx4 v[48:51], v[48:49], off nt
	s_nop 0
	global_load_dwordx4 v[60:63], v[72:73], off nt
	v_lshl_add_u64 v[72:73], v[72:73], 0, s[0:1]
	v_lshl_add_u64 v[80:81], v[72:73], 0, s[0:1]
	global_load_dwordx4 v[72:75], v[72:73], off nt
	s_nop 0
	global_load_dwordx4 v[76:79], v[80:81], off nt
	v_lshl_add_u64 v[80:81], v[80:81], 0, s[0:1]
	v_lshl_add_u64 v[88:89], v[80:81], 0, s[0:1]
	global_load_dwordx4 v[80:83], v[80:81], off nt
	s_nop 0
	global_load_dwordx4 v[84:87], v[88:89], off nt
	v_lshl_add_u64 v[88:89], v[88:89], 0, s[0:1]
	v_lshl_add_u64 v[96:97], v[88:89], 0, s[0:1]
	v_lshl_add_u64 v[100:101], v[96:97], 0, s[0:1]
	v_lshl_add_u64 v[104:105], v[100:101], 0, s[0:1]
	v_lshl_add_u64 v[108:109], v[104:105], 0, s[0:1]
	v_lshl_add_u64 v[112:113], v[108:109], 0, s[0:1]
	v_lshl_add_u64 v[116:117], v[112:113], 0, s[0:1]
	v_lshl_add_u64 v[120:121], v[116:117], 0, s[0:1]
	v_lshl_add_u64 v[124:125], v[120:121], 0, s[0:1]
	global_load_dwordx4 v[88:91], v[88:89], off nt
	s_nop 0
	global_load_dwordx4 v[92:95], v[96:97], off nt
	s_nop 0
	global_load_dwordx4 v[96:99], v[100:101], off nt
	s_nop 0
	global_load_dwordx4 v[100:103], v[104:105], off nt
	s_nop 0
	global_load_dwordx4 v[104:107], v[108:109], off nt
	s_nop 0
	global_load_dwordx4 v[108:111], v[112:113], off nt
	s_nop 0
	global_load_dwordx4 v[112:115], v[116:117], off nt
	s_nop 0
	global_load_dwordx4 v[116:119], v[120:121], off nt
	s_nop 0
	global_load_dwordx4 v[120:123], v[124:125], off nt
	v_lshl_add_u64 v[124:125], v[124:125], 0, s[0:1]
	global_load_dwordx4 v[124:127], v[124:125], off nt
	s_waitcnt vmcnt(16)
	s_branch .LcvwP2b_a

; #define LAS __attribute__((address_space(3)))
; #define LDS_WAIT() asm volatile("s_waitcnt lgkmcnt(0)" ::: "memory")
; __device__ __forceinline__ unsigned cvt_pk_bf16(float lo, float hi) { unsigned r; asm volatile("v_cvt_pk_bf16_f32 %0, %1, %2" : "=v"(r) : "v"(lo), "v"(hi)); return r; }
; __device__ __forceinline__ void t64_finish(const f32x4 (&tv)[16], unsigned char* dst, int ldd, int f8, LAS unsigned char* scr, int lane) {
;     const int g = lane >> 4, i16 = lane & 15;
; #pragma unroll
;     for (int i = 0; i < 16; ++i) { v2u w; w.x = cvt_pk_bf16(tv[i].x, tv[i].y); w.y = cvt_pk_bf16(tv[i].z, tv[i].w); *(LAS v2u*)(scr + (8 * i + (lane >> 3)) * 64 + 8 * (lane & 7)) = w; }
;     LDS_WAIT(); asm volatile("" ::: "memory");
;     const int q = i16 >> 2, pp = i16 & 3;
;     bf16x8 o[8];
; #pragma unroll
;     for (int jj = 0; jj < 8; ++jj) { const int c = 4 * jj + g, nb = c & 1, kg = c >> 1;
;         LAS unsigned char* ra = scr + (8 * kg + q) * 64 + 32 * nb + 8 * pp;
;         const s16x4 lo = __builtin_bit_cast(s16x4, __builtin_amdgcn_ds_read_tr16_b64_v4i16((LAS s16x4*)ra));
;         const s16x4 hi = __builtin_bit_cast(s16x4, __builtin_amdgcn_ds_read_tr16_b64_v4i16((LAS s16x4*)(ra + 4 * 64)));
;         o[jj] = __builtin_shufflevector(lo, hi, 0, 1, 2, 3, 4, 5, 6, 7); }
;     LDS_WAIT(); asm volatile("" ::: "memory");
; #pragma unroll
;     for (int jj = 0; jj < 8; ++jj) { const int c = 4 * jj + g, nb = c & 1, kg = c >> 1; const int n = 16 * nb + i16;
;         *(LAS bf16x8*)(scr + n * 256 + 16 * (kg ^ (n & 15))) = o[jj]; }
;     LDS_WAIT(); asm volatile("" ::: "memory");
; __device__ __forceinline__ void convert_range(const float* w_gate, const float* w_up, const float* w_down, bf16* BTGU, bf16* BTD, int x0, int x1, LAS unsigned char* scr, int lane) {
;     ...
;             t64_finish(tc, B.dst, B.ldd, B.f8, scr, lane);
.LcvwP2b_a:
	v_cvt_pk_bf16_f32 v132, v0, v1
	v_cvt_pk_bf16_f32 v133, v2, v3
	v_add_u32_e32 v134, v163, v165
	ds_write_b64 v134, v[132:133]
	v_cvt_pk_bf16_f32 v132, v4, v5
	v_cvt_pk_bf16_f32 v133, v6, v7
	ds_write_b64 v134, v[132:133] offset:512
	v_cvt_pk_bf16_f32 v132, v8, v9
	v_cvt_pk_bf16_f32 v133, v10, v11
	ds_write_b64 v134, v[132:133] offset:1024
	v_cvt_pk_bf16_f32 v132, v12, v13
	v_cvt_pk_bf16_f32 v133, v14, v15
	ds_write_b64 v134, v[132:133] offset:1536
	v_cvt_pk_bf16_f32 v132, v16, v17
	v_cvt_pk_bf16_f32 v133, v18, v19
	ds_write_b64 v134, v[132:133] offset:2048
	v_cvt_pk_bf16_f32 v132, v20, v21
	v_cvt_pk_bf16_f32 v133, v22, v23
	ds_write_b64 v134, v[132:133] offset:2560
	v_cvt_pk_bf16_f32 v132, v24, v25
	v_cvt_pk_bf16_f32 v133, v26, v27
	ds_write_b64 v134, v[132:133] offset:3072
	v_cvt_pk_bf16_f32 v132, v28, v29
	v_cvt_pk_bf16_f32 v133, v30, v31
	ds_write_b64 v134, v[132:133] offset:3584
	v_cvt_pk_bf16_f32 v132, v32, v33
	v_cvt_pk_bf16_f32 v133, v34, v35
	ds_write_b64 v134, v[132:133] offset:4096
	v_cvt_pk_bf16_f32 v132, v36, v37
	v_cvt_pk_bf16_f32 v133, v38, v39
	ds_write_b64 v134, v[132:133] offset:4608
	v_cvt_pk_bf16_f32 v132, v40, v41
	v_cvt_pk_bf16_f32 v133, v42, v43
	ds_write_b64 v134, v[132:133] offset:5120
	v_cvt_pk_bf16_f32 v132, v44, v45
	v_cvt_pk_bf16_f32 v133, v46, v47
	ds_write_b64 v134, v[132:133] offset:5632
	v_cvt_pk_bf16_f32 v132, v52, v53
	v_cvt_pk_bf16_f32 v133, v54, v55
	ds_write_b64 v134, v[132:133] offset:6144
	v_cvt_pk_bf16_f32 v132, v56, v57
	v_cvt_pk_bf16_f32 v133, v58, v59
	ds_write_b64 v134, v[132:133] offset:6656
	v_cvt_pk_bf16_f32 v132, v64, v65
	v_cvt_pk_bf16_f32 v133, v66, v67
	ds_write_b64 v134, v[132:133] offset:7168
	v_cvt_pk_bf16_f32 v132, v68, v69
	v_cvt_pk_bf16_f32 v133, v70, v71
	ds_write_b64 v134, v[132:133] offset:7680
	s_waitcnt lgkmcnt(0)
	v_add_u32_e32 v135, v167, v169
	ds_read_b64_tr_b16 v[138:139], v135
	ds_read_b64_tr_b16 v[140:141], v135 offset:256
	ds_read_b64_tr_b16 v[142:143], v135 offset:1024
	ds_read_b64_tr_b16 v[144:145], v135 offset:1280
	ds_read_b64_tr_b16 v[146:147], v135 offset:2048
	ds_read_b64_tr_b16 v[148:149], v135 offset:2304
	ds_read_b64_tr_b16 v[150:151], v135 offset:3072
	ds_read_b64_tr_b16 v[152:153], v135 offset:3328
	ds_read_b64_tr_b16 v[170:171], v135 offset:4096
	ds_read_b64_tr_b16 v[172:173], v135 offset:4352
	ds_read_b64_tr_b16 v[174:175], v135 offset:5120
	ds_read_b64_tr_b16 v[176:177], v135 offset:5376
	ds_read_b64_tr_b16 v[178:179], v135 offset:6144
	ds_read_b64_tr_b16 v[180:181], v135 offset:6400
	ds_read_b64_tr_b16 v[182:183], v135 offset:7168
	ds_read_b64_tr_b16 v[184:185], v135 offset:7424
	s_waitcnt lgkmcnt(0)
	v_add_u32_e32 v136, v204, v205
	v_add_u32_e32 v137, v204, v206
	s_waitcnt lgkmcnt(14)
	ds_write_b128 v136, v[138:141]
	s_waitcnt lgkmcnt(13)
	ds_write_b128 v137, v[142:145]
	v_add_u32_e32 v138, v204, v207
	v_add_u32_e32 v139, v204, v208
	v_add_u32_e32 v140, v204, v209
	v_add_u32_e32 v141, v204, v210
	v_add_u32_e32 v142, v204, v211
	v_add_u32_e32 v143, v204, v212
	s_waitcnt lgkmcnt(12)
	ds_write_b128 v138, v[146:149]
	s_waitcnt lgkmcnt(11)
	ds_write_b128 v139, v[150:153]
	s_waitcnt lgkmcnt(10)
	ds_write_b128 v140, v[170:173]
	s_waitcnt lgkmcnt(9)
	ds_write_b128 v141, v[174:177]
	s_waitcnt lgkmcnt(8)
	ds_write_b128 v142, v[178:181]
	s_waitcnt lgkmcnt(7)
	ds_write_b128 v143, v[182:185]
	s_waitcnt lgkmcnt(0)
	v_add_u32_e32 v144, v213, v214
	ds_read_b128 v[146:149], v144
	v_add_u32_e32 v145, v213, v215
	ds_read_b128 v[150:153], v145
	v_mov_b32_e32 v170, v129
	v_mov_b32_e32 v171, v129
	s_waitcnt lgkmcnt(1)
	v_lshlrev_b32_e32 v128, 16, v146
	v_and_b32_e32 v131, 0xffff0000, v146
	v_mul_f32_e32 v128, 0x42800000, v128
	v_mul_f32_e32 v131, 0x42800000, v131
	v_cvt_pk_fp8_f32 v170, v128, v131
	v_lshlrev_b32_e32 v146, 16, v147
	v_and_b32_e32 v131, 0xffff0000, v147
	v_mul_f32_e32 v128, 0x42800000, v146
	v_mul_f32_e32 v131, 0x42800000, v131
	v_cvt_pk_fp8_f32 v170, v128, v131 op_sel:[0,0,1]
	v_lshlrev_b32_e32 v128, 16, v148
	v_and_b32_e32 v131, 0xffff0000, v148
	v_mul_f32_e32 v128, 0x42800000, v128
	v_mul_f32_e32 v131, 0x42800000, v131
	v_cvt_pk_fp8_f32 v171, v128, v131
	v_lshlrev_b32_e32 v146, 16, v149
	v_and_b32_e32 v131, 0xffff0000, v149
	v_mul_f32_e32 v128, 0x42800000, v146
	v_mul_f32_e32 v131, 0x42800000, v131
	v_cvt_pk_fp8_f32 v171, v128, v131 op_sel:[0,0,1]
	s_waitcnt lgkmcnt(0)
	v_lshlrev_b32_e32 v128, 16, v150
	v_and_b32_e32 v131, 0xffff0000, v150
	v_mul_f32_e32 v128, 0x42800000, v128
	v_mul_f32_e32 v131, 0x42800000, v131
	v_mov_b32_e32 v172, v129
	v_cvt_pk_fp8_f32 v172, v128, v131
	v_lshlrev_b32_e32 v146, 16, v151
	v_and_b32_e32 v131, 0xffff0000, v151
	v_mul_f32_e32 v128, 0x42800000, v146
	v_mul_f32_e32 v131, 0x42800000, v131
	v_cvt_pk_fp8_f32 v172, v128, v131 op_sel:[0,0,1]
	v_lshlrev_b32_e32 v128, 16, v152
	v_and_b32_e32 v131, 0xffff0000, v152
	v_mul_f32_e32 v128, 0x42800000, v128
	v_mul_f32_e32 v131, 0x42800000, v131
	v_mov_b32_e32 v173, v129
	v_cvt_pk_fp8_f32 v173, v128, v131
	v_lshlrev_b32_e32 v146, 16, v153
	v_mul_f32_e32 v128, 0x42800000, v146
	v_and_b32_e32 v131, 0xffff0000, v153
	v_add_u32_e32 v146, v216, v217
	v_mul_f32_e32 v131, 0x42800000, v131
	ds_read_b128 v[148:151], v146
	v_cvt_pk_fp8_f32 v173, v128, v131 op_sel:[0,0,1]
	v_lshl_add_u64 v[132:133], s[6:7], 0, v[160:161]
	v_mad_u64_u32 v[152:153], s[22:23], s45, v158, v[132:133]
	v_add_u32_e32 v147, v216, v218
	global_store_dwordx4 v[152:153], v[170:173], off
	ds_read_b128 v[152:155], v147
	s_waitcnt lgkmcnt(1)
; #define GAS __attribute__((address_space(1)))
; #define LAS __attribute__((address_space(3)))
; __device__ __forceinline__ unsigned pk4_fp8(float a, float b, float c, float d) { int p = 0; p = __builtin_amdgcn_cvt_pk_fp8_f32(a, b, p, false); p = __builtin_amdgcn_cvt_pk_fp8_f32(c, d, p, true); return (unsigned)p; }
; __device__ __forceinline__ void t64_finish(const f32x4 (&tv)[16], unsigned char* dst, int ldd, int f8, LAS unsigned char* scr, int lane) {
;     ...
;     for (int it = 0; it < 4; ++it) { const int n = 8 * it + rr;
;         const v4u v0 = *(const LAS v4u*)(scr + n * 256 + 16 * ((2 * cc) ^ (n & 15))), v1 = *(const LAS v4u*)(scr + n * 256 + 16 * ((2 * cc + 1) ^ (n & 15)));
;         if (f8) { v4u o4; o4.x = pk4_fp8(bf_lo(v0.x) * W8_SCALE, bf_hi(v0.x) * W8_SCALE, bf_lo(v0.y) * W8_SCALE, bf_hi(v0.y) * W8_SCALE);
;             o4.y = pk4_fp8(bf_lo(v0.z) * W8_SCALE, bf_hi(v0.z) * W8_SCALE, bf_lo(v0.w) * W8_SCALE, bf_hi(v0.w) * W8_SCALE);
;             o4.z = pk4_fp8(bf_lo(v1.x) * W8_SCALE, bf_hi(v1.x) * W8_SCALE, bf_lo(v1.y) * W8_SCALE, bf_hi(v1.y) * W8_SCALE);
;             o4.w = pk4_fp8(bf_lo(v1.z) * W8_SCALE, bf_hi(v1.z) * W8_SCALE, bf_lo(v1.w) * W8_SCALE, bf_hi(v1.w) * W8_SCALE);
;             __builtin_nontemporal_store(o4, (GAS v4u*)(dst + (size_t)n * ldd + 16 * cc)); }
;         else { *(GAS v4u*)(dst + (size_t)n * ldd + 32 * cc) = v0; *(GAS v4u*)(dst + (size_t)n * ldd + 32 * cc + 16) = v1; } }
; __device__ __forceinline__ XItem xitem(const float* w_gate, const float* w_up, const float* w_down, bf16* BTGU, bf16* BTD, int r) {
;     ...
;     { const int per = (DFF / 128) * (DM / 32); const int e = r / per, r3 = r % per; const int nblk = DM / 32, kb = r3 / nblk, nb = r3 % nblk;
;         it.src = w_down + (size_t)e * DFF * DM + (size_t)(128 * kb) * DM + 32 * nb; it.ldw = DM; it.dst = (unsigned char*)BTD + ((size_t)e * DM + 32 * nb) * DFF + 128 * kb; it.ldd = DFF; it.f8 = 1; return it; }
; __device__ __forceinline__ void convert_range(const float* w_gate, const float* w_up, const float* w_down, bf16* BTGU, bf16* BTD, int x0, int x1, LAS unsigned char* scr, int lane) {
;     ...
;         if (hasB) {
;             if (x + 2 < x1) { A = xitem(w_gate, w_up, w_down, BTGU, BTD, x + 2); t64_load(A.src, A.ldw, lane, ta); }
;             t64_finish(tc, B.dst, B.ldd, B.f8, scr, lane);
;         }
;     }
	v_lshlrev_b32_e32 v128, 16, v148
	v_and_b32_e32 v131, 0xffff0000, v148
	v_mul_f32_e32 v128, 0x42800000, v128
	v_mul_f32_e32 v131, 0x42800000, v131
	v_mov_b32_e32 v170, v129
	v_cvt_pk_fp8_f32 v170, v128, v131
	v_lshlrev_b32_e32 v148, 16, v149
	v_and_b32_e32 v131, 0xffff0000, v149
	v_mul_f32_e32 v128, 0x42800000, v148
	v_mul_f32_e32 v131, 0x42800000, v131
	v_cvt_pk_fp8_f32 v170, v128, v131 op_sel:[0,0,1]
	v_lshlrev_b32_e32 v128, 16, v150
	v_and_b32_e32 v131, 0xffff0000, v150
	v_mul_f32_e32 v128, 0x42800000, v128
	v_mul_f32_e32 v131, 0x42800000, v131
	v_mov_b32_e32 v171, v129
	v_cvt_pk_fp8_f32 v171, v128, v131
	v_lshlrev_b32_e32 v148, 16, v151
	v_and_b32_e32 v131, 0xffff0000, v151
	v_mul_f32_e32 v128, 0x42800000, v148
	v_mul_f32_e32 v131, 0x42800000, v131
	v_cvt_pk_fp8_f32 v171, v128, v131 op_sel:[0,0,1]
	s_waitcnt lgkmcnt(0)
	v_lshlrev_b32_e32 v128, 16, v152
	v_and_b32_e32 v131, 0xffff0000, v152
	v_mul_f32_e32 v128, 0x42800000, v128
	v_mul_f32_e32 v131, 0x42800000, v131
	v_mov_b32_e32 v172, v129
	v_cvt_pk_fp8_f32 v172, v128, v131
	v_lshlrev_b32_e32 v148, 16, v153
	v_and_b32_e32 v131, 0xffff0000, v153
	v_mul_f32_e32 v128, 0x42800000, v148
	v_mul_f32_e32 v131, 0x42800000, v131
	v_cvt_pk_fp8_f32 v172, v128, v131 op_sel:[0,0,1]
	v_lshlrev_b32_e32 v128, 16, v154
	v_and_b32_e32 v131, 0xffff0000, v154
	v_mul_f32_e32 v128, 0x42800000, v128
	v_mul_f32_e32 v131, 0x42800000, v131
	v_mov_b32_e32 v173, v129
	v_cvt_pk_fp8_f32 v173, v128, v131
	v_lshlrev_b32_e32 v148, 16, v155
	v_mul_f32_e32 v128, 0x42800000, v148
	v_and_b32_e32 v131, 0xffff0000, v155
	v_add_u32_e32 v148, v219, v214
	v_mul_f32_e32 v131, 0x42800000, v131
	ds_read_b128 v[150:153], v148
	v_cvt_pk_fp8_f32 v173, v128, v131 op_sel:[0,0,1]
	v_mad_u64_u32 v[154:155], s[22:23], s45, v162, v[132:133]
	v_add_u32_e32 v149, v219, v215
	global_store_dwordx4 v[154:155], v[170:173], off
	ds_read_b128 v[170:173], v149
	s_waitcnt lgkmcnt(1)
	v_lshlrev_b32_e32 v128, 16, v150
	v_and_b32_e32 v131, 0xffff0000, v150
	v_mul_f32_e32 v128, 0x42800000, v128
	v_mul_f32_e32 v131, 0x42800000, v131
	v_mov_b32_e32 v174, v129
	v_cvt_pk_fp8_f32 v174, v128, v131
	v_lshlrev_b32_e32 v150, 16, v151
	v_and_b32_e32 v131, 0xffff0000, v151
	v_mul_f32_e32 v128, 0x42800000, v150
	v_mul_f32_e32 v131, 0x42800000, v131
	v_cvt_pk_fp8_f32 v174, v128, v131 op_sel:[0,0,1]
	v_lshlrev_b32_e32 v128, 16, v152
	v_and_b32_e32 v131, 0xffff0000, v152
	v_mul_f32_e32 v128, 0x42800000, v128
	v_mul_f32_e32 v131, 0x42800000, v131
	v_mov_b32_e32 v175, v129
	v_cvt_pk_fp8_f32 v175, v128, v131
	v_lshlrev_b32_e32 v150, 16, v153
	v_and_b32_e32 v131, 0xffff0000, v153
	v_mul_f32_e32 v128, 0x42800000, v150
	v_mul_f32_e32 v131, 0x42800000, v131
	v_cvt_pk_fp8_f32 v175, v128, v131 op_sel:[0,0,1]
	s_waitcnt lgkmcnt(0)
	v_lshlrev_b32_e32 v128, 16, v170
	v_and_b32_e32 v131, 0xffff0000, v170
	v_mul_f32_e32 v128, 0x42800000, v128
	v_mul_f32_e32 v131, 0x42800000, v131
	v_mov_b32_e32 v176, v129
	v_cvt_pk_fp8_f32 v176, v128, v131
	v_lshlrev_b32_e32 v150, 16, v171
	v_and_b32_e32 v131, 0xffff0000, v171
	v_mul_f32_e32 v128, 0x42800000, v150
	v_mul_f32_e32 v131, 0x42800000, v131
	v_cvt_pk_fp8_f32 v176, v128, v131 op_sel:[0,0,1]
	v_lshlrev_b32_e32 v128, 16, v172
	v_and_b32_e32 v131, 0xffff0000, v172
	v_mul_f32_e32 v128, 0x42800000, v128
	v_mul_f32_e32 v131, 0x42800000, v131
	v_lshlrev_b32_e32 v150, 16, v173
	v_mov_b32_e32 v177, v129
	v_cvt_pk_fp8_f32 v177, v128, v131
	v_mul_f32_e32 v128, 0x42800000, v150
	v_add_u32_e32 v150, v220, v221
	ds_read_b128 v[152:155], v150
	v_and_b32_e32 v131, 0xffff0000, v173
	v_mul_f32_e32 v131, 0x42800000, v131
	v_add_u32_e32 v151, v220, v222
	v_cvt_pk_fp8_f32 v177, v128, v131 op_sel:[0,0,1]
	ds_read_b128 v[170:173], v151
	s_waitcnt lgkmcnt(1)
	v_lshlrev_b32_e32 v128, 16, v152
	v_and_b32_e32 v131, 0xffff0000, v152
	v_mul_f32_e32 v128, 0x42800000, v128
	v_mul_f32_e32 v131, 0x42800000, v131
	v_mov_b32_e32 v152, v129
	v_cvt_pk_fp8_f32 v152, v128, v131
	v_lshlrev_b32_e32 v168, 16, v153
	v_and_b32_e32 v131, 0xffff0000, v153
	v_mul_f32_e32 v128, 0x42800000, v168
	v_mul_f32_e32 v131, 0x42800000, v131
	v_cvt_pk_fp8_f32 v152, v128, v131 op_sel:[0,0,1]
	v_lshlrev_b32_e32 v128, 16, v154
	v_and_b32_e32 v131, 0xffff0000, v154
	v_mul_f32_e32 v128, 0x42800000, v128
	v_mul_f32_e32 v131, 0x42800000, v131
	v_mov_b32_e32 v153, v129
	v_cvt_pk_fp8_f32 v153, v128, v131
	v_lshlrev_b32_e32 v154, 16, v155
	v_and_b32_e32 v131, 0xffff0000, v155
	v_mul_f32_e32 v128, 0x42800000, v154
	v_mul_f32_e32 v131, 0x42800000, v131
	v_cvt_pk_fp8_f32 v153, v128, v131 op_sel:[0,0,1]
	s_waitcnt lgkmcnt(0)
	v_lshlrev_b32_e32 v128, 16, v170
	v_and_b32_e32 v131, 0xffff0000, v170
	v_mul_f32_e32 v128, 0x42800000, v128
	v_mul_f32_e32 v131, 0x42800000, v131
	v_mov_b32_e32 v154, v129
	v_cvt_pk_fp8_f32 v154, v128, v131
	v_lshlrev_b32_e32 v155, 16, v171
	v_and_b32_e32 v131, 0xffff0000, v171
	v_mul_f32_e32 v128, 0x42800000, v155
	v_mul_f32_e32 v131, 0x42800000, v131
	v_cvt_pk_fp8_f32 v154, v128, v131 op_sel:[0,0,1]
	v_lshlrev_b32_e32 v128, 16, v172
	v_and_b32_e32 v131, 0xffff0000, v172
	v_mul_f32_e32 v128, 0x42800000, v128
	v_mul_f32_e32 v131, 0x42800000, v131
	v_mov_b32_e32 v155, v129
	v_cvt_pk_fp8_f32 v155, v128, v131
	v_lshlrev_b32_e32 v168, 16, v173
	v_and_b32_e32 v131, 0xffff0000, v173
	v_mul_f32_e32 v128, 0x42800000, v168
	v_mul_f32_e32 v131, 0x42800000, v131
	v_cvt_pk_fp8_f32 v155, v128, v131 op_sel:[0,0,1]
	v_mad_u64_u32 v[178:179], s[22:23], s45, v164, v[132:133]
	v_mad_u64_u32 v[132:133], s[22:23], s45, v166, v[132:133]
	global_store_dwordx4 v[178:179], v[174:177], off
	global_store_dwordx4 v[132:133], v[152:155], off
	s_waitcnt lgkmcnt(0)
	s_andn2_b64 vcc, exec, s[20:21]
	s_cbranch_vccnz .LBB0_270
	s_add_i32 s41, s44, 0x8001
	s_cmp_ge_i32 s41, s66
	s_cbranch_scc1 .LcvwP2b_b
	s_cmpk_gt_i32 s33, 0x7ffd
	s_mov_b64 s[22:23], -1
	s_cbranch_scc0 .LBB0_282
	s_add_i32 s0, s44, 1
	s_lshr_b32 s0, s0, 9
	s_lshl_b64 s[6:7], s[0:1], 23
	s_add_u32 s6, s58, s6
	s_addc_u32 s7, s59, s7
	s_and_b32 s22, s42, 0x380
	s_lshl_b32 s20, s22, 13
	s_add_u32 s6, s6, s20
	s_addc_u32 s7, s7, 0
	s_and_b32 s23, s43, 0x7e0
	s_lshl_b32 s20, s23, 2
	s_add_u32 s20, s6, s20
	s_addc_u32 s21, s7, 0
	s_lshl_b64 s[6:7], s[0:1], 21
	s_lshl_b32 s0, s23, 10
	s_add_u32 s6, s70, s6
	s_addc_u32 s7, s71, s7
	s_add_u32 s0, s6, s0
	s_addc_u32 s7, s7, 0
	s_add_u32 s6, s0, s22
	s_addc_u32 s7, s7, 0
	s_mov_b64 s[22:23], 0

; __device__ __forceinline__ int lane_id_v() { int l; asm volatile("v_mbcnt_lo_u32_b32 %0, -1, 0\n\tv_mbcnt_hi_u32_b32 %0, -1, %0" : "=v"(l)); return l; }
; __device__ __forceinline__ void convert_range(const float* w_gate, const float* w_up, const float* w_down, bf16* BTGU, bf16* BTD, int x0, int x1, LAS unsigned char* scr, int lane) {
;     ...
;         if (hasB) { B = xitem(w_gate, w_up, w_down, BTGU, BTD, x + 1); t64_load(B.src, B.ldw, lane, tc); }
;         t64_finish(ta, A.dst, A.ldd, A.f8, scr, lane);
; __global__ void __launch_bounds__(512, 2) hymba_fwd(Args args) {
;     ...
;             {
;                 const int units = tb[32] * 8, rem = units % G; int tailb = rem > 0 ? G - rem : G, ti = rem > 0 ? bx - rem : bx;
;                 if (tb[66]) { if (tb[67] > 0) { tailb = tb[67]; ti = tb[68]; } else { tailb = G; ti = bx; } }
;                 if (ti >= 0) { const int lane = lane_id_v(); const int q = (CV_N5 + tailb * 8 - 1) / (tailb * 8), x0 = (ti * 8 + wave) * q, x1 = (x0 + q < CV_N5) ? x0 + q : CV_N5;
;                     convert_range(args.w_gate, args.w_up, args.w_down, BTGU, BTD, CV_GU + CV_D - CV_N5 + x0, CV_GU + CV_D - CV_N5 + x1, lds + wave * 8448, lane); }
.LBB0_767:
	v_mad_i64_i32 v[0:1], s[12:13], s4, v128, 0
	v_lshl_add_u64 v[0:1], v[0:1], 2, s[10:11]
	v_lshlrev_b32_e32 v132, 2, v130
	v_lshl_add_u64 v[4:5], v[0:1], 0, v[132:133]
	s_lshl_b32 s4, s4, 5
	v_lshl_add_u64 v[6:7], v[4:5], 0, s[4:5]
	v_lshl_add_u64 v[12:13], v[6:7], 0, s[4:5]
	v_lshl_add_u64 v[14:15], v[12:13], 0, s[4:5]
	global_load_dwordx4 v[40:43], v[4:5], off nt
	global_load_dwordx4 v[0:3], v[6:7], off nt
	s_nop 0
	global_load_dwordx4 v[4:7], v[12:13], off nt
	global_load_dwordx4 v[8:11], v[14:15], off nt
	v_lshl_add_u64 v[12:13], v[14:15], 0, s[4:5]
	v_lshl_add_u64 v[20:21], v[12:13], 0, s[4:5]
	global_load_dwordx4 v[12:15], v[12:13], off nt
	s_nop 0
	global_load_dwordx4 v[16:19], v[20:21], off nt
	v_lshl_add_u64 v[20:21], v[20:21], 0, s[4:5]
	v_lshl_add_u64 v[28:29], v[20:21], 0, s[4:5]
	v_lshl_add_u64 v[32:33], v[28:29], 0, s[4:5]
	v_lshl_add_u64 v[36:37], v[32:33], 0, s[4:5]
	v_lshl_add_u64 v[44:45], v[36:37], 0, s[4:5]
	v_lshl_add_u64 v[48:49], v[44:45], 0, s[4:5]
	v_lshl_add_u64 v[52:53], v[48:49], 0, s[4:5]
	v_lshl_add_u64 v[56:57], v[52:53], 0, s[4:5]
	v_lshl_add_u64 v[60:61], v[56:57], 0, s[4:5]
	global_load_dwordx4 v[20:23], v[20:21], off nt
	s_nop 0
	global_load_dwordx4 v[24:27], v[28:29], off nt
	s_nop 0
	global_load_dwordx4 v[28:31], v[32:33], off nt
	s_nop 0
	global_load_dwordx4 v[32:35], v[36:37], off nt
	s_nop 0
	global_load_dwordx4 v[36:39], v[44:45], off nt
	s_nop 0
	global_load_dwordx4 v[44:47], v[48:49], off nt
	s_nop 0
	global_load_dwordx4 v[48:51], v[52:53], off nt
	s_nop 0
	global_load_dwordx4 v[52:55], v[56:57], off nt
	s_nop 0
	global_load_dwordx4 v[56:59], v[60:61], off nt
	v_lshl_add_u64 v[60:61], v[60:61], 0, s[4:5]
	global_load_dwordx4 v[60:63], v[60:61], off nt
	s_waitcnt vmcnt(16)
	s_branch .LBB0_768
.LcvwP5_b:
	s_waitcnt vmcnt(0)
.LBB0_768:
	v_cvt_pk_bf16_f32 v142, v64, v65
	v_cvt_pk_bf16_f32 v143, v66, v67
	ds_write_b64 v149, v[142:143]
	v_cvt_pk_bf16_f32 v142, v68, v69
	v_cvt_pk_bf16_f32 v143, v70, v71
	ds_write_b64 v149, v[142:143] offset:512
	v_cvt_pk_bf16_f32 v142, v72, v73
	v_cvt_pk_bf16_f32 v143, v74, v75
	ds_write_b64 v149, v[142:143] offset:1024
	v_cvt_pk_bf16_f32 v142, v76, v77
	v_cvt_pk_bf16_f32 v143, v78, v79
	ds_write_b64 v149, v[142:143] offset:1536
	v_cvt_pk_bf16_f32 v142, v80, v81
	v_cvt_pk_bf16_f32 v143, v82, v83
	ds_write_b64 v149, v[142:143] offset:2048
	v_cvt_pk_bf16_f32 v142, v84, v85
	v_cvt_pk_bf16_f32 v143, v86, v87
	ds_write_b64 v149, v[142:143] offset:2560
	v_cvt_pk_bf16_f32 v142, v88, v89
	v_cvt_pk_bf16_f32 v143, v90, v91
	ds_write_b64 v149, v[142:143] offset:3072
	v_cvt_pk_bf16_f32 v142, v92, v93
	v_cvt_pk_bf16_f32 v143, v94, v95
	ds_write_b64 v149, v[142:143] offset:3584
	v_cvt_pk_bf16_f32 v142, v96, v97
	v_cvt_pk_bf16_f32 v143, v98, v99
	ds_write_b64 v149, v[142:143] offset:4096
	v_cvt_pk_bf16_f32 v142, v100, v101
	v_cvt_pk_bf16_f32 v143, v102, v103
	ds_write_b64 v149, v[142:143] offset:4608
	v_cvt_pk_bf16_f32 v142, v104, v105
	v_cvt_pk_bf16_f32 v143, v106, v107
	ds_write_b64 v149, v[142:143] offset:5120
	v_cvt_pk_bf16_f32 v142, v108, v109
	v_cvt_pk_bf16_f32 v143, v110, v111
	ds_write_b64 v149, v[142:143] offset:5632
	v_cvt_pk_bf16_f32 v142, v112, v113
	v_cvt_pk_bf16_f32 v143, v114, v115
	ds_write_b64 v149, v[142:143] offset:6144
	v_cvt_pk_bf16_f32 v142, v116, v117
	v_cvt_pk_bf16_f32 v143, v118, v119
	ds_write_b64 v149, v[142:143] offset:6656
	v_cvt_pk_bf16_f32 v142, v120, v121
	v_cvt_pk_bf16_f32 v143, v122, v123
	ds_write_b64 v149, v[142:143] offset:7168
	v_cvt_pk_bf16_f32 v142, v124, v125
	v_cvt_pk_bf16_f32 v143, v126, v127
	ds_write_b64 v149, v[142:143] offset:7680
	s_waitcnt lgkmcnt(0)
	ds_read_b64_tr_b16 v[174:175], v169
	ds_read_b64_tr_b16 v[176:177], v169 offset:256
	ds_read_b64_tr_b16 v[178:179], v150
	ds_read_b64_tr_b16 v[180:181], v150 offset:256
	ds_read_b64_tr_b16 v[182:183], v151
	ds_read_b64_tr_b16 v[184:185], v151 offset:256
	ds_read_b64_tr_b16 v[186:187], v152
	ds_read_b64_tr_b16 v[188:189], v152 offset:256
	ds_read_b64_tr_b16 v[190:191], v153
	ds_read_b64_tr_b16 v[192:193], v153 offset:256
	ds_read_b64_tr_b16 v[194:195], v154
	ds_read_b64_tr_b16 v[196:197], v154 offset:256
	ds_read_b64_tr_b16 v[198:199], v155
	ds_read_b64_tr_b16 v[200:201], v155 offset:256
	ds_read_b64_tr_b16 v[202:203], v156
	ds_read_b64_tr_b16 v[204:205], v156 offset:256
	s_waitcnt lgkmcnt(0)
	s_waitcnt lgkmcnt(14)
	ds_write_b128 v157, v[174:177]
	s_waitcnt lgkmcnt(13)
	ds_write_b128 v158, v[178:181]
	s_waitcnt lgkmcnt(12)
	ds_write_b128 v159, v[182:185]
	s_waitcnt lgkmcnt(11)
	ds_write_b128 v160, v[186:189]
	s_waitcnt lgkmcnt(10)
	ds_write_b128 v161, v[190:193]
	s_waitcnt lgkmcnt(9)
	ds_write_b128 v162, v[194:197]
	s_waitcnt lgkmcnt(8)
	ds_write_b128 v163, v[198:201]
	s_waitcnt lgkmcnt(7)
	ds_write_b128 v164, v[202:205]
	s_waitcnt lgkmcnt(0)
	ds_read_b128 v[174:177], v170
	ds_read_b128 v[178:181], v171
	v_lshl_add_u64 v[142:143], s[8:9], 0, v[134:135]
	s_waitcnt lgkmcnt(1)
	v_lshlrev_b32_e32 v132, 16, v174
	v_and_b32_e32 v169, 0xffff0000, v174
	v_mul_f32_e32 v132, 0x42800000, v132
	v_mul_f32_e32 v169, 0x42800000, v169
	v_mov_b32_e32 v174, v133
	v_cvt_pk_fp8_f32 v174, v132, v169
	v_lshlrev_b32_e32 v170, 16, v175
	v_and_b32_e32 v169, 0xffff0000, v175
	v_mul_f32_e32 v132, 0x42800000, v170
	v_mul_f32_e32 v169, 0x42800000, v169
	v_cvt_pk_fp8_f32 v174, v132, v169 op_sel:[0,0,1]
	v_lshlrev_b32_e32 v132, 16, v176
	v_and_b32_e32 v169, 0xffff0000, v176
	v_mul_f32_e32 v132, 0x42800000, v132
	v_mul_f32_e32 v169, 0x42800000, v169
	v_mov_b32_e32 v175, v133
	v_cvt_pk_fp8_f32 v175, v132, v169
	v_lshlrev_b32_e32 v170, 16, v177
	v_and_b32_e32 v169, 0xffff0000, v177
	v_mul_f32_e32 v132, 0x42800000, v170
	v_mul_f32_e32 v169, 0x42800000, v169
	v_cvt_pk_fp8_f32 v175, v132, v169 op_sel:[0,0,1]
	s_waitcnt lgkmcnt(0)
; #define GAS __attribute__((address_space(1)))
; #define LAS __attribute__((address_space(3)))
; __device__ __forceinline__ unsigned pk4_fp8(float a, float b, float c, float d) { int p = 0; p = __builtin_amdgcn_cvt_pk_fp8_f32(a, b, p, false); p = __builtin_amdgcn_cvt_pk_fp8_f32(c, d, p, true); return (unsigned)p; }
; __device__ __forceinline__ void t64_finish(const f32x4 (&tv)[16], unsigned char* dst, int ldd, int f8, LAS unsigned char* scr, int lane) {
;     ...
;     for (int it = 0; it < 4; ++it) { const int n = 8 * it + rr;
;         const v4u v0 = *(const LAS v4u*)(scr + n * 256 + 16 * ((2 * cc) ^ (n & 15))), v1 = *(const LAS v4u*)(scr + n * 256 + 16 * ((2 * cc + 1) ^ (n & 15)));
;         if (f8) { v4u o4; o4.x = pk4_fp8(bf_lo(v0.x) * W8_SCALE, bf_hi(v0.x) * W8_SCALE, bf_lo(v0.y) * W8_SCALE, bf_hi(v0.y) * W8_SCALE);
;             o4.y = pk4_fp8(bf_lo(v0.z) * W8_SCALE, bf_hi(v0.z) * W8_SCALE, bf_lo(v0.w) * W8_SCALE, bf_hi(v0.w) * W8_SCALE);
;             o4.z = pk4_fp8(bf_lo(v1.x) * W8_SCALE, bf_hi(v1.x) * W8_SCALE, bf_lo(v1.y) * W8_SCALE, bf_hi(v1.y) * W8_SCALE);
;             o4.w = pk4_fp8(bf_lo(v1.z) * W8_SCALE, bf_hi(v1.z) * W8_SCALE, bf_lo(v1.w) * W8_SCALE, bf_hi(v1.w) * W8_SCALE);
;             __builtin_nontemporal_store(o4, (GAS v4u*)(dst + (size_t)n * ldd + 16 * cc)); }
;         else { *(GAS v4u*)(dst + (size_t)n * ldd + 32 * cc) = v0; *(GAS v4u*)(dst + (size_t)n * ldd + 32 * cc + 16) = v1; } }
	v_lshlrev_b32_e32 v132, 16, v178
	v_and_b32_e32 v169, 0xffff0000, v178
	v_mul_f32_e32 v132, 0x42800000, v132
	v_mul_f32_e32 v169, 0x42800000, v169
	v_mov_b32_e32 v176, v133
	v_cvt_pk_fp8_f32 v176, v132, v169
	v_lshlrev_b32_e32 v170, 16, v179
	v_and_b32_e32 v169, 0xffff0000, v179
	v_mul_f32_e32 v132, 0x42800000, v170
	v_mul_f32_e32 v169, 0x42800000, v169
	v_cvt_pk_fp8_f32 v176, v132, v169 op_sel:[0,0,1]
	v_lshlrev_b32_e32 v132, 16, v180
	v_and_b32_e32 v169, 0xffff0000, v180
	v_mul_f32_e32 v132, 0x42800000, v132
	v_mul_f32_e32 v169, 0x42800000, v169
	v_mov_b32_e32 v177, v133
	v_cvt_pk_fp8_f32 v177, v132, v169
	v_lshlrev_b32_e32 v170, 16, v181
	v_and_b32_e32 v169, 0xffff0000, v181
	v_mul_f32_e32 v132, 0x42800000, v170
	v_mul_f32_e32 v169, 0x42800000, v169
	ds_read_b128 v[178:181], v165
	v_cvt_pk_fp8_f32 v177, v132, v169 op_sel:[0,0,1]
	v_mad_u64_u32 v[170:171], s[10:11], s14, v128, v[142:143]
	v_mov_b32_e32 v132, v171
	v_mad_u64_u32 v[182:183], s[10:11], s14, v129, v[132:133]
	v_mov_b32_e32 v171, v182
	global_store_dwordx4 v[170:171], v[174:177], off
	ds_read_b128 v[174:177], v166
	s_waitcnt lgkmcnt(1)
	v_lshlrev_b32_e32 v132, 16, v178
	v_and_b32_e32 v169, 0xffff0000, v178
	v_mul_f32_e32 v132, 0x42800000, v132
	v_mul_f32_e32 v169, 0x42800000, v169
	v_mov_b32_e32 v178, v133
	v_cvt_pk_fp8_f32 v178, v132, v169
	v_lshlrev_b32_e32 v170, 16, v179
	v_and_b32_e32 v169, 0xffff0000, v179
	v_mul_f32_e32 v132, 0x42800000, v170
	v_mul_f32_e32 v169, 0x42800000, v169
	v_cvt_pk_fp8_f32 v178, v132, v169 op_sel:[0,0,1]
	v_lshlrev_b32_e32 v132, 16, v180
	v_and_b32_e32 v169, 0xffff0000, v180
	v_mul_f32_e32 v132, 0x42800000, v132
	v_mul_f32_e32 v169, 0x42800000, v169
	v_mov_b32_e32 v179, v133
	v_cvt_pk_fp8_f32 v179, v132, v169
	v_lshlrev_b32_e32 v170, 16, v181
	v_and_b32_e32 v169, 0xffff0000, v181
	v_mul_f32_e32 v132, 0x42800000, v170
	v_mul_f32_e32 v169, 0x42800000, v169
	v_cvt_pk_fp8_f32 v179, v132, v169 op_sel:[0,0,1]
	s_waitcnt lgkmcnt(0)
	v_lshlrev_b32_e32 v132, 16, v174
	v_and_b32_e32 v169, 0xffff0000, v174
	v_mul_f32_e32 v132, 0x42800000, v132
	v_mul_f32_e32 v169, 0x42800000, v169
	v_mov_b32_e32 v180, v133
	v_cvt_pk_fp8_f32 v180, v132, v169
	v_lshlrev_b32_e32 v170, 16, v175
	v_and_b32_e32 v169, 0xffff0000, v175
	v_mul_f32_e32 v132, 0x42800000, v170
	v_mul_f32_e32 v169, 0x42800000, v169
	v_cvt_pk_fp8_f32 v180, v132, v169 op_sel:[0,0,1]
	v_lshlrev_b32_e32 v132, 16, v176
	v_and_b32_e32 v169, 0xffff0000, v176
	v_mul_f32_e32 v132, 0x42800000, v132
	v_mul_f32_e32 v169, 0x42800000, v169
	v_mov_b32_e32 v181, v133
	v_lshlrev_b32_e32 v170, 16, v177
	v_cvt_pk_fp8_f32 v181, v132, v169
	v_and_b32_e32 v169, 0xffff0000, v177
	ds_read_b128 v[174:177], v172
	v_mul_f32_e32 v132, 0x42800000, v170
	v_mul_f32_e32 v169, 0x42800000, v169
	v_mad_u64_u32 v[170:171], s[10:11], s14, v136, v[142:143]
	v_cvt_pk_fp8_f32 v181, v132, v169 op_sel:[0,0,1]
	v_mov_b32_e32 v132, v171
	v_mad_u64_u32 v[182:183], s[10:11], s14, v131, v[132:133]
	s_waitcnt lgkmcnt(0)
	v_lshlrev_b32_e32 v132, 16, v174
	v_and_b32_e32 v169, 0xffff0000, v174
	v_mul_f32_e32 v132, 0x42800000, v132
	v_mul_f32_e32 v169, 0x42800000, v169
	v_mov_b32_e32 v174, v133
	v_cvt_pk_fp8_f32 v174, v132, v169
	v_mov_b32_e32 v171, v182
	global_store_dwordx4 v[170:171], v[178:181], off
	v_and_b32_e32 v169, 0xffff0000, v175
	v_mul_f32_e32 v169, 0x42800000, v169
	v_lshlrev_b32_e32 v178, 16, v175
	v_mul_f32_e32 v132, 0x42800000, v178
	v_cvt_pk_fp8_f32 v174, v132, v169 op_sel:[0,0,1]
	v_lshlrev_b32_e32 v132, 16, v176
	v_and_b32_e32 v169, 0xffff0000, v176
	ds_read_b128 v[170:173], v173
	v_mul_f32_e32 v132, 0x42800000, v132
	v_mul_f32_e32 v169, 0x42800000, v169
	v_mov_b32_e32 v175, v133
	v_cvt_pk_fp8_f32 v175, v132, v169
	v_lshlrev_b32_e32 v176, 16, v177
	v_and_b32_e32 v169, 0xffff0000, v177
	v_mul_f32_e32 v132, 0x42800000, v176
	v_mul_f32_e32 v169, 0x42800000, v169
	v_cvt_pk_fp8_f32 v175, v132, v169 op_sel:[0,0,1]
	s_waitcnt lgkmcnt(0)
	v_lshlrev_b32_e32 v132, 16, v170
	v_and_b32_e32 v169, 0xffff0000, v170
	v_mul_f32_e32 v132, 0x42800000, v132
	v_mul_f32_e32 v169, 0x42800000, v169
	v_mov_b32_e32 v176, v133
	v_cvt_pk_fp8_f32 v176, v132, v169
	v_lshlrev_b32_e32 v170, 16, v171
	v_and_b32_e32 v169, 0xffff0000, v171
	v_mul_f32_e32 v132, 0x42800000, v170
	v_mul_f32_e32 v169, 0x42800000, v169
	v_cvt_pk_fp8_f32 v176, v132, v169 op_sel:[0,0,1]
	v_lshlrev_b32_e32 v132, 16, v172
	v_and_b32_e32 v169, 0xffff0000, v172
	v_mul_f32_e32 v132, 0x42800000, v132
	v_mul_f32_e32 v169, 0x42800000, v169
	v_mov_b32_e32 v177, v133
	v_cvt_pk_fp8_f32 v177, v132, v169
	v_lshlrev_b32_e32 v170, 16, v173
	v_and_b32_e32 v169, 0xffff0000, v173
	v_mul_f32_e32 v132, 0x42800000, v170
	v_mul_f32_e32 v169, 0x42800000, v169
	ds_read_b128 v[170:173], v167
	v_cvt_pk_fp8_f32 v177, v132, v169 op_sel:[0,0,1]
	v_mad_u64_u32 v[178:179], s[10:11], s14, v138, v[142:143]
	v_mov_b32_e32 v132, v179
	v_mad_u64_u32 v[180:181], s[10:11], s14, v137, v[132:133]
	v_mov_b32_e32 v179, v180
	global_store_dwordx4 v[178:179], v[174:177], off
	ds_read_b128 v[174:177], v168
	s_waitcnt lgkmcnt(1)
	v_lshlrev_b32_e32 v132, 16, v170
	v_and_b32_e32 v169, 0xffff0000, v170
	v_mul_f32_e32 v132, 0x42800000, v132
	v_mul_f32_e32 v169, 0x42800000, v169
	v_mov_b32_e32 v170, v133
	v_cvt_pk_fp8_f32 v170, v132, v169
	v_lshlrev_b32_e32 v178, 16, v171
	v_and_b32_e32 v169, 0xffff0000, v171
	v_mul_f32_e32 v132, 0x42800000, v178
	v_mul_f32_e32 v169, 0x42800000, v169
	v_cvt_pk_fp8_f32 v170, v132, v169 op_sel:[0,0,1]
	v_lshlrev_b32_e32 v132, 16, v172
	v_and_b32_e32 v169, 0xffff0000, v172
	v_mul_f32_e32 v132, 0x42800000, v132
	v_mul_f32_e32 v169, 0x42800000, v169
	v_mov_b32_e32 v171, v133
	v_cvt_pk_fp8_f32 v171, v132, v169
	v_lshlrev_b32_e32 v172, 16, v173
	v_and_b32_e32 v169, 0xffff0000, v173
	v_mul_f32_e32 v132, 0x42800000, v172
	v_mul_f32_e32 v169, 0x42800000, v169
	v_cvt_pk_fp8_f32 v171, v132, v169 op_sel:[0,0,1]
	s_waitcnt lgkmcnt(0)
	v_lshlrev_b32_e32 v132, 16, v174
	v_and_b32_e32 v169, 0xffff0000, v174
	v_mul_f32_e32 v132, 0x42800000, v132
	v_mul_f32_e32 v169, 0x42800000, v169
	v_mov_b32_e32 v172, v133
	v_cvt_pk_fp8_f32 v172, v132, v169
	v_lshlrev_b32_e32 v173, 16, v175
	v_and_b32_e32 v169, 0xffff0000, v175
	v_mul_f32_e32 v132, 0x42800000, v173
	v_mul_f32_e32 v169, 0x42800000, v169
	v_cvt_pk_fp8_f32 v172, v132, v169 op_sel:[0,0,1]
	v_lshlrev_b32_e32 v132, 16, v176
	v_and_b32_e32 v169, 0xffff0000, v176
	v_mul_f32_e32 v132, 0x42800000, v132
	v_mul_f32_e32 v169, 0x42800000, v169
	v_mov_b32_e32 v173, v133
	v_cvt_pk_fp8_f32 v173, v132, v169
	v_lshlrev_b32_e32 v174, 16, v177
	v_and_b32_e32 v169, 0xffff0000, v177
	v_mul_f32_e32 v132, 0x42800000, v174
	v_mul_f32_e32 v169, 0x42800000, v169
	v_cvt_pk_fp8_f32 v173, v132, v169 op_sel:[0,0,1]
	v_mad_u64_u32 v[142:143], s[10:11], s14, v140, v[142:143]
	v_mov_b32_e32 v132, v143
	v_mad_u64_u32 v[174:175], s[10:11], s14, v139, v[132:133]
	v_mov_b32_e32 v143, v174
	global_store_dwordx4 v[142:143], v[170:173], off
	s_waitcnt lgkmcnt(0)

; __device__ __forceinline__ void t64_load(const float* Wsrc, int ldw, int lane, f32x4 (&tv)[16]) {
;     const float* p = Wsrc + (size_t)(lane >> 3) * ldw + 4 * (lane & 7);
; #pragma unroll
;     for (int i = 0; i < 16; ++i) { tv[i] = __builtin_nontemporal_load((const f32x4*)p); p += 8 * ldw; }
; }
; __device__ __forceinline__ void convert_range(const float* w_gate, const float* w_up, const float* w_down, bf16* BTGU, bf16* BTD, int x0, int x1, LAS unsigned char* scr, int lane) {
;     ...
;             if (x + 2 < x1) { A = xitem(w_gate, w_up, w_down, BTGU, BTD, x + 2); t64_load(A.src, A.ldw, lane, ta); }
.LBB0_776:
	v_mad_i64_i32 v[64:65], s[22:23], s4, v128, 0
	v_lshl_add_u64 v[64:65], v[64:65], 2, s[12:13]
	v_lshlrev_b32_e32 v132, 2, v130
	v_lshl_add_u64 v[72:73], v[64:65], 0, v[132:133]
	s_lshl_b32 s4, s4, 5
	v_lshl_add_u64 v[74:75], v[72:73], 0, s[4:5]
	v_lshl_add_u64 v[80:81], v[74:75], 0, s[4:5]
	v_lshl_add_u64 v[82:83], v[80:81], 0, s[4:5]
	global_load_dwordx4 v[64:67], v[72:73], off nt
	global_load_dwordx4 v[68:71], v[74:75], off nt
	s_nop 0
	global_load_dwordx4 v[72:75], v[80:81], off nt
	global_load_dwordx4 v[76:79], v[82:83], off nt
	v_lshl_add_u64 v[80:81], v[82:83], 0, s[4:5]
	v_lshl_add_u64 v[88:89], v[80:81], 0, s[4:5]
	global_load_dwordx4 v[80:83], v[80:81], off nt
	s_nop 0
	global_load_dwordx4 v[84:87], v[88:89], off nt
	v_lshl_add_u64 v[88:89], v[88:89], 0, s[4:5]
	v_lshl_add_u64 v[96:97], v[88:89], 0, s[4:5]
	v_lshl_add_u64 v[100:101], v[96:97], 0, s[4:5]
	v_lshl_add_u64 v[104:105], v[100:101], 0, s[4:5]
	v_lshl_add_u64 v[108:109], v[104:105], 0, s[4:5]
	v_lshl_add_u64 v[112:113], v[108:109], 0, s[4:5]
	v_lshl_add_u64 v[116:117], v[112:113], 0, s[4:5]
	v_lshl_add_u64 v[120:121], v[116:117], 0, s[4:5]
	v_lshl_add_u64 v[124:125], v[120:121], 0, s[4:5]
	global_load_dwordx4 v[88:91], v[88:89], off nt
	s_nop 0
	global_load_dwordx4 v[92:95], v[96:97], off nt
	s_nop 0
	global_load_dwordx4 v[96:99], v[100:101], off nt
	s_nop 0
	global_load_dwordx4 v[100:103], v[104:105], off nt
	s_nop 0
	global_load_dwordx4 v[104:107], v[108:109], off nt
	s_nop 0
	global_load_dwordx4 v[108:111], v[112:113], off nt
	s_nop 0
	global_load_dwordx4 v[112:115], v[116:117], off nt
	s_nop 0
	global_load_dwordx4 v[116:119], v[120:121], off nt
	s_nop 0
	global_load_dwordx4 v[120:123], v[124:125], off nt
	v_lshl_add_u64 v[124:125], v[124:125], 0, s[4:5]
	global_load_dwordx4 v[124:127], v[124:125], off nt
	s_waitcnt vmcnt(16)
	s_branch .LcvwP5_a

; #define LAS __attribute__((address_space(3)))
; #define LDS_WAIT() asm volatile("s_waitcnt lgkmcnt(0)" ::: "memory")
; __device__ __forceinline__ unsigned cvt_pk_bf16(float lo, float hi) { unsigned r; asm volatile("v_cvt_pk_bf16_f32 %0, %1, %2" : "=v"(r) : "v"(lo), "v"(hi)); return r; }
; __device__ __forceinline__ void t64_finish(const f32x4 (&tv)[16], unsigned char* dst, int ldd, int f8, LAS unsigned char* scr, int lane) {
;     const int g = lane >> 4, i16 = lane & 15;
; #pragma unroll
;     for (int i = 0; i < 16; ++i) { v2u w; w.x = cvt_pk_bf16(tv[i].x, tv[i].y); w.y = cvt_pk_bf16(tv[i].z, tv[i].w); *(LAS v2u*)(scr + (8 * i + (lane >> 3)) * 64 + 8 * (lane & 7)) = w; }
;     LDS_WAIT(); asm volatile("" ::: "memory");
;     const int q = i16 >> 2, pp = i16 & 3;
;     bf16x8 o[8];
; #pragma unroll
;     for (int jj = 0; jj < 8; ++jj) { const int c = 4 * jj + g, nb = c & 1, kg = c >> 1;
;         LAS unsigned char* ra = scr + (8 * kg + q) * 64 + 32 * nb + 8 * pp;
;         const s16x4 lo = __builtin_bit_cast(s16x4, __builtin_amdgcn_ds_read_tr16_b64_v4i16((LAS s16x4*)ra));
;         const s16x4 hi = __builtin_bit_cast(s16x4, __builtin_amdgcn_ds_read_tr16_b64_v4i16((LAS s16x4*)(ra + 4 * 64)));
;         o[jj] = __builtin_shufflevector(lo, hi, 0, 1, 2, 3, 4, 5, 6, 7); }
;     LDS_WAIT(); asm volatile("" ::: "memory");
; #pragma unroll
;     for (int jj = 0; jj < 8; ++jj) { const int c = 4 * jj + g, nb = c & 1, kg = c >> 1; const int n = 16 * nb + i16;
;         *(LAS bf16x8*)(scr + n * 256 + 16 * (kg ^ (n & 15))) = o[jj]; }
;     LDS_WAIT(); asm volatile("" ::: "memory");
; __device__ __forceinline__ void convert_range(const float* w_gate, const float* w_up, const float* w_down, bf16* BTGU, bf16* BTD, int x0, int x1, LAS unsigned char* scr, int lane) {
;     ...
;             t64_finish(tc, B.dst, B.ldd, B.f8, scr, lane);
.LcvwP5_a:
	v_cvt_pk_bf16_f32 v142, v40, v41
	v_cvt_pk_bf16_f32 v143, v42, v43
	ds_write_b64 v149, v[142:143]
	v_cvt_pk_bf16_f32 v142, v0, v1
	v_cvt_pk_bf16_f32 v143, v2, v3
	ds_write_b64 v149, v[142:143] offset:512
	v_cvt_pk_bf16_f32 v142, v4, v5
	v_cvt_pk_bf16_f32 v143, v6, v7
	ds_write_b64 v149, v[142:143] offset:1024
	v_cvt_pk_bf16_f32 v142, v8, v9
	v_cvt_pk_bf16_f32 v143, v10, v11
	ds_write_b64 v149, v[142:143] offset:1536
	v_cvt_pk_bf16_f32 v142, v12, v13
	v_cvt_pk_bf16_f32 v143, v14, v15
	ds_write_b64 v149, v[142:143] offset:2048
	v_cvt_pk_bf16_f32 v142, v16, v17
	v_cvt_pk_bf16_f32 v143, v18, v19
	ds_write_b64 v149, v[142:143] offset:2560
	v_cvt_pk_bf16_f32 v142, v20, v21
	v_cvt_pk_bf16_f32 v143, v22, v23
	ds_write_b64 v149, v[142:143] offset:3072
	v_cvt_pk_bf16_f32 v142, v24, v25
	v_cvt_pk_bf16_f32 v143, v26, v27
	ds_write_b64 v149, v[142:143] offset:3584
	v_cvt_pk_bf16_f32 v142, v28, v29
	v_cvt_pk_bf16_f32 v143, v30, v31
	ds_write_b64 v149, v[142:143] offset:4096
	v_cvt_pk_bf16_f32 v142, v32, v33
	v_cvt_pk_bf16_f32 v143, v34, v35
	ds_write_b64 v149, v[142:143] offset:4608
	v_cvt_pk_bf16_f32 v142, v36, v37
	v_cvt_pk_bf16_f32 v143, v38, v39
	ds_write_b64 v149, v[142:143] offset:5120
	v_cvt_pk_bf16_f32 v142, v44, v45
	v_cvt_pk_bf16_f32 v143, v46, v47
	ds_write_b64 v149, v[142:143] offset:5632
	v_cvt_pk_bf16_f32 v142, v48, v49
	v_cvt_pk_bf16_f32 v143, v50, v51
	ds_write_b64 v149, v[142:143] offset:6144
	v_cvt_pk_bf16_f32 v142, v52, v53
	v_cvt_pk_bf16_f32 v143, v54, v55
	ds_write_b64 v149, v[142:143] offset:6656
	v_cvt_pk_bf16_f32 v142, v56, v57
	v_cvt_pk_bf16_f32 v143, v58, v59
	ds_write_b64 v149, v[142:143] offset:7168
	v_cvt_pk_bf16_f32 v142, v60, v61
	v_cvt_pk_bf16_f32 v143, v62, v63
	ds_write_b64 v149, v[142:143] offset:7680
	s_waitcnt lgkmcnt(0)
	v_add_u32_e32 v169, v141, v144
	ds_read_b64_tr_b16 v[170:171], v169
	ds_read_b64_tr_b16 v[172:173], v169 offset:256
	ds_read_b64_tr_b16 v[174:175], v150
	ds_read_b64_tr_b16 v[176:177], v150 offset:256
	ds_read_b64_tr_b16 v[178:179], v151
	ds_read_b64_tr_b16 v[180:181], v151 offset:256
	ds_read_b64_tr_b16 v[182:183], v152
	ds_read_b64_tr_b16 v[184:185], v152 offset:256
	ds_read_b64_tr_b16 v[186:187], v153
	ds_read_b64_tr_b16 v[188:189], v153 offset:256
	ds_read_b64_tr_b16 v[190:191], v154
	ds_read_b64_tr_b16 v[192:193], v154 offset:256
	ds_read_b64_tr_b16 v[194:195], v155
	ds_read_b64_tr_b16 v[196:197], v155 offset:256
	ds_read_b64_tr_b16 v[198:199], v156
	ds_read_b64_tr_b16 v[200:201], v156 offset:256
	s_waitcnt lgkmcnt(0)
	s_waitcnt lgkmcnt(14)
	ds_write_b128 v157, v[170:173]
	s_waitcnt lgkmcnt(13)
	ds_write_b128 v158, v[174:177]
	s_waitcnt lgkmcnt(12)
	ds_write_b128 v159, v[178:181]
	s_waitcnt lgkmcnt(11)
	ds_write_b128 v160, v[182:185]
	s_waitcnt lgkmcnt(10)
	ds_write_b128 v161, v[186:189]
	s_waitcnt lgkmcnt(9)
	ds_write_b128 v162, v[190:193]
	s_waitcnt lgkmcnt(8)
	ds_write_b128 v163, v[194:197]
	s_waitcnt lgkmcnt(7)
	ds_write_b128 v164, v[198:201]
	s_waitcnt lgkmcnt(0)
	v_add_u32_e32 v170, v145, v146
	ds_read_b128 v[172:175], v170
	v_add_u32_e32 v171, v145, v147
	ds_read_b128 v[176:179], v171
	v_lshl_add_u64 v[142:143], s[6:7], 0, v[134:135]
	s_andn2_b64 vcc, exec, s[10:11]
	s_waitcnt lgkmcnt(1)
	v_lshlrev_b32_e32 v132, 16, v172
	v_and_b32_e32 v172, 0xffff0000, v172
	v_mul_f32_e32 v132, 0x42800000, v132
	v_mul_f32_e32 v180, 0x42800000, v172
	v_mov_b32_e32 v172, v133
	v_cvt_pk_fp8_f32 v172, v132, v180
	v_lshlrev_b32_e32 v181, 16, v173
	v_and_b32_e32 v173, 0xffff0000, v173
	v_mul_f32_e32 v132, 0x42800000, v181
	v_mul_f32_e32 v173, 0x42800000, v173
	v_cvt_pk_fp8_f32 v172, v132, v173 op_sel:[0,0,1]
	v_lshlrev_b32_e32 v132, 16, v174
	v_and_b32_e32 v173, 0xffff0000, v174
	v_mul_f32_e32 v132, 0x42800000, v132
	v_mul_f32_e32 v174, 0x42800000, v173
	v_mov_b32_e32 v173, v133
	v_cvt_pk_fp8_f32 v173, v132, v174
	v_lshlrev_b32_e32 v180, 16, v175
	v_and_b32_e32 v174, 0xffff0000, v175
	v_mul_f32_e32 v132, 0x42800000, v180
	v_mul_f32_e32 v174, 0x42800000, v174
	v_cvt_pk_fp8_f32 v173, v132, v174 op_sel:[0,0,1]
	s_waitcnt lgkmcnt(0)
	v_lshlrev_b32_e32 v132, 16, v176
	v_and_b32_e32 v174, 0xffff0000, v176
	v_mul_f32_e32 v132, 0x42800000, v132
	v_mul_f32_e32 v175, 0x42800000, v174
	v_mov_b32_e32 v174, v133
	v_cvt_pk_fp8_f32 v174, v132, v175
	v_lshlrev_b32_e32 v176, 16, v177
	v_and_b32_e32 v175, 0xffff0000, v177
	v_mul_f32_e32 v132, 0x42800000, v176
	v_mul_f32_e32 v175, 0x42800000, v175
	v_cvt_pk_fp8_f32 v174, v132, v175 op_sel:[0,0,1]
	v_lshlrev_b32_e32 v132, 16, v178
	v_and_b32_e32 v175, 0xffff0000, v178
	v_mul_f32_e32 v132, 0x42800000, v132
	v_mul_f32_e32 v176, 0x42800000, v175
	v_mov_b32_e32 v175, v133
	v_cvt_pk_fp8_f32 v175, v132, v176
	v_lshlrev_b32_e32 v177, 16, v179
	v_and_b32_e32 v176, 0xffff0000, v179
	v_mul_f32_e32 v132, 0x42800000, v177
	v_mul_f32_e32 v176, 0x42800000, v176
	v_cvt_pk_fp8_f32 v175, v132, v176 op_sel:[0,0,1]
	ds_read_b128 v[176:179], v165
	v_mad_u64_u32 v[180:181], s[12:13], s17, v128, v[142:143]
	v_mov_b32_e32 v132, v181
	v_mad_u64_u32 v[182:183], s[12:13], s17, v129, v[132:133]
	v_mov_b32_e32 v181, v182
	global_store_dwordx4 v[180:181], v[172:175], off
	ds_read_b128 v[172:175], v166
	s_waitcnt lgkmcnt(1)
	v_lshlrev_b32_e32 v132, 16, v176
	v_and_b32_e32 v176, 0xffff0000, v176
	v_mul_f32_e32 v132, 0x42800000, v132
	v_mul_f32_e32 v180, 0x42800000, v176
	v_mov_b32_e32 v176, v133
	v_cvt_pk_fp8_f32 v176, v132, v180
	v_lshlrev_b32_e32 v181, 16, v177
	v_and_b32_e32 v177, 0xffff0000, v177
	v_mul_f32_e32 v132, 0x42800000, v181
	v_mul_f32_e32 v177, 0x42800000, v177
	v_cvt_pk_fp8_f32 v176, v132, v177 op_sel:[0,0,1]
	v_lshlrev_b32_e32 v132, 16, v178
	v_and_b32_e32 v177, 0xffff0000, v178
	v_mul_f32_e32 v132, 0x42800000, v132
	v_mul_f32_e32 v178, 0x42800000, v177
	v_mov_b32_e32 v177, v133
	v_cvt_pk_fp8_f32 v177, v132, v178
	v_lshlrev_b32_e32 v180, 16, v179
	v_and_b32_e32 v178, 0xffff0000, v179
	v_mul_f32_e32 v132, 0x42800000, v180
	v_mul_f32_e32 v178, 0x42800000, v178
	v_cvt_pk_fp8_f32 v177, v132, v178 op_sel:[0,0,1]
	s_waitcnt lgkmcnt(0)
; #define GAS __attribute__((address_space(1)))
; #define LAS __attribute__((address_space(3)))
; __device__ __forceinline__ unsigned pk4_fp8(float a, float b, float c, float d) { int p = 0; p = __builtin_amdgcn_cvt_pk_fp8_f32(a, b, p, false); p = __builtin_amdgcn_cvt_pk_fp8_f32(c, d, p, true); return (unsigned)p; }
; __device__ __forceinline__ void t64_finish(const f32x4 (&tv)[16], unsigned char* dst, int ldd, int f8, LAS unsigned char* scr, int lane) {
;     ...
;     for (int it = 0; it < 4; ++it) { const int n = 8 * it + rr;
;         const v4u v0 = *(const LAS v4u*)(scr + n * 256 + 16 * ((2 * cc) ^ (n & 15))), v1 = *(const LAS v4u*)(scr + n * 256 + 16 * ((2 * cc + 1) ^ (n & 15)));
;         if (f8) { v4u o4; o4.x = pk4_fp8(bf_lo(v0.x) * W8_SCALE, bf_hi(v0.x) * W8_SCALE, bf_lo(v0.y) * W8_SCALE, bf_hi(v0.y) * W8_SCALE);
;             o4.y = pk4_fp8(bf_lo(v0.z) * W8_SCALE, bf_hi(v0.z) * W8_SCALE, bf_lo(v0.w) * W8_SCALE, bf_hi(v0.w) * W8_SCALE);
;             o4.z = pk4_fp8(bf_lo(v1.x) * W8_SCALE, bf_hi(v1.x) * W8_SCALE, bf_lo(v1.y) * W8_SCALE, bf_hi(v1.y) * W8_SCALE);
;             o4.w = pk4_fp8(bf_lo(v1.z) * W8_SCALE, bf_hi(v1.z) * W8_SCALE, bf_lo(v1.w) * W8_SCALE, bf_hi(v1.w) * W8_SCALE);
;             __builtin_nontemporal_store(o4, (GAS v4u*)(dst + (size_t)n * ldd + 16 * cc)); }
;         else { *(GAS v4u*)(dst + (size_t)n * ldd + 32 * cc) = v0; *(GAS v4u*)(dst + (size_t)n * ldd + 32 * cc + 16) = v1; } }
; __device__ __forceinline__ XItem xitem(const float* w_gate, const float* w_up, const float* w_down, bf16* BTGU, bf16* BTD, int r) {
;     ...
;     { const int per = (DFF / 128) * (DM / 32); const int e = r / per, r3 = r % per; const int nblk = DM / 32, kb = r3 / nblk, nb = r3 % nblk;
;         it.src = w_down + (size_t)e * DFF * DM + (size_t)(128 * kb) * DM + 32 * nb; it.ldw = DM; it.dst = (unsigned char*)BTD + ((size_t)e * DM + 32 * nb) * DFF + 128 * kb; it.ldd = DFF; it.f8 = 1; return it; }
; __device__ __forceinline__ void convert_range(const float* w_gate, const float* w_up, const float* w_down, bf16* BTGU, bf16* BTD, int x0, int x1, LAS unsigned char* scr, int lane) {
;     ...
;         if (hasB) {
;             if (x + 2 < x1) { A = xitem(w_gate, w_up, w_down, BTGU, BTD, x + 2); t64_load(A.src, A.ldw, lane, ta); }
;             t64_finish(tc, B.dst, B.ldd, B.f8, scr, lane);
;         }
;     }
	v_lshlrev_b32_e32 v132, 16, v172
	v_and_b32_e32 v172, 0xffff0000, v172
	v_mul_f32_e32 v132, 0x42800000, v132
	v_mul_f32_e32 v172, 0x42800000, v172
	v_mov_b32_e32 v178, v133
	v_cvt_pk_fp8_f32 v178, v132, v172
	v_lshlrev_b32_e32 v179, 16, v173
	v_and_b32_e32 v172, 0xffff0000, v173
	v_mul_f32_e32 v132, 0x42800000, v179
	v_mul_f32_e32 v172, 0x42800000, v172
	v_cvt_pk_fp8_f32 v178, v132, v172 op_sel:[0,0,1]
	v_lshlrev_b32_e32 v132, 16, v174
	v_and_b32_e32 v172, 0xffff0000, v174
	v_mul_f32_e32 v132, 0x42800000, v132
	v_mul_f32_e32 v172, 0x42800000, v172
	v_mov_b32_e32 v179, v133
	v_cvt_pk_fp8_f32 v179, v132, v172
	v_lshlrev_b32_e32 v173, 16, v175
	v_and_b32_e32 v172, 0xffff0000, v175
	v_mul_f32_e32 v132, 0x42800000, v173
	v_mul_f32_e32 v172, 0x42800000, v172
	v_cvt_pk_fp8_f32 v179, v132, v172 op_sel:[0,0,1]
	v_add_u32_e32 v172, v148, v146
	ds_read_b128 v[180:183], v172
	v_mad_u64_u32 v[174:175], s[12:13], s17, v136, v[142:143]
	v_mov_b32_e32 v132, v175
	v_mad_u64_u32 v[184:185], s[12:13], s17, v131, v[132:133]
	v_mov_b32_e32 v175, v184
	v_add_u32_e32 v173, v148, v147
	global_store_dwordx4 v[174:175], v[176:179], off
	ds_read_b128 v[174:177], v173
	s_waitcnt lgkmcnt(1)
	v_lshlrev_b32_e32 v132, 16, v180
	v_and_b32_e32 v178, 0xffff0000, v180
	v_mul_f32_e32 v132, 0x42800000, v132
	v_mul_f32_e32 v179, 0x42800000, v178
	v_mov_b32_e32 v178, v133
	v_cvt_pk_fp8_f32 v178, v132, v179
	v_lshlrev_b32_e32 v180, 16, v181
	v_and_b32_e32 v179, 0xffff0000, v181
	v_mul_f32_e32 v132, 0x42800000, v180
	v_mul_f32_e32 v179, 0x42800000, v179
	v_cvt_pk_fp8_f32 v178, v132, v179 op_sel:[0,0,1]
	v_lshlrev_b32_e32 v132, 16, v182
	v_and_b32_e32 v179, 0xffff0000, v182
	v_mul_f32_e32 v132, 0x42800000, v132
	v_mul_f32_e32 v180, 0x42800000, v179
	v_mov_b32_e32 v179, v133
	v_cvt_pk_fp8_f32 v179, v132, v180
	v_lshlrev_b32_e32 v181, 16, v183
	v_and_b32_e32 v180, 0xffff0000, v183
	v_mul_f32_e32 v132, 0x42800000, v181
	v_mul_f32_e32 v180, 0x42800000, v180
	v_cvt_pk_fp8_f32 v179, v132, v180 op_sel:[0,0,1]
	s_waitcnt lgkmcnt(0)
	v_lshlrev_b32_e32 v132, 16, v174
	v_and_b32_e32 v174, 0xffff0000, v174
	v_mul_f32_e32 v132, 0x42800000, v132
	v_mul_f32_e32 v174, 0x42800000, v174
	v_mov_b32_e32 v180, v133
	v_cvt_pk_fp8_f32 v180, v132, v174
	v_lshlrev_b32_e32 v181, 16, v175
	v_and_b32_e32 v174, 0xffff0000, v175
	v_mul_f32_e32 v132, 0x42800000, v181
	v_mul_f32_e32 v174, 0x42800000, v174
	v_cvt_pk_fp8_f32 v180, v132, v174 op_sel:[0,0,1]
	v_lshlrev_b32_e32 v132, 16, v176
	v_and_b32_e32 v174, 0xffff0000, v176
	v_mul_f32_e32 v132, 0x42800000, v132
	v_mul_f32_e32 v174, 0x42800000, v174
	v_mov_b32_e32 v181, v133
	v_cvt_pk_fp8_f32 v181, v132, v174
	v_lshlrev_b32_e32 v175, 16, v177
	v_and_b32_e32 v174, 0xffff0000, v177
	v_mul_f32_e32 v132, 0x42800000, v175
	v_mul_f32_e32 v174, 0x42800000, v174
	v_cvt_pk_fp8_f32 v181, v132, v174 op_sel:[0,0,1]
	ds_read_b128 v[174:177], v167
	v_mad_u64_u32 v[182:183], s[12:13], s17, v138, v[142:143]
	v_mov_b32_e32 v132, v183
	v_mad_u64_u32 v[184:185], s[12:13], s17, v137, v[132:133]
	v_mov_b32_e32 v183, v184
	global_store_dwordx4 v[182:183], v[178:181], off
	ds_read_b128 v[178:181], v168
	s_waitcnt lgkmcnt(1)
	v_lshlrev_b32_e32 v132, 16, v174
	v_and_b32_e32 v174, 0xffff0000, v174
	v_mul_f32_e32 v132, 0x42800000, v132
	v_mul_f32_e32 v182, 0x42800000, v174
	v_mov_b32_e32 v174, v133
	v_cvt_pk_fp8_f32 v174, v132, v182
	v_lshlrev_b32_e32 v183, 16, v175
	v_and_b32_e32 v175, 0xffff0000, v175
	v_mul_f32_e32 v132, 0x42800000, v183
	v_mul_f32_e32 v175, 0x42800000, v175
	v_cvt_pk_fp8_f32 v174, v132, v175 op_sel:[0,0,1]
	v_lshlrev_b32_e32 v132, 16, v176
	v_and_b32_e32 v175, 0xffff0000, v176
	v_mul_f32_e32 v132, 0x42800000, v132
	v_mul_f32_e32 v176, 0x42800000, v175
	v_mov_b32_e32 v175, v133
	v_cvt_pk_fp8_f32 v175, v132, v176
	v_lshlrev_b32_e32 v182, 16, v177
	v_and_b32_e32 v176, 0xffff0000, v177
	v_mul_f32_e32 v132, 0x42800000, v182
	v_mul_f32_e32 v176, 0x42800000, v176
	v_cvt_pk_fp8_f32 v175, v132, v176 op_sel:[0,0,1]
	s_waitcnt lgkmcnt(0)
	v_lshlrev_b32_e32 v132, 16, v178
	v_and_b32_e32 v176, 0xffff0000, v178
	v_mul_f32_e32 v132, 0x42800000, v132
	v_mul_f32_e32 v177, 0x42800000, v176
	v_mov_b32_e32 v176, v133
	v_cvt_pk_fp8_f32 v176, v132, v177
	v_lshlrev_b32_e32 v178, 16, v179
	v_and_b32_e32 v177, 0xffff0000, v179
	v_mul_f32_e32 v132, 0x42800000, v178
	v_mul_f32_e32 v177, 0x42800000, v177
	v_cvt_pk_fp8_f32 v176, v132, v177 op_sel:[0,0,1]
	v_lshlrev_b32_e32 v132, 16, v180
	v_and_b32_e32 v177, 0xffff0000, v180
	v_mul_f32_e32 v132, 0x42800000, v132
	v_mul_f32_e32 v178, 0x42800000, v177
	v_mov_b32_e32 v177, v133
	v_cvt_pk_fp8_f32 v177, v132, v178
	v_lshlrev_b32_e32 v179, 16, v181
	v_and_b32_e32 v178, 0xffff0000, v181
	v_mul_f32_e32 v132, 0x42800000, v179
	v_mul_f32_e32 v178, 0x42800000, v178
	v_cvt_pk_fp8_f32 v177, v132, v178 op_sel:[0,0,1]
	v_mad_u64_u32 v[142:143], s[12:13], s17, v140, v[142:143]
	v_mov_b32_e32 v132, v143
	v_mad_u64_u32 v[178:179], s[12:13], s17, v139, v[132:133]
	v_mov_b32_e32 v143, v178
	global_store_dwordx4 v[142:143], v[174:177], off
	s_waitcnt lgkmcnt(0)
	s_cbranch_vccnz .LBB0_769
	s_add_i32 s15, s20, 0x8001
	s_cmp_ge_i32 s15, s16
	s_cbranch_scc1 .LcvwP5_b
	s_cmpk_gt_i32 s21, 0x7ffd
	s_mov_b64 s[12:13], -1
	s_cbranch_scc0 .LBB0_781
	s_add_i32 s4, s20, 1
	s_lshr_b32 s4, s4, 9
	s_lshl_b64 s[6:7], s[4:5], 23
	s_add_u32 s6, s58, s6
	s_addc_u32 s7, s59, s7
	s_and_b32 s12, s18, 0x380
	s_lshl_b32 s10, s12, 13
	s_add_u32 s6, s6, s10
	s_addc_u32 s7, s7, 0
	s_and_b32 s13, s19, 0x7e0
	s_lshl_b32 s10, s13, 2
	s_add_u32 s10, s6, s10
	s_addc_u32 s11, s7, 0
	s_lshl_b64 s[6:7], s[4:5], 21
	s_lshl_b32 s4, s13, 10
	s_add_u32 s6, s70, s6
	s_addc_u32 s7, s71, s7
	s_add_u32 s4, s6, s4
	s_addc_u32 s7, s7, 0
	s_add_u32 s6, s4, s12
	s_addc_u32 s7, s7, 0
	s_mov_b64 s[12:13], 0
